# v66 + GEMM K-loops: LDS-DMA loads addressed as SGPR base + 32-bit lane VGPR (M0 compensates the immediate offset), ~100 64-bit VALU address adds removed
# baseline (speedup 1.0000x reference)
.LBB0_98:
	s_add_u32 s54, s50, s52
	s_addc_u32 s55, s51, s53
	v_or_b32_e32 v146, 0x10000, v145
	v_add_u32_e32 v150, 0x10400, v145
	v_add_u32_e32 v154, 0x10800, v145
	v_add_u32_e32 v158, 0x10c00, v145
	v_or_b32_e32 v162, 0x14000, v145
	v_add_u32_e32 v166, 0x14400, v145
	v_add_u32_e32 v170, 0x14800, v145
	v_add_u32_e32 v174, 0x14c00, v145
	s_add_u32 s54, s54, 0x100
	ds_read_b128 v[146:149], v146
	ds_read_b128 v[150:153], v150
	ds_read_b128 v[154:157], v154
	ds_read_b128 v[158:161], v158
	ds_read_b128 v[162:165], v162
	ds_read_b128 v[166:169], v166
	ds_read_b128 v[170:173], v170
	ds_read_b128 v[174:177], v174
	s_addc_u32 s55, s55, 0
	s_add_u32 vcc_lo, s95, s52
	s_addc_u32 vcc_hi, s46, s53
	s_cmpk_eq_i32 s52, 0x1500
	s_cselect_b32 s57, s43, s55
	s_cselect_b32 s56, s42, s54
	s_cselect_b32 s55, s49, vcc_hi
	s_cselect_b32 s54, s48, vcc_lo
	s_mov_b32 m0, s89
	v_lshl_add_u64 v[194:195], v[140:141], 0, s[52:53]
	ds_read_b128 v[178:181], v144
	ds_read_b128 v[182:185], v144 offset:1024
	ds_read_b128 v[186:189], v144 offset:2048
	ds_read_b128 v[190:193], v144 offset:3072
	ds_read_b128 v[200:203], v144 offset:4096
	ds_read_b128 v[204:207], v144 offset:5120
	ds_read_b128 v[208:211], v144 offset:6144
	ds_read_b128 v[212:215], v144 offset:7168
	global_load_lds_dwordx4 v[194:195], off
	v_lshl_add_u64 v[194:195], v[142:143], 0, s[52:53]
	s_mov_b32 m0, s90
	s_nop 0
	global_load_lds_dwordx4 v[194:195], off
	s_waitcnt vmcnt(8)
	s_waitcnt lgkmcnt(0)
	s_barrier
	s_setprio 1
	s_waitcnt lgkmcnt(0)
	v_mfma_f32_16x16x32_bf16 v[126:129], v[146:149], v[178:181], v[126:129]
	v_mfma_f32_16x16x32_bf16 v[122:125], v[154:157], v[178:181], v[122:125]
	v_mfma_f32_16x16x32_bf16 v[110:113], v[146:149], v[186:189], v[110:113]
	v_mfma_f32_16x16x32_bf16 v[106:109], v[154:157], v[186:189], v[106:109]
	v_mfma_f32_16x16x32_bf16 v[94:97], v[146:149], v[200:203], v[94:97]
	v_mfma_f32_16x16x32_bf16 v[90:93], v[154:157], v[200:203], v[90:93]
	v_mfma_f32_16x16x32_bf16 v[78:81], v[146:149], v[208:211], v[78:81]
	v_mfma_f32_16x16x32_bf16 v[74:77], v[154:157], v[208:211], v[74:77]
	v_mfma_f32_16x16x32_bf16 v[126:129], v[150:153], v[182:185], v[126:129]
	v_mfma_f32_16x16x32_bf16 v[122:125], v[158:161], v[182:185], v[122:125]
	v_mfma_f32_16x16x32_bf16 v[110:113], v[150:153], v[190:193], v[110:113]
	v_mfma_f32_16x16x32_bf16 v[106:109], v[158:161], v[190:193], v[106:109]
	v_mfma_f32_16x16x32_bf16 v[94:97], v[150:153], v[204:207], v[94:97]
	v_mfma_f32_16x16x32_bf16 v[90:93], v[158:161], v[204:207], v[90:93]
	v_mfma_f32_16x16x32_bf16 v[78:81], v[150:153], v[212:215], v[78:81]
	v_mfma_f32_16x16x32_bf16 v[74:77], v[158:161], v[212:215], v[74:77]
	s_setprio 0
	s_setprio 1
	v_mfma_f32_16x16x32_bf16 v[118:121], v[162:165], v[178:181], v[118:121]
	v_mfma_f32_16x16x32_bf16 v[114:117], v[170:173], v[178:181], v[114:117]
	v_mfma_f32_16x16x32_bf16 v[102:105], v[162:165], v[186:189], v[102:105]
	v_mfma_f32_16x16x32_bf16 v[98:101], v[170:173], v[186:189], v[98:101]
	v_mfma_f32_16x16x32_bf16 v[86:89], v[162:165], v[200:203], v[86:89]
	v_mfma_f32_16x16x32_bf16 v[82:85], v[170:173], v[200:203], v[82:85]
	v_mfma_f32_16x16x32_bf16 v[70:73], v[162:165], v[208:211], v[70:73]
	v_mfma_f32_16x16x32_bf16 v[66:69], v[170:173], v[208:211], v[66:69]
	v_mfma_f32_16x16x32_bf16 v[118:121], v[166:169], v[182:185], v[118:121]
	v_mfma_f32_16x16x32_bf16 v[114:117], v[174:177], v[182:185], v[114:117]
	v_mfma_f32_16x16x32_bf16 v[102:105], v[166:169], v[190:193], v[102:105]
	v_mfma_f32_16x16x32_bf16 v[98:101], v[174:177], v[190:193], v[98:101]
	v_mfma_f32_16x16x32_bf16 v[86:89], v[166:169], v[204:207], v[86:89]
	v_mfma_f32_16x16x32_bf16 v[82:85], v[174:177], v[204:207], v[82:85]
	v_mfma_f32_16x16x32_bf16 v[70:73], v[166:169], v[212:215], v[70:73]
	v_mfma_f32_16x16x32_bf16 v[66:69], v[174:177], v[212:215], v[66:69]
	s_setprio 0
	s_barrier
	s_mov_b32 m0, s58
	v_lshl_add_u64 v[194:195], s[54:55], 0, v[0:1]
	s_add_u32 vcc_lo, s54, 0xb0000
	ds_read_b128 v[178:181], v144 offset:16384
	ds_read_b128 v[182:185], v144 offset:17408
	ds_read_b128 v[186:189], v144 offset:18432
	ds_read_b128 v[190:193], v144 offset:19456
	ds_read_b128 v[200:203], v144 offset:20480
	ds_read_b128 v[204:207], v144 offset:21504
	ds_read_b128 v[208:211], v144 offset:22528
	ds_read_b128 v[212:215], v144 offset:23552
	global_load_lds_dwordx4 v0, s[54:55]
	v_lshl_add_u64 v[216:217], s[54:55], 0, v[130:131]
	s_mov_b32 m0, s59
	s_addc_u32 vcc_hi, s55, 0
	global_load_lds_dwordx4 v130, s[54:55]
	s_mov_b32 m0, s60
	v_lshl_add_u64 v[220:221], s[56:57], 0, v[132:133]
	global_load_lds_dwordx4 v0, vcc
	s_mov_b32 m0, s61
	s_nop 0
	global_load_lds_dwordx4 v130, vcc
	v_lshl_add_u64 v[218:219], s[56:57], 0, v[134:135]
	s_mov_b32 m0, s39
	s_nop 0
	global_load_lds_dwordx4 v134, s[56:57]
	s_mov_b32 m0, s64
	s_nop 0
	global_load_lds_dwordx4 v132, s[56:57]
	s_waitcnt vmcnt(8)
	s_waitcnt lgkmcnt(0)
	s_barrier
	s_setprio 1
	s_waitcnt lgkmcnt(0)
	v_mfma_f32_16x16x32_bf16 v[62:65], v[146:149], v[178:181], v[62:65]
	v_mfma_f32_16x16x32_bf16 v[58:61], v[154:157], v[178:181], v[58:61]
	v_mfma_f32_16x16x32_bf16 v[46:49], v[146:149], v[186:189], v[46:49]
	v_mfma_f32_16x16x32_bf16 v[42:45], v[154:157], v[186:189], v[42:45]
	v_mfma_f32_16x16x32_bf16 v[30:33], v[146:149], v[200:203], v[30:33]
	v_mfma_f32_16x16x32_bf16 v[26:29], v[154:157], v[200:203], v[26:29]
	v_mfma_f32_16x16x32_bf16 v[14:17], v[146:149], v[208:211], v[14:17]
	v_mfma_f32_16x16x32_bf16 v[10:13], v[154:157], v[208:211], v[10:13]
	v_mfma_f32_16x16x32_bf16 v[62:65], v[150:153], v[182:185], v[62:65]
	v_mfma_f32_16x16x32_bf16 v[58:61], v[158:161], v[182:185], v[58:61]
	v_mfma_f32_16x16x32_bf16 v[46:49], v[150:153], v[190:193], v[46:49]
	v_mfma_f32_16x16x32_bf16 v[42:45], v[158:161], v[190:193], v[42:45]
	v_mfma_f32_16x16x32_bf16 v[30:33], v[150:153], v[204:207], v[30:33]
	v_mfma_f32_16x16x32_bf16 v[26:29], v[158:161], v[204:207], v[26:29]
	v_mfma_f32_16x16x32_bf16 v[14:17], v[150:153], v[212:215], v[14:17]
	v_mfma_f32_16x16x32_bf16 v[10:13], v[158:161], v[212:215], v[10:13]
	s_setprio 0
	s_setprio 1
	v_mfma_f32_16x16x32_bf16 v[54:57], v[162:165], v[178:181], v[54:57]
	v_mfma_f32_16x16x32_bf16 v[50:53], v[170:173], v[178:181], v[50:53]
	v_mfma_f32_16x16x32_bf16 v[38:41], v[162:165], v[186:189], v[38:41]
	v_mfma_f32_16x16x32_bf16 v[34:37], v[170:173], v[186:189], v[34:37]
	v_mfma_f32_16x16x32_bf16 v[22:25], v[162:165], v[200:203], v[22:25]
	v_mfma_f32_16x16x32_bf16 v[18:21], v[170:173], v[200:203], v[18:21]
	v_mfma_f32_16x16x32_bf16 v[6:9], v[162:165], v[208:211], v[6:9]
	v_mfma_f32_16x16x32_bf16 v[2:5], v[170:173], v[208:211], v[2:5]
	v_mfma_f32_16x16x32_bf16 v[54:57], v[166:169], v[182:185], v[54:57]
	v_mfma_f32_16x16x32_bf16 v[50:53], v[174:177], v[182:185], v[50:53]
	v_mfma_f32_16x16x32_bf16 v[38:41], v[166:169], v[190:193], v[38:41]
	v_mfma_f32_16x16x32_bf16 v[34:37], v[174:177], v[190:193], v[34:37]
	v_mfma_f32_16x16x32_bf16 v[22:25], v[166:169], v[204:207], v[22:25]
	v_mfma_f32_16x16x32_bf16 v[18:21], v[174:177], v[204:207], v[18:21]
	v_mfma_f32_16x16x32_bf16 v[6:9], v[166:169], v[212:215], v[6:9]
	v_mfma_f32_16x16x32_bf16 v[2:5], v[174:177], v[212:215], v[2:5]
	s_setprio 0
	s_barrier
	v_or_b32_e32 v146, 0x18000, v145
	v_add_u32_e32 v150, 0x18400, v145
	v_add_u32_e32 v154, 0x18800, v145
	v_add_u32_e32 v158, 0x18c00, v145
	v_or_b32_e32 v162, 0x1c000, v145
	v_add_u32_e32 v166, 0x1c400, v145
	v_add_u32_e32 v170, 0x1c800, v145
	v_add_u32_e32 v174, 0x1cc00, v145
	ds_read_b128 v[146:149], v146
	ds_read_b128 v[150:153], v150
	ds_read_b128 v[154:157], v154
	ds_read_b128 v[158:161], v158
	ds_read_b128 v[162:165], v162
	ds_read_b128 v[166:169], v166
	ds_read_b128 v[170:173], v170
	ds_read_b128 v[174:177], v174
	s_add_u32 s56, s56, 0xb0000
	s_addc_u32 s57, s57, 0
	s_mov_b32 m0, s65
	ds_read_b128 v[178:181], v144 offset:32768
	ds_read_b128 v[182:185], v144 offset:33792
	ds_read_b128 v[186:189], v144 offset:34816
	ds_read_b128 v[190:193], v144 offset:35840
	ds_read_b128 v[200:203], v144 offset:36864
	ds_read_b128 v[204:207], v144 offset:37888
	ds_read_b128 v[208:211], v144 offset:38912
	ds_read_b128 v[212:215], v144 offset:39936
	global_load_lds_dwordx4 v134, s[56:57]
	s_mov_b32 m0, s66
	s_nop 0
	global_load_lds_dwordx4 v132, s[56:57]
	s_waitcnt vmcnt(8)
	s_waitcnt lgkmcnt(0)
	s_barrier
	s_setprio 1
	s_waitcnt lgkmcnt(0)
	v_mfma_f32_16x16x32_bf16 v[126:129], v[146:149], v[178:181], v[126:129]
	v_mfma_f32_16x16x32_bf16 v[122:125], v[154:157], v[178:181], v[122:125]
	v_mfma_f32_16x16x32_bf16 v[110:113], v[146:149], v[186:189], v[110:113]
	v_mfma_f32_16x16x32_bf16 v[106:109], v[154:157], v[186:189], v[106:109]
	v_mfma_f32_16x16x32_bf16 v[94:97], v[146:149], v[200:203], v[94:97]
	v_mfma_f32_16x16x32_bf16 v[90:93], v[154:157], v[200:203], v[90:93]
	v_mfma_f32_16x16x32_bf16 v[78:81], v[146:149], v[208:211], v[78:81]
	v_mfma_f32_16x16x32_bf16 v[74:77], v[154:157], v[208:211], v[74:77]
	v_mfma_f32_16x16x32_bf16 v[126:129], v[150:153], v[182:185], v[126:129]
	v_mfma_f32_16x16x32_bf16 v[122:125], v[158:161], v[182:185], v[122:125]
	v_mfma_f32_16x16x32_bf16 v[110:113], v[150:153], v[190:193], v[110:113]
	v_mfma_f32_16x16x32_bf16 v[106:109], v[158:161], v[190:193], v[106:109]
	v_mfma_f32_16x16x32_bf16 v[94:97], v[150:153], v[204:207], v[94:97]
	v_mfma_f32_16x16x32_bf16 v[90:93], v[158:161], v[204:207], v[90:93]
	v_mfma_f32_16x16x32_bf16 v[78:81], v[150:153], v[212:215], v[78:81]
	v_mfma_f32_16x16x32_bf16 v[74:77], v[158:161], v[212:215], v[74:77]
	s_setprio 0
	s_setprio 1
	v_mfma_f32_16x16x32_bf16 v[118:121], v[162:165], v[178:181], v[118:121]
	v_mfma_f32_16x16x32_bf16 v[114:117], v[170:173], v[178:181], v[114:117]
	v_mfma_f32_16x16x32_bf16 v[102:105], v[162:165], v[186:189], v[102:105]
	v_mfma_f32_16x16x32_bf16 v[98:101], v[170:173], v[186:189], v[98:101]
	v_mfma_f32_16x16x32_bf16 v[86:89], v[162:165], v[200:203], v[86:89]
	v_mfma_f32_16x16x32_bf16 v[82:85], v[170:173], v[200:203], v[82:85]
	v_mfma_f32_16x16x32_bf16 v[70:73], v[162:165], v[208:211], v[70:73]
	v_mfma_f32_16x16x32_bf16 v[66:69], v[170:173], v[208:211], v[66:69]
	v_mfma_f32_16x16x32_bf16 v[118:121], v[166:169], v[182:185], v[118:121]
	v_mfma_f32_16x16x32_bf16 v[114:117], v[174:177], v[182:185], v[114:117]
	v_mfma_f32_16x16x32_bf16 v[102:105], v[166:169], v[190:193], v[102:105]
	v_mfma_f32_16x16x32_bf16 v[98:101], v[174:177], v[190:193], v[98:101]
	v_mfma_f32_16x16x32_bf16 v[86:89], v[166:169], v[204:207], v[86:89]
	v_mfma_f32_16x16x32_bf16 v[82:85], v[174:177], v[204:207], v[82:85]
	v_mfma_f32_16x16x32_bf16 v[70:73], v[166:169], v[212:215], v[70:73]
	v_mfma_f32_16x16x32_bf16 v[66:69], v[174:177], v[212:215], v[66:69]
	s_setprio 0
	s_barrier
	s_mov_b32 m0, s67
	v_lshl_add_u64 v[194:195], v[194:195], 0, s[18:19]
	s_add_u32 s54, s54, 0xb0080
	ds_read_b128 v[178:181], v144 offset:49152
	ds_read_b128 v[182:185], v144 offset:50176
	ds_read_b128 v[186:189], v144 offset:51200
	ds_read_b128 v[190:193], v144 offset:52224
	ds_read_b128 v[200:203], v144 offset:53248
	ds_read_b128 v[204:207], v144 offset:54272
	ds_read_b128 v[208:211], v144 offset:55296
	ds_read_b128 v[212:215], v144 offset:56320
	global_load_lds_dwordx4 v[194:195], off
	v_lshl_add_u64 v[194:195], v[216:217], 0, s[18:19]
	s_mov_b32 m0, s80
	s_addc_u32 s55, s55, 0
	global_load_lds_dwordx4 v[194:195], off
	s_mov_b32 m0, s84
	s_nop 0
	global_load_lds_dwordx4 v0, s[54:55]
	s_mov_b32 m0, s85
	s_nop 0
	global_load_lds_dwordx4 v130, s[54:55]
	v_lshl_add_u64 v[194:195], v[218:219], 0, s[18:19]
	s_mov_b32 m0, s82
	s_nop 0
	global_load_lds_dwordx4 v[194:195], off
	v_lshl_add_u64 v[194:195], v[220:221], 0, s[18:19]
	s_mov_b32 m0, s83
	s_nop 0
	global_load_lds_dwordx4 v[194:195], off
	s_waitcnt vmcnt(8)
	s_waitcnt lgkmcnt(0)
	s_barrier
	s_setprio 1
	s_waitcnt lgkmcnt(0)
	v_mfma_f32_16x16x32_bf16 v[62:65], v[146:149], v[178:181], v[62:65]
	v_mfma_f32_16x16x32_bf16 v[58:61], v[154:157], v[178:181], v[58:61]
	v_mfma_f32_16x16x32_bf16 v[46:49], v[146:149], v[186:189], v[46:49]
	v_mfma_f32_16x16x32_bf16 v[42:45], v[154:157], v[186:189], v[42:45]
	v_mfma_f32_16x16x32_bf16 v[30:33], v[146:149], v[200:203], v[30:33]
	v_mfma_f32_16x16x32_bf16 v[26:29], v[154:157], v[200:203], v[26:29]
	v_mfma_f32_16x16x32_bf16 v[14:17], v[146:149], v[208:211], v[14:17]
	v_mfma_f32_16x16x32_bf16 v[10:13], v[154:157], v[208:211], v[10:13]
	v_mfma_f32_16x16x32_bf16 v[62:65], v[150:153], v[182:185], v[62:65]
	v_mfma_f32_16x16x32_bf16 v[58:61], v[158:161], v[182:185], v[58:61]
	v_mfma_f32_16x16x32_bf16 v[46:49], v[150:153], v[190:193], v[46:49]
	v_mfma_f32_16x16x32_bf16 v[42:45], v[158:161], v[190:193], v[42:45]
	v_mfma_f32_16x16x32_bf16 v[30:33], v[150:153], v[204:207], v[30:33]
	v_mfma_f32_16x16x32_bf16 v[26:29], v[158:161], v[204:207], v[26:29]
	v_mfma_f32_16x16x32_bf16 v[14:17], v[150:153], v[212:215], v[14:17]
	v_mfma_f32_16x16x32_bf16 v[10:13], v[158:161], v[212:215], v[10:13]
	s_setprio 0
	s_setprio 1
	v_mfma_f32_16x16x32_bf16 v[54:57], v[162:165], v[178:181], v[54:57]
	v_mfma_f32_16x16x32_bf16 v[50:53], v[170:173], v[178:181], v[50:53]
	v_mfma_f32_16x16x32_bf16 v[38:41], v[162:165], v[186:189], v[38:41]
	v_mfma_f32_16x16x32_bf16 v[34:37], v[170:173], v[186:189], v[34:37]
	v_mfma_f32_16x16x32_bf16 v[22:25], v[162:165], v[200:203], v[22:25]
	v_mfma_f32_16x16x32_bf16 v[18:21], v[170:173], v[200:203], v[18:21]
	v_mfma_f32_16x16x32_bf16 v[6:9], v[162:165], v[208:211], v[6:9]
	v_mfma_f32_16x16x32_bf16 v[2:5], v[170:173], v[208:211], v[2:5]
	v_mfma_f32_16x16x32_bf16 v[54:57], v[166:169], v[182:185], v[54:57]
	v_mfma_f32_16x16x32_bf16 v[50:53], v[174:177], v[182:185], v[50:53]
	v_mfma_f32_16x16x32_bf16 v[38:41], v[166:169], v[190:193], v[38:41]
	v_mfma_f32_16x16x32_bf16 v[34:37], v[174:177], v[190:193], v[34:37]
	v_mfma_f32_16x16x32_bf16 v[22:25], v[166:169], v[204:207], v[22:25]
	v_mfma_f32_16x16x32_bf16 v[18:21], v[174:177], v[204:207], v[18:21]
	v_mfma_f32_16x16x32_bf16 v[6:9], v[166:169], v[212:215], v[6:9]
	v_mfma_f32_16x16x32_bf16 v[2:5], v[174:177], v[212:215], v[2:5]
	s_setprio 0
	s_barrier
	s_add_i32 s47, s47, 2
	s_add_u32 s52, s52, 0x100
	s_addc_u32 s53, s53, 0
	s_cmp_gt_u32 s47, 41
	s_cbranch_scc0 .LBB0_98
	s_and_b64 vcc, exec, s[16:17]
	s_cbranch_vccz .LBB0_101
	s_barrier

.LBB0_357:
	v_or_b32_e32 v0, 0x10000, v220
	v_add_u32_e32 v50, 0x10400, v220
	ds_read_b128 v[46:49], v0
	ds_read_b128 v[50:53], v50
	v_add_u32_e32 v0, 0x10800, v220
	v_add_u32_e32 v62, 0x10c00, v220
	ds_read_b128 v[58:61], v0
	ds_read_b128 v[62:65], v62
	v_or_b32_e32 v0, 0x14000, v220
	v_add_u32_e32 v78, 0x14400, v220
	ds_read_b128 v[74:77], v0
	ds_read_b128 v[78:81], v78
	v_add_u32_e32 v0, 0x14800, v220
	v_add_u32_e32 v86, 0x14c00, v220
	ds_read_b128 v[82:85], v0
	ds_read_b128 v[86:89], v86
	s_add_u32 s50, s40, 0xfffc0080
	s_addc_u32 s51, s41, -1
	s_cmp_eq_u32 vcc_hi, 12
	s_cselect_b32 s83, s29, s51
	s_cselect_b32 s82, s37, s50
	s_cselect_b32 s67, s39, vcc_lo
	s_cselect_b32 s66, s57, s59
	s_add_i32 m0, s88, 0xc000
	ds_read_b128 v[192:195], v219
	ds_read_b128 v[200:203], v219 offset:1024
	ds_read_b128 v[204:207], v219 offset:2048
	ds_read_b128 v[208:211], v219 offset:3072
	ds_read_b128 v[212:215], v219 offset:4096
	ds_read_b128 v[236:239], v219 offset:5120
	ds_read_b128 v[240:243], v219 offset:6144
	ds_read_b128 v[244:247], v219 offset:7168
	global_load_lds_dwordx4 v170, s[40:41]
	s_add_i32 m0, s88, 0xe000
	s_nop 0
	global_load_lds_dwordx4 v172, s[40:41]
	s_waitcnt vmcnt(8)
	s_waitcnt lgkmcnt(0)
	s_barrier
	s_setprio 1
	s_waitcnt lgkmcnt(0)
	v_mfma_f32_16x16x32_bf16 v[158:161], v[46:49], v[192:195], v[158:161]
	v_mfma_f32_16x16x32_bf16 v[154:157], v[58:61], v[192:195], v[154:157]
	v_mfma_f32_16x16x32_bf16 v[142:145], v[46:49], v[204:207], v[142:145]
	v_mfma_f32_16x16x32_bf16 v[138:141], v[58:61], v[204:207], v[138:141]
	v_mfma_f32_16x16x32_bf16 v[126:129], v[46:49], v[212:215], v[126:129]
	v_mfma_f32_16x16x32_bf16 v[122:125], v[58:61], v[212:215], v[122:125]
	v_mfma_f32_16x16x32_bf16 v[110:113], v[46:49], v[240:243], v[110:113]
	v_mfma_f32_16x16x32_bf16 v[106:109], v[58:61], v[240:243], v[106:109]
	v_mfma_f32_16x16x32_bf16 v[158:161], v[50:53], v[200:203], v[158:161]
	v_mfma_f32_16x16x32_bf16 v[154:157], v[62:65], v[200:203], v[154:157]
	v_mfma_f32_16x16x32_bf16 v[142:145], v[50:53], v[208:211], v[142:145]
	v_mfma_f32_16x16x32_bf16 v[138:141], v[62:65], v[208:211], v[138:141]
	v_mfma_f32_16x16x32_bf16 v[126:129], v[50:53], v[236:239], v[126:129]
	v_mfma_f32_16x16x32_bf16 v[122:125], v[62:65], v[236:239], v[122:125]
	v_mfma_f32_16x16x32_bf16 v[110:113], v[50:53], v[244:247], v[110:113]
	v_mfma_f32_16x16x32_bf16 v[106:109], v[62:65], v[244:247], v[106:109]
	s_setprio 0
	s_setprio 1
	v_mfma_f32_16x16x32_bf16 v[150:153], v[74:77], v[192:195], v[150:153]
	v_mfma_f32_16x16x32_bf16 v[146:149], v[82:85], v[192:195], v[146:149]
	v_mfma_f32_16x16x32_bf16 v[134:137], v[74:77], v[204:207], v[134:137]
	v_mfma_f32_16x16x32_bf16 v[130:133], v[82:85], v[204:207], v[130:133]
	v_mfma_f32_16x16x32_bf16 v[118:121], v[74:77], v[212:215], v[118:121]
	v_mfma_f32_16x16x32_bf16 v[114:117], v[82:85], v[212:215], v[114:117]
	v_mfma_f32_16x16x32_bf16 v[102:105], v[74:77], v[240:243], v[102:105]
	v_mfma_f32_16x16x32_bf16 v[98:101], v[82:85], v[240:243], v[98:101]
	v_mfma_f32_16x16x32_bf16 v[150:153], v[78:81], v[200:203], v[150:153]
	v_mfma_f32_16x16x32_bf16 v[146:149], v[86:89], v[200:203], v[146:149]
	v_mfma_f32_16x16x32_bf16 v[134:137], v[78:81], v[208:211], v[134:137]
	v_mfma_f32_16x16x32_bf16 v[130:133], v[86:89], v[208:211], v[130:133]
	v_mfma_f32_16x16x32_bf16 v[118:121], v[78:81], v[236:239], v[118:121]
	v_mfma_f32_16x16x32_bf16 v[114:117], v[86:89], v[236:239], v[114:117]
	v_mfma_f32_16x16x32_bf16 v[102:105], v[78:81], v[244:247], v[102:105]
	v_mfma_f32_16x16x32_bf16 v[98:101], v[86:89], v[244:247], v[98:101]
	s_setprio 0
	s_barrier
	s_mov_b32 m0, s90
	s_add_u32 s50, s66, 0x40000
	ds_read_b128 v[192:195], v219 offset:16384
	ds_read_b128 v[200:203], v219 offset:17408
	ds_read_b128 v[204:207], v219 offset:18432
	ds_read_b128 v[208:211], v219 offset:19456
	ds_read_b128 v[212:215], v219 offset:20480
	ds_read_b128 v[236:239], v219 offset:21504
	ds_read_b128 v[240:243], v219 offset:22528
	ds_read_b128 v[244:247], v219 offset:23552
	global_load_lds_dwordx4 v166, s[66:67]
	v_lshl_add_u64 v[216:217], s[66:67], 0, v[162:163]
	s_mov_b32 m0, s91
	s_addc_u32 s51, s67, 0
	global_load_lds_dwordx4 v162, s[66:67]
	s_mov_b32 m0, s92
	s_nop 0
	global_load_lds_dwordx4 v166, s[50:51]
	s_mov_b32 m0, s93
	s_nop 0
	global_load_lds_dwordx4 v162, s[50:51]
	s_mov_b32 m0, s88
	s_nop 0
	global_load_lds_dwordx4 v168, s[82:83]
	s_mov_b32 m0, s94
	s_nop 0
	global_load_lds_dwordx4 v164, s[82:83]
	s_waitcnt vmcnt(8)
	s_waitcnt lgkmcnt(0)
	s_barrier
	s_setprio 1
	s_waitcnt lgkmcnt(0)
	v_mfma_f32_16x16x32_bf16 v[94:97], v[46:49], v[192:195], v[94:97]
	v_mfma_f32_16x16x32_bf16 v[90:93], v[58:61], v[192:195], v[90:93]
	v_mfma_f32_16x16x32_bf16 v[54:57], v[46:49], v[204:207], v[54:57]
	v_mfma_f32_16x16x32_bf16 v[42:45], v[58:61], v[204:207], v[42:45]
	v_mfma_f32_16x16x32_bf16 v[30:33], v[46:49], v[212:215], v[30:33]
	v_mfma_f32_16x16x32_bf16 v[26:29], v[58:61], v[212:215], v[26:29]
	v_mfma_f32_16x16x32_bf16 v[14:17], v[46:49], v[240:243], v[14:17]
	v_mfma_f32_16x16x32_bf16 v[10:13], v[58:61], v[240:243], v[10:13]
	v_mfma_f32_16x16x32_bf16 v[94:97], v[50:53], v[200:203], v[94:97]
	v_mfma_f32_16x16x32_bf16 v[90:93], v[62:65], v[200:203], v[90:93]
	v_mfma_f32_16x16x32_bf16 v[54:57], v[50:53], v[208:211], v[54:57]
	v_mfma_f32_16x16x32_bf16 v[42:45], v[62:65], v[208:211], v[42:45]
	v_mfma_f32_16x16x32_bf16 v[30:33], v[50:53], v[236:239], v[30:33]
	v_mfma_f32_16x16x32_bf16 v[26:29], v[62:65], v[236:239], v[26:29]
	v_mfma_f32_16x16x32_bf16 v[14:17], v[50:53], v[244:247], v[14:17]
	v_mfma_f32_16x16x32_bf16 v[10:13], v[62:65], v[244:247], v[10:13]
	s_setprio 0
	s_setprio 1
	v_mfma_f32_16x16x32_bf16 v[38:41], v[74:77], v[204:207], v[38:41]
	v_mfma_f32_16x16x32_bf16 v[34:37], v[82:85], v[204:207], v[34:37]
	v_mfma_f32_16x16x32_bf16 v[22:25], v[74:77], v[212:215], v[22:25]
	v_mfma_f32_16x16x32_bf16 v[18:21], v[82:85], v[212:215], v[18:21]
	v_mfma_f32_16x16x32_bf16 v[6:9], v[74:77], v[240:243], v[6:9]
	v_mfma_f32_16x16x32_bf16 v[2:5], v[82:85], v[240:243], v[2:5]
	v_mfma_f32_16x16x32_bf16 v[46:49], v[74:77], v[192:195], v[70:73]
	v_mfma_f32_16x16x32_bf16 v[50:53], v[82:85], v[192:195], v[66:69]
	v_mfma_f32_16x16x32_bf16 v[38:41], v[78:81], v[208:211], v[38:41]
	v_mfma_f32_16x16x32_bf16 v[34:37], v[86:89], v[208:211], v[34:37]
	v_mfma_f32_16x16x32_bf16 v[22:25], v[78:81], v[236:239], v[22:25]
	v_mfma_f32_16x16x32_bf16 v[18:21], v[86:89], v[236:239], v[18:21]
	v_mfma_f32_16x16x32_bf16 v[6:9], v[78:81], v[244:247], v[6:9]
	v_mfma_f32_16x16x32_bf16 v[2:5], v[86:89], v[244:247], v[2:5]
	v_mfma_f32_16x16x32_bf16 v[46:49], v[78:81], v[200:203], v[46:49]
	v_mfma_f32_16x16x32_bf16 v[50:53], v[86:89], v[200:203], v[50:53]
	s_setprio 0
	s_barrier
	v_or_b32_e32 v0, 0x18000, v220
	v_add_u32_e32 v62, 0x18400, v220
	ds_read_b128 v[58:61], v0
	ds_read_b128 v[62:65], v62
	v_add_u32_e32 v0, 0x18800, v220
	v_add_u32_e32 v70, 0x18c00, v220
	ds_read_b128 v[66:69], v0
	ds_read_b128 v[70:73], v70
	v_or_b32_e32 v0, 0x1c000, v220
	v_add_u32_e32 v78, 0x1c400, v220
	ds_read_b128 v[74:77], v0
	ds_read_b128 v[78:81], v78
	v_add_u32_e32 v0, 0x1c800, v220
	v_add_u32_e32 v86, 0x1cc00, v220
	ds_read_b128 v[82:85], v0
	ds_read_b128 v[86:89], v86
	s_add_u32 s50, s82, 0x40000
	s_addc_u32 s51, s83, 0
	s_mov_b32 m0, s95
	ds_read_b128 v[192:195], v219 offset:32768
	ds_read_b128 v[200:203], v219 offset:33792
	ds_read_b128 v[204:207], v219 offset:34816
	ds_read_b128 v[208:211], v219 offset:35840
	ds_read_b128 v[212:215], v219 offset:36864
	ds_read_b128 v[236:239], v219 offset:37888
	ds_read_b128 v[240:243], v219 offset:38912
	ds_read_b128 v[244:247], v219 offset:39936
	global_load_lds_dwordx4 v168, s[50:51]
	s_mov_b32 m0, s0
	s_nop 0
	global_load_lds_dwordx4 v164, s[50:51]
	s_waitcnt vmcnt(8)
	s_waitcnt lgkmcnt(0)
	s_barrier
	s_setprio 1
	s_waitcnt lgkmcnt(0)
	v_mfma_f32_16x16x32_bf16 v[158:161], v[58:61], v[192:195], v[158:161]
	v_mfma_f32_16x16x32_bf16 v[154:157], v[66:69], v[192:195], v[154:157]
	v_mfma_f32_16x16x32_bf16 v[142:145], v[58:61], v[204:207], v[142:145]
	v_mfma_f32_16x16x32_bf16 v[138:141], v[66:69], v[204:207], v[138:141]
	v_mfma_f32_16x16x32_bf16 v[126:129], v[58:61], v[212:215], v[126:129]
	v_mfma_f32_16x16x32_bf16 v[122:125], v[66:69], v[212:215], v[122:125]
	v_mfma_f32_16x16x32_bf16 v[110:113], v[58:61], v[240:243], v[110:113]
	v_mfma_f32_16x16x32_bf16 v[106:109], v[66:69], v[240:243], v[106:109]
	v_mfma_f32_16x16x32_bf16 v[158:161], v[62:65], v[200:203], v[158:161]
	v_mfma_f32_16x16x32_bf16 v[154:157], v[70:73], v[200:203], v[154:157]
	v_mfma_f32_16x16x32_bf16 v[142:145], v[62:65], v[208:211], v[142:145]
	v_mfma_f32_16x16x32_bf16 v[138:141], v[70:73], v[208:211], v[138:141]
	v_mfma_f32_16x16x32_bf16 v[126:129], v[62:65], v[236:239], v[126:129]
	v_mfma_f32_16x16x32_bf16 v[122:125], v[70:73], v[236:239], v[122:125]
	v_mfma_f32_16x16x32_bf16 v[110:113], v[62:65], v[244:247], v[110:113]
	v_mfma_f32_16x16x32_bf16 v[106:109], v[70:73], v[244:247], v[106:109]
	s_setprio 0
	s_setprio 1
	v_mfma_f32_16x16x32_bf16 v[150:153], v[74:77], v[192:195], v[150:153]
	v_mfma_f32_16x16x32_bf16 v[146:149], v[82:85], v[192:195], v[146:149]
	v_mfma_f32_16x16x32_bf16 v[134:137], v[74:77], v[204:207], v[134:137]
	v_mfma_f32_16x16x32_bf16 v[130:133], v[82:85], v[204:207], v[130:133]
	v_mfma_f32_16x16x32_bf16 v[118:121], v[74:77], v[212:215], v[118:121]
	v_mfma_f32_16x16x32_bf16 v[114:117], v[82:85], v[212:215], v[114:117]
	v_mfma_f32_16x16x32_bf16 v[102:105], v[74:77], v[240:243], v[102:105]
	v_mfma_f32_16x16x32_bf16 v[98:101], v[82:85], v[240:243], v[98:101]
	v_mfma_f32_16x16x32_bf16 v[150:153], v[78:81], v[200:203], v[150:153]
	v_mfma_f32_16x16x32_bf16 v[146:149], v[86:89], v[200:203], v[146:149]
	v_mfma_f32_16x16x32_bf16 v[134:137], v[78:81], v[208:211], v[134:137]
	v_mfma_f32_16x16x32_bf16 v[130:133], v[86:89], v[208:211], v[130:133]
	v_mfma_f32_16x16x32_bf16 v[118:121], v[78:81], v[236:239], v[118:121]
	v_mfma_f32_16x16x32_bf16 v[114:117], v[86:89], v[236:239], v[114:117]
	v_mfma_f32_16x16x32_bf16 v[102:105], v[78:81], v[244:247], v[102:105]
	v_mfma_f32_16x16x32_bf16 v[98:101], v[86:89], v[244:247], v[98:101]
	s_setprio 0
	s_barrier
	s_add_i32 m0, s1, 0xffffff80
	s_add_u32 s50, s66, 0x40080
	ds_read_b128 v[192:195], v219 offset:49152
	ds_read_b128 v[200:203], v219 offset:50176
	ds_read_b128 v[204:207], v219 offset:51200
	ds_read_b128 v[208:211], v219 offset:52224
	ds_read_b128 v[212:215], v219 offset:53248
	ds_read_b128 v[236:239], v219 offset:54272
	ds_read_b128 v[240:243], v219 offset:55296
	ds_read_b128 v[244:247], v219 offset:56320
	global_load_lds_dwordx4 v166, s[66:67] offset:128
	v_lshl_add_u64 v[182:183], v[216:217], 0, s[18:19]
	s_mov_b32 m0, s14
	s_addc_u32 s51, s67, 0
	global_load_lds_dwordx4 v[182:183], off
	s_mov_b32 m0, s34
	s_nop 0
	global_load_lds_dwordx4 v166, s[50:51]
	s_mov_b32 m0, s35
	s_nop 0
	global_load_lds_dwordx4 v162, s[50:51]
	s_add_i32 m0, s15, 0xffffff80
	s_nop 0
	global_load_lds_dwordx4 v168, s[82:83] offset:128
	s_add_i32 m0, s31, 0xffffff80
	s_nop 0
	global_load_lds_dwordx4 v164, s[82:83] offset:128
	s_waitcnt vmcnt(8)
	s_waitcnt lgkmcnt(0)
	s_barrier
	s_setprio 1
	s_waitcnt lgkmcnt(0)
	v_mfma_f32_16x16x32_bf16 v[94:97], v[58:61], v[192:195], v[94:97]
	v_mfma_f32_16x16x32_bf16 v[90:93], v[66:69], v[192:195], v[90:93]
	v_mfma_f32_16x16x32_bf16 v[54:57], v[58:61], v[204:207], v[54:57]
	v_mfma_f32_16x16x32_bf16 v[42:45], v[66:69], v[204:207], v[42:45]
	v_mfma_f32_16x16x32_bf16 v[30:33], v[58:61], v[212:215], v[30:33]
	v_mfma_f32_16x16x32_bf16 v[26:29], v[66:69], v[212:215], v[26:29]
	v_mfma_f32_16x16x32_bf16 v[14:17], v[58:61], v[240:243], v[14:17]
	v_mfma_f32_16x16x32_bf16 v[10:13], v[66:69], v[240:243], v[10:13]
	v_mfma_f32_16x16x32_bf16 v[94:97], v[62:65], v[200:203], v[94:97]
	v_mfma_f32_16x16x32_bf16 v[90:93], v[70:73], v[200:203], v[90:93]
	v_mfma_f32_16x16x32_bf16 v[54:57], v[62:65], v[208:211], v[54:57]
	v_mfma_f32_16x16x32_bf16 v[42:45], v[70:73], v[208:211], v[42:45]
	v_mfma_f32_16x16x32_bf16 v[30:33], v[62:65], v[236:239], v[30:33]
	v_mfma_f32_16x16x32_bf16 v[26:29], v[70:73], v[236:239], v[26:29]
	v_mfma_f32_16x16x32_bf16 v[14:17], v[62:65], v[244:247], v[14:17]
	v_mfma_f32_16x16x32_bf16 v[10:13], v[70:73], v[244:247], v[10:13]
	s_setprio 0
	s_setprio 1
	v_mfma_f32_16x16x32_bf16 v[46:49], v[74:77], v[192:195], v[46:49]
	v_mfma_f32_16x16x32_bf16 v[70:73], v[78:81], v[200:203], v[46:49]
	v_mfma_f32_16x16x32_bf16 v[46:49], v[82:85], v[192:195], v[50:53]
	v_mfma_f32_16x16x32_bf16 v[38:41], v[74:77], v[204:207], v[38:41]
	v_mfma_f32_16x16x32_bf16 v[34:37], v[82:85], v[204:207], v[34:37]
	v_mfma_f32_16x16x32_bf16 v[22:25], v[74:77], v[212:215], v[22:25]
	v_mfma_f32_16x16x32_bf16 v[18:21], v[82:85], v[212:215], v[18:21]
	v_mfma_f32_16x16x32_bf16 v[6:9], v[74:77], v[240:243], v[6:9]
	v_mfma_f32_16x16x32_bf16 v[2:5], v[82:85], v[240:243], v[2:5]
	v_mfma_f32_16x16x32_bf16 v[66:69], v[86:89], v[200:203], v[46:49]
	v_mfma_f32_16x16x32_bf16 v[38:41], v[78:81], v[208:211], v[38:41]
	v_mfma_f32_16x16x32_bf16 v[34:37], v[86:89], v[208:211], v[34:37]
	v_mfma_f32_16x16x32_bf16 v[22:25], v[78:81], v[236:239], v[22:25]
	v_mfma_f32_16x16x32_bf16 v[18:21], v[86:89], v[236:239], v[18:21]
	v_mfma_f32_16x16x32_bf16 v[6:9], v[78:81], v[244:247], v[6:9]
	v_mfma_f32_16x16x32_bf16 v[2:5], v[86:89], v[244:247], v[2:5]
	s_setprio 0
	s_barrier
	s_add_i32 vcc_hi, vcc_hi, 2
	s_add_u32 s40, s40, 0x100
	s_addc_u32 s41, s41, 0
	s_add_u32 s59, s59, 0x100
	s_addc_u32 vcc_lo, vcc_lo, 0
	s_cmp_gt_u32 vcc_hi, 13
	s_cbranch_scc0 .LBB0_357
	v_readlane_b32 s40, v253, 55
	v_readlane_b32 s41, v253, 56
	s_and_b64 vcc, exec, s[40:41]
	s_cbranch_vccz .LBB0_360
	s_barrier

.LBB0_397:
	s_add_u32 s52, s48, s50
	s_addc_u32 s53, s49, s51
	v_or_b32_e32 v146, 0x10000, v145
	v_add_u32_e32 v150, 0x10400, v145
	v_add_u32_e32 v154, 0x10800, v145
	v_add_u32_e32 v158, 0x10c00, v145
	v_or_b32_e32 v162, 0x14000, v145
	v_add_u32_e32 v166, 0x14400, v145
	v_add_u32_e32 v170, 0x14800, v145
	v_add_u32_e32 v174, 0x14c00, v145
	s_add_u32 s52, s52, 0x100
	ds_read_b128 v[146:149], v146
	ds_read_b128 v[150:153], v150
	ds_read_b128 v[154:157], v154
	ds_read_b128 v[158:161], v158
	ds_read_b128 v[162:165], v162
	ds_read_b128 v[166:169], v166
	ds_read_b128 v[170:173], v170
	ds_read_b128 v[174:177], v174
	s_addc_u32 s53, s53, 0
	s_add_u32 s93, s39, s50
	s_addc_u32 s94, s41, s51
	s_cmpk_eq_i32 s50, 0x700
	s_cselect_b32 s55, s90, s53
	s_cselect_b32 s54, s91, s52
	s_cselect_b32 s53, s45, s94
	s_cselect_b32 s52, s44, s93
	v_lshl_add_u64 v[194:195], v[140:141], 0, s[50:51]
	s_add_i32 m0, s57, 0xc000
	ds_read_b128 v[178:181], v144
	ds_read_b128 v[182:185], v144 offset:1024
	ds_read_b128 v[186:189], v144 offset:2048
	ds_read_b128 v[190:193], v144 offset:3072
	ds_read_b128 v[200:203], v144 offset:4096
	ds_read_b128 v[204:207], v144 offset:5120
	ds_read_b128 v[208:211], v144 offset:6144
	ds_read_b128 v[212:215], v144 offset:7168
	global_load_lds_dwordx4 v[194:195], off
	v_lshl_add_u64 v[194:195], v[142:143], 0, s[50:51]
	s_add_i32 m0, s57, 0xe000
	s_nop 0
	global_load_lds_dwordx4 v[194:195], off
	s_waitcnt vmcnt(8)
	s_waitcnt lgkmcnt(0)
	s_barrier
	s_setprio 1
	s_waitcnt lgkmcnt(0)
	v_mfma_f32_16x16x32_bf16 v[126:129], v[146:149], v[178:181], v[126:129]
	v_mfma_f32_16x16x32_bf16 v[122:125], v[154:157], v[178:181], v[122:125]
	v_mfma_f32_16x16x32_bf16 v[110:113], v[146:149], v[186:189], v[110:113]
	v_mfma_f32_16x16x32_bf16 v[106:109], v[154:157], v[186:189], v[106:109]
	v_mfma_f32_16x16x32_bf16 v[94:97], v[146:149], v[200:203], v[94:97]
	v_mfma_f32_16x16x32_bf16 v[90:93], v[154:157], v[200:203], v[90:93]
	v_mfma_f32_16x16x32_bf16 v[78:81], v[146:149], v[208:211], v[78:81]
	v_mfma_f32_16x16x32_bf16 v[74:77], v[154:157], v[208:211], v[74:77]
	v_mfma_f32_16x16x32_bf16 v[126:129], v[150:153], v[182:185], v[126:129]
	v_mfma_f32_16x16x32_bf16 v[122:125], v[158:161], v[182:185], v[122:125]
	v_mfma_f32_16x16x32_bf16 v[110:113], v[150:153], v[190:193], v[110:113]
	v_mfma_f32_16x16x32_bf16 v[106:109], v[158:161], v[190:193], v[106:109]
	v_mfma_f32_16x16x32_bf16 v[94:97], v[150:153], v[204:207], v[94:97]
	v_mfma_f32_16x16x32_bf16 v[90:93], v[158:161], v[204:207], v[90:93]
	v_mfma_f32_16x16x32_bf16 v[78:81], v[150:153], v[212:215], v[78:81]
	v_mfma_f32_16x16x32_bf16 v[74:77], v[158:161], v[212:215], v[74:77]
	s_setprio 0
	s_setprio 1
	v_mfma_f32_16x16x32_bf16 v[118:121], v[162:165], v[178:181], v[118:121]
	v_mfma_f32_16x16x32_bf16 v[114:117], v[170:173], v[178:181], v[114:117]
	v_mfma_f32_16x16x32_bf16 v[102:105], v[162:165], v[186:189], v[102:105]
	v_mfma_f32_16x16x32_bf16 v[98:101], v[170:173], v[186:189], v[98:101]
	v_mfma_f32_16x16x32_bf16 v[86:89], v[162:165], v[200:203], v[86:89]
	v_mfma_f32_16x16x32_bf16 v[82:85], v[170:173], v[200:203], v[82:85]
	v_mfma_f32_16x16x32_bf16 v[70:73], v[162:165], v[208:211], v[70:73]
	v_mfma_f32_16x16x32_bf16 v[66:69], v[170:173], v[208:211], v[66:69]
	v_mfma_f32_16x16x32_bf16 v[118:121], v[166:169], v[182:185], v[118:121]
	v_mfma_f32_16x16x32_bf16 v[114:117], v[174:177], v[182:185], v[114:117]
	v_mfma_f32_16x16x32_bf16 v[102:105], v[166:169], v[190:193], v[102:105]
	v_mfma_f32_16x16x32_bf16 v[98:101], v[174:177], v[190:193], v[98:101]
	v_mfma_f32_16x16x32_bf16 v[86:89], v[166:169], v[204:207], v[86:89]
	v_mfma_f32_16x16x32_bf16 v[82:85], v[174:177], v[204:207], v[82:85]
	v_mfma_f32_16x16x32_bf16 v[70:73], v[166:169], v[212:215], v[70:73]
	v_mfma_f32_16x16x32_bf16 v[66:69], v[174:177], v[212:215], v[66:69]
	s_setprio 0
	s_barrier
	s_mov_b32 m0, s58
	v_lshl_add_u64 v[194:195], s[52:53], 0, v[0:1]
	s_add_u32 s94, s52, 0x40000
	ds_read_b128 v[178:181], v144 offset:16384
	ds_read_b128 v[182:185], v144 offset:17408
	ds_read_b128 v[186:189], v144 offset:18432
	ds_read_b128 v[190:193], v144 offset:19456
	ds_read_b128 v[200:203], v144 offset:20480
	ds_read_b128 v[204:207], v144 offset:21504
	ds_read_b128 v[208:211], v144 offset:22528
	ds_read_b128 v[212:215], v144 offset:23552
	global_load_lds_dwordx4 v0, s[52:53]
	v_lshl_add_u64 v[216:217], s[52:53], 0, v[130:131]
	s_mov_b32 m0, s59
	s_addc_u32 s95, s53, 0
	global_load_lds_dwordx4 v130, s[52:53]
	s_mov_b32 m0, s60
	v_lshl_add_u64 v[220:221], s[54:55], 0, v[132:133]
	global_load_lds_dwordx4 v0, s[94:95]
	s_mov_b32 m0, s61
	s_nop 0
	global_load_lds_dwordx4 v130, s[94:95]
	v_lshl_add_u64 v[218:219], s[54:55], 0, v[134:135]
	s_mov_b32 m0, s57
	s_nop 0
	global_load_lds_dwordx4 v134, s[54:55]
	s_mov_b32 m0, s64
	s_nop 0
	global_load_lds_dwordx4 v132, s[54:55]
	s_waitcnt vmcnt(8)
	s_waitcnt lgkmcnt(0)
	s_barrier
	s_setprio 1
	s_waitcnt lgkmcnt(0)
	v_mfma_f32_16x16x32_bf16 v[62:65], v[146:149], v[178:181], v[62:65]
	v_mfma_f32_16x16x32_bf16 v[58:61], v[154:157], v[178:181], v[58:61]
	v_mfma_f32_16x16x32_bf16 v[46:49], v[146:149], v[186:189], v[46:49]
	v_mfma_f32_16x16x32_bf16 v[42:45], v[154:157], v[186:189], v[42:45]
	v_mfma_f32_16x16x32_bf16 v[30:33], v[146:149], v[200:203], v[30:33]
	v_mfma_f32_16x16x32_bf16 v[26:29], v[154:157], v[200:203], v[26:29]
	v_mfma_f32_16x16x32_bf16 v[14:17], v[146:149], v[208:211], v[14:17]
	v_mfma_f32_16x16x32_bf16 v[10:13], v[154:157], v[208:211], v[10:13]
	v_mfma_f32_16x16x32_bf16 v[62:65], v[150:153], v[182:185], v[62:65]
	v_mfma_f32_16x16x32_bf16 v[58:61], v[158:161], v[182:185], v[58:61]
	v_mfma_f32_16x16x32_bf16 v[46:49], v[150:153], v[190:193], v[46:49]
	v_mfma_f32_16x16x32_bf16 v[42:45], v[158:161], v[190:193], v[42:45]
	v_mfma_f32_16x16x32_bf16 v[30:33], v[150:153], v[204:207], v[30:33]
	v_mfma_f32_16x16x32_bf16 v[26:29], v[158:161], v[204:207], v[26:29]
	v_mfma_f32_16x16x32_bf16 v[14:17], v[150:153], v[212:215], v[14:17]
	v_mfma_f32_16x16x32_bf16 v[10:13], v[158:161], v[212:215], v[10:13]
	s_setprio 0
	s_setprio 1
	v_mfma_f32_16x16x32_bf16 v[54:57], v[162:165], v[178:181], v[54:57]
	v_mfma_f32_16x16x32_bf16 v[50:53], v[170:173], v[178:181], v[50:53]
	v_mfma_f32_16x16x32_bf16 v[38:41], v[162:165], v[186:189], v[38:41]
	v_mfma_f32_16x16x32_bf16 v[34:37], v[170:173], v[186:189], v[34:37]
	v_mfma_f32_16x16x32_bf16 v[22:25], v[162:165], v[200:203], v[22:25]
	v_mfma_f32_16x16x32_bf16 v[18:21], v[170:173], v[200:203], v[18:21]
	v_mfma_f32_16x16x32_bf16 v[6:9], v[162:165], v[208:211], v[6:9]
	v_mfma_f32_16x16x32_bf16 v[2:5], v[170:173], v[208:211], v[2:5]
	v_mfma_f32_16x16x32_bf16 v[54:57], v[166:169], v[182:185], v[54:57]
	v_mfma_f32_16x16x32_bf16 v[50:53], v[174:177], v[182:185], v[50:53]
	v_mfma_f32_16x16x32_bf16 v[38:41], v[166:169], v[190:193], v[38:41]
	v_mfma_f32_16x16x32_bf16 v[34:37], v[174:177], v[190:193], v[34:37]
	v_mfma_f32_16x16x32_bf16 v[22:25], v[166:169], v[204:207], v[22:25]
	v_mfma_f32_16x16x32_bf16 v[18:21], v[174:177], v[204:207], v[18:21]
	v_mfma_f32_16x16x32_bf16 v[6:9], v[166:169], v[212:215], v[6:9]
	v_mfma_f32_16x16x32_bf16 v[2:5], v[174:177], v[212:215], v[2:5]
	s_setprio 0
	s_barrier
	v_or_b32_e32 v146, 0x18000, v145
	v_add_u32_e32 v150, 0x18400, v145
	v_add_u32_e32 v154, 0x18800, v145
	v_add_u32_e32 v158, 0x18c00, v145
	v_or_b32_e32 v162, 0x1c000, v145
	v_add_u32_e32 v166, 0x1c400, v145
	v_add_u32_e32 v170, 0x1c800, v145
	v_add_u32_e32 v174, 0x1cc00, v145
	ds_read_b128 v[146:149], v146
	ds_read_b128 v[150:153], v150
	ds_read_b128 v[154:157], v154
	ds_read_b128 v[158:161], v158
	ds_read_b128 v[162:165], v162
	ds_read_b128 v[166:169], v166
	ds_read_b128 v[170:173], v170
	ds_read_b128 v[174:177], v174
	s_add_u32 s54, s54, 0x40000
	s_addc_u32 s55, s55, 0
	s_mov_b32 m0, s65
	ds_read_b128 v[178:181], v144 offset:32768
	ds_read_b128 v[182:185], v144 offset:33792
	ds_read_b128 v[186:189], v144 offset:34816
	ds_read_b128 v[190:193], v144 offset:35840
	ds_read_b128 v[200:203], v144 offset:36864
	ds_read_b128 v[204:207], v144 offset:37888
	ds_read_b128 v[208:211], v144 offset:38912
	ds_read_b128 v[212:215], v144 offset:39936
	global_load_lds_dwordx4 v134, s[54:55]
	s_mov_b32 m0, s66
	s_nop 0
	global_load_lds_dwordx4 v132, s[54:55]
	s_waitcnt vmcnt(8)
	s_waitcnt lgkmcnt(0)
	s_barrier
	s_setprio 1
	s_waitcnt lgkmcnt(0)
	v_mfma_f32_16x16x32_bf16 v[126:129], v[146:149], v[178:181], v[126:129]
	v_mfma_f32_16x16x32_bf16 v[122:125], v[154:157], v[178:181], v[122:125]
	v_mfma_f32_16x16x32_bf16 v[110:113], v[146:149], v[186:189], v[110:113]
	v_mfma_f32_16x16x32_bf16 v[106:109], v[154:157], v[186:189], v[106:109]
	v_mfma_f32_16x16x32_bf16 v[94:97], v[146:149], v[200:203], v[94:97]
	v_mfma_f32_16x16x32_bf16 v[90:93], v[154:157], v[200:203], v[90:93]
	v_mfma_f32_16x16x32_bf16 v[78:81], v[146:149], v[208:211], v[78:81]
	v_mfma_f32_16x16x32_bf16 v[74:77], v[154:157], v[208:211], v[74:77]
	v_mfma_f32_16x16x32_bf16 v[126:129], v[150:153], v[182:185], v[126:129]
	v_mfma_f32_16x16x32_bf16 v[122:125], v[158:161], v[182:185], v[122:125]
	v_mfma_f32_16x16x32_bf16 v[110:113], v[150:153], v[190:193], v[110:113]
	v_mfma_f32_16x16x32_bf16 v[106:109], v[158:161], v[190:193], v[106:109]
	v_mfma_f32_16x16x32_bf16 v[94:97], v[150:153], v[204:207], v[94:97]
	v_mfma_f32_16x16x32_bf16 v[90:93], v[158:161], v[204:207], v[90:93]
	v_mfma_f32_16x16x32_bf16 v[78:81], v[150:153], v[212:215], v[78:81]
	v_mfma_f32_16x16x32_bf16 v[74:77], v[158:161], v[212:215], v[74:77]
	s_setprio 0
	s_setprio 1
	v_mfma_f32_16x16x32_bf16 v[118:121], v[162:165], v[178:181], v[118:121]
	v_mfma_f32_16x16x32_bf16 v[114:117], v[170:173], v[178:181], v[114:117]
	v_mfma_f32_16x16x32_bf16 v[102:105], v[162:165], v[186:189], v[102:105]
	v_mfma_f32_16x16x32_bf16 v[98:101], v[170:173], v[186:189], v[98:101]
	v_mfma_f32_16x16x32_bf16 v[86:89], v[162:165], v[200:203], v[86:89]
	v_mfma_f32_16x16x32_bf16 v[82:85], v[170:173], v[200:203], v[82:85]
	v_mfma_f32_16x16x32_bf16 v[70:73], v[162:165], v[208:211], v[70:73]
	v_mfma_f32_16x16x32_bf16 v[66:69], v[170:173], v[208:211], v[66:69]
	v_mfma_f32_16x16x32_bf16 v[118:121], v[166:169], v[182:185], v[118:121]
	v_mfma_f32_16x16x32_bf16 v[114:117], v[174:177], v[182:185], v[114:117]
	v_mfma_f32_16x16x32_bf16 v[102:105], v[166:169], v[190:193], v[102:105]
	v_mfma_f32_16x16x32_bf16 v[98:101], v[174:177], v[190:193], v[98:101]
	v_mfma_f32_16x16x32_bf16 v[86:89], v[166:169], v[204:207], v[86:89]
	v_mfma_f32_16x16x32_bf16 v[82:85], v[174:177], v[204:207], v[82:85]
	v_mfma_f32_16x16x32_bf16 v[70:73], v[166:169], v[212:215], v[70:73]
	v_mfma_f32_16x16x32_bf16 v[66:69], v[174:177], v[212:215], v[66:69]
	s_setprio 0
	s_barrier
	s_mov_b32 m0, s67
	v_lshl_add_u64 v[194:195], v[194:195], 0, s[18:19]
	s_add_u32 s52, s52, 0x40080
	ds_read_b128 v[178:181], v144 offset:49152
	ds_read_b128 v[182:185], v144 offset:50176
	ds_read_b128 v[186:189], v144 offset:51200
	ds_read_b128 v[190:193], v144 offset:52224
	ds_read_b128 v[200:203], v144 offset:53248
	ds_read_b128 v[204:207], v144 offset:54272
	ds_read_b128 v[208:211], v144 offset:55296
	ds_read_b128 v[212:215], v144 offset:56320
	global_load_lds_dwordx4 v[194:195], off
	v_lshl_add_u64 v[194:195], v[216:217], 0, s[18:19]
	s_mov_b32 m0, s80
	s_addc_u32 s53, s53, 0
	global_load_lds_dwordx4 v[194:195], off
	s_mov_b32 m0, s84
	s_nop 0
	global_load_lds_dwordx4 v0, s[52:53]
	s_mov_b32 m0, s85
	s_nop 0
	global_load_lds_dwordx4 v130, s[52:53]
	v_lshl_add_u64 v[194:195], v[218:219], 0, s[18:19]
	s_mov_b32 m0, s82
	s_nop 0
	global_load_lds_dwordx4 v[194:195], off
	v_lshl_add_u64 v[194:195], v[220:221], 0, s[18:19]
	s_mov_b32 m0, s83
	s_nop 0
	global_load_lds_dwordx4 v[194:195], off
	s_waitcnt vmcnt(8)
	s_waitcnt lgkmcnt(0)
	s_barrier
	s_setprio 1
	s_waitcnt lgkmcnt(0)
	v_mfma_f32_16x16x32_bf16 v[62:65], v[146:149], v[178:181], v[62:65]
	v_mfma_f32_16x16x32_bf16 v[58:61], v[154:157], v[178:181], v[58:61]
	v_mfma_f32_16x16x32_bf16 v[46:49], v[146:149], v[186:189], v[46:49]
	v_mfma_f32_16x16x32_bf16 v[42:45], v[154:157], v[186:189], v[42:45]
	v_mfma_f32_16x16x32_bf16 v[30:33], v[146:149], v[200:203], v[30:33]
	v_mfma_f32_16x16x32_bf16 v[26:29], v[154:157], v[200:203], v[26:29]
	v_mfma_f32_16x16x32_bf16 v[14:17], v[146:149], v[208:211], v[14:17]
	v_mfma_f32_16x16x32_bf16 v[10:13], v[154:157], v[208:211], v[10:13]
	v_mfma_f32_16x16x32_bf16 v[62:65], v[150:153], v[182:185], v[62:65]
	v_mfma_f32_16x16x32_bf16 v[58:61], v[158:161], v[182:185], v[58:61]
	v_mfma_f32_16x16x32_bf16 v[46:49], v[150:153], v[190:193], v[46:49]
	v_mfma_f32_16x16x32_bf16 v[42:45], v[158:161], v[190:193], v[42:45]
	v_mfma_f32_16x16x32_bf16 v[30:33], v[150:153], v[204:207], v[30:33]
	v_mfma_f32_16x16x32_bf16 v[26:29], v[158:161], v[204:207], v[26:29]
	v_mfma_f32_16x16x32_bf16 v[14:17], v[150:153], v[212:215], v[14:17]
	v_mfma_f32_16x16x32_bf16 v[10:13], v[158:161], v[212:215], v[10:13]
	s_setprio 0
	s_setprio 1
	v_mfma_f32_16x16x32_bf16 v[54:57], v[162:165], v[178:181], v[54:57]
	v_mfma_f32_16x16x32_bf16 v[50:53], v[170:173], v[178:181], v[50:53]
	v_mfma_f32_16x16x32_bf16 v[38:41], v[162:165], v[186:189], v[38:41]
	v_mfma_f32_16x16x32_bf16 v[34:37], v[170:173], v[186:189], v[34:37]
	v_mfma_f32_16x16x32_bf16 v[22:25], v[162:165], v[200:203], v[22:25]
	v_mfma_f32_16x16x32_bf16 v[18:21], v[170:173], v[200:203], v[18:21]
	v_mfma_f32_16x16x32_bf16 v[6:9], v[162:165], v[208:211], v[6:9]
	v_mfma_f32_16x16x32_bf16 v[2:5], v[170:173], v[208:211], v[2:5]
	v_mfma_f32_16x16x32_bf16 v[54:57], v[166:169], v[182:185], v[54:57]
	v_mfma_f32_16x16x32_bf16 v[50:53], v[174:177], v[182:185], v[50:53]
	v_mfma_f32_16x16x32_bf16 v[38:41], v[166:169], v[190:193], v[38:41]
	v_mfma_f32_16x16x32_bf16 v[34:37], v[174:177], v[190:193], v[34:37]
	v_mfma_f32_16x16x32_bf16 v[22:25], v[166:169], v[204:207], v[22:25]
	v_mfma_f32_16x16x32_bf16 v[18:21], v[174:177], v[204:207], v[18:21]
	v_mfma_f32_16x16x32_bf16 v[6:9], v[166:169], v[212:215], v[6:9]
	v_mfma_f32_16x16x32_bf16 v[2:5], v[174:177], v[212:215], v[2:5]
	s_setprio 0
	s_barrier
	s_add_i32 s92, s92, 2
	s_add_u32 s50, s50, 0x100
	s_addc_u32 s51, s51, 0
	s_cmp_gt_u32 s92, 13
	s_cbranch_scc0 .LBB0_397
	s_and_b64 vcc, exec, s[14:15]
	s_cbranch_vccz .LBB0_400
	s_barrier

.LBB0_438:
	v_or_b32_e32 v163, 0x10000, v162
	v_add_u32_e32 v168, 0x10400, v162
	ds_read_b128 v[164:167], v163
	ds_read_b128 v[168:171], v168
	v_add_u32_e32 v163, 0x10800, v162
	v_add_u32_e32 v176, 0x10c00, v162
	s_add_u32 s50, s16, s48
	ds_read_b128 v[172:175], v163
	ds_read_b128 v[176:179], v176
	v_or_b32_e32 v163, 0x14000, v162
	v_add_u32_e32 v184, 0x14400, v162
	s_addc_u32 s51, s17, s49
	ds_read_b128 v[180:183], v163
	ds_read_b128 v[184:187], v184
	v_add_u32_e32 v163, 0x14800, v162
	v_add_u32_e32 v192, 0x14c00, v162
	s_add_u32 s50, s50, 0x100
	ds_read_b128 v[188:191], v163
	ds_read_b128 v[192:195], v192
	s_addc_u32 s51, s51, 0
	s_add_u32 s91, s41, s48
	s_addc_u32 s92, s89, s49
	s_cmpk_eq_i32 s48, 0x700
	s_cselect_b32 s53, s29, s51
	s_cselect_b32 s52, s39, s50
	s_cselect_b32 s51, s45, s92
	s_cselect_b32 s50, s44, s91
	v_lshl_add_u64 v[226:227], v[156:157], 0, s[48:49]
	s_add_i32 m0, s58, 0xc000
	ds_read_b128 v[200:203], v161
	ds_read_b128 v[204:207], v161 offset:1024
	ds_read_b128 v[208:211], v161 offset:2048
	ds_read_b128 v[212:215], v161 offset:3072
	ds_read_b128 v[216:219], v161 offset:4096
	ds_read_b128 v[220:223], v161 offset:5120
	ds_read_b128 v[236:239], v161 offset:6144
	ds_read_b128 v[240:243], v161 offset:7168
	global_load_lds_dwordx4 v[226:227], off
	v_lshl_add_u64 v[226:227], v[158:159], 0, s[48:49]
	s_add_i32 m0, s58, 0xe000
	s_nop 0
	global_load_lds_dwordx4 v[226:227], off
	s_waitcnt vmcnt(8)
	s_waitcnt lgkmcnt(0)
	s_barrier
	s_setprio 1
	s_waitcnt lgkmcnt(0)
	v_mfma_f32_16x16x32_bf16 v[126:129], v[164:167], v[200:203], v[126:129]
	v_mfma_f32_16x16x32_bf16 v[122:125], v[172:175], v[200:203], v[122:125]
	v_mfma_f32_16x16x32_bf16 v[110:113], v[164:167], v[208:211], v[110:113]
	v_mfma_f32_16x16x32_bf16 v[106:109], v[172:175], v[208:211], v[106:109]
	v_mfma_f32_16x16x32_bf16 v[94:97], v[164:167], v[216:219], v[94:97]
	v_mfma_f32_16x16x32_bf16 v[90:93], v[172:175], v[216:219], v[90:93]
	v_mfma_f32_16x16x32_bf16 v[86:89], v[164:167], v[236:239], v[86:89]
	v_mfma_f32_16x16x32_bf16 v[78:81], v[172:175], v[236:239], v[78:81]
	v_mfma_f32_16x16x32_bf16 v[126:129], v[168:171], v[204:207], v[126:129]
	v_mfma_f32_16x16x32_bf16 v[122:125], v[176:179], v[204:207], v[122:125]
	v_mfma_f32_16x16x32_bf16 v[110:113], v[168:171], v[212:215], v[110:113]
	v_mfma_f32_16x16x32_bf16 v[106:109], v[176:179], v[212:215], v[106:109]
	v_mfma_f32_16x16x32_bf16 v[94:97], v[168:171], v[220:223], v[94:97]
	v_mfma_f32_16x16x32_bf16 v[90:93], v[176:179], v[220:223], v[90:93]
	v_mfma_f32_16x16x32_bf16 v[86:89], v[168:171], v[240:243], v[86:89]
	v_mfma_f32_16x16x32_bf16 v[78:81], v[176:179], v[240:243], v[78:81]
	s_setprio 0
	s_setprio 1
	v_mfma_f32_16x16x32_bf16 v[118:121], v[180:183], v[200:203], v[118:121]
	v_mfma_f32_16x16x32_bf16 v[114:117], v[188:191], v[200:203], v[114:117]
	v_mfma_f32_16x16x32_bf16 v[102:105], v[180:183], v[208:211], v[102:105]
	v_mfma_f32_16x16x32_bf16 v[98:101], v[188:191], v[208:211], v[98:101]
	v_mfma_f32_16x16x32_bf16 v[82:85], v[180:183], v[216:219], v[82:85]
	v_mfma_f32_16x16x32_bf16 v[74:77], v[188:191], v[216:219], v[74:77]
	v_mfma_f32_16x16x32_bf16 v[70:73], v[180:183], v[236:239], v[70:73]
	v_mfma_f32_16x16x32_bf16 v[66:69], v[188:191], v[236:239], v[66:69]
	v_mfma_f32_16x16x32_bf16 v[118:121], v[184:187], v[204:207], v[118:121]
	v_mfma_f32_16x16x32_bf16 v[114:117], v[192:195], v[204:207], v[114:117]
	v_mfma_f32_16x16x32_bf16 v[102:105], v[184:187], v[212:215], v[102:105]
	v_mfma_f32_16x16x32_bf16 v[98:101], v[192:195], v[212:215], v[98:101]
	v_mfma_f32_16x16x32_bf16 v[82:85], v[184:187], v[220:223], v[82:85]
	v_mfma_f32_16x16x32_bf16 v[74:77], v[192:195], v[220:223], v[74:77]
	v_mfma_f32_16x16x32_bf16 v[70:73], v[184:187], v[240:243], v[70:73]
	v_mfma_f32_16x16x32_bf16 v[66:69], v[192:195], v[240:243], v[66:69]
	s_setprio 0
	s_barrier
	s_mov_b32 m0, s59
	v_lshl_add_u64 v[226:227], s[50:51], 0, v[0:1]
	s_add_u32 s92, s50, 0x40000
	ds_read_b128 v[200:203], v161 offset:16384
	ds_read_b128 v[204:207], v161 offset:17408
	ds_read_b128 v[208:211], v161 offset:18432
	ds_read_b128 v[212:215], v161 offset:19456
	ds_read_b128 v[216:219], v161 offset:20480
	ds_read_b128 v[220:223], v161 offset:21504
	ds_read_b128 v[236:239], v161 offset:22528
	ds_read_b128 v[240:243], v161 offset:23552
	global_load_lds_dwordx4 v0, s[50:51]
	v_lshl_add_u64 v[244:245], s[50:51], 0, v[142:143]
	s_mov_b32 m0, s60
	s_addc_u32 s93, s51, 0
	global_load_lds_dwordx4 v142, s[50:51]
	s_mov_b32 m0, s61
	v_lshl_add_u64 v[248:249], s[52:53], 0, v[144:145]
	global_load_lds_dwordx4 v0, s[92:93]
	s_mov_b32 m0, s62
	s_nop 0
	global_load_lds_dwordx4 v142, s[92:93]
	v_lshl_add_u64 v[246:247], s[52:53], 0, v[148:149]
	s_mov_b32 m0, s58
	s_nop 0
	global_load_lds_dwordx4 v148, s[52:53]
	s_mov_b32 m0, s63
	s_nop 0
	global_load_lds_dwordx4 v144, s[52:53]
	s_waitcnt vmcnt(8)
	s_waitcnt lgkmcnt(0)
	s_barrier
	s_setprio 1
	s_waitcnt lgkmcnt(0)
	v_mfma_f32_16x16x32_bf16 v[62:65], v[164:167], v[200:203], v[62:65]
	v_mfma_f32_16x16x32_bf16 v[58:61], v[172:175], v[200:203], v[58:61]
	v_mfma_f32_16x16x32_bf16 v[54:57], v[164:167], v[208:211], v[54:57]
	v_mfma_f32_16x16x32_bf16 v[46:49], v[172:175], v[208:211], v[46:49]
	v_mfma_f32_16x16x32_bf16 v[30:33], v[164:167], v[216:219], v[30:33]
	v_mfma_f32_16x16x32_bf16 v[26:29], v[172:175], v[216:219], v[26:29]
	v_mfma_f32_16x16x32_bf16 v[22:25], v[164:167], v[236:239], v[22:25]
	v_mfma_f32_16x16x32_bf16 v[14:17], v[172:175], v[236:239], v[14:17]
	v_mfma_f32_16x16x32_bf16 v[62:65], v[168:171], v[204:207], v[62:65]
	v_mfma_f32_16x16x32_bf16 v[58:61], v[176:179], v[204:207], v[58:61]
	v_mfma_f32_16x16x32_bf16 v[54:57], v[168:171], v[212:215], v[54:57]
	v_mfma_f32_16x16x32_bf16 v[46:49], v[176:179], v[212:215], v[46:49]
	v_mfma_f32_16x16x32_bf16 v[30:33], v[168:171], v[220:223], v[30:33]
	v_mfma_f32_16x16x32_bf16 v[26:29], v[176:179], v[220:223], v[26:29]
	v_mfma_f32_16x16x32_bf16 v[22:25], v[168:171], v[240:243], v[22:25]
	v_mfma_f32_16x16x32_bf16 v[14:17], v[176:179], v[240:243], v[14:17]
	s_setprio 0
	s_setprio 1
	v_mfma_f32_16x16x32_bf16 v[50:53], v[180:183], v[200:203], v[50:53]
	v_mfma_f32_16x16x32_bf16 v[42:45], v[188:191], v[200:203], v[42:45]
	v_mfma_f32_16x16x32_bf16 v[38:41], v[180:183], v[208:211], v[38:41]
	v_mfma_f32_16x16x32_bf16 v[34:37], v[188:191], v[208:211], v[34:37]
	v_mfma_f32_16x16x32_bf16 v[18:21], v[180:183], v[216:219], v[18:21]
	v_mfma_f32_16x16x32_bf16 v[10:13], v[188:191], v[216:219], v[10:13]
	v_mfma_f32_16x16x32_bf16 v[6:9], v[180:183], v[236:239], v[6:9]
	v_mfma_f32_16x16x32_bf16 v[2:5], v[188:191], v[236:239], v[2:5]
	v_mfma_f32_16x16x32_bf16 v[50:53], v[184:187], v[204:207], v[50:53]
	v_mfma_f32_16x16x32_bf16 v[42:45], v[192:195], v[204:207], v[42:45]
	v_mfma_f32_16x16x32_bf16 v[38:41], v[184:187], v[212:215], v[38:41]
	v_mfma_f32_16x16x32_bf16 v[34:37], v[192:195], v[212:215], v[34:37]
	v_mfma_f32_16x16x32_bf16 v[18:21], v[184:187], v[220:223], v[18:21]
	v_mfma_f32_16x16x32_bf16 v[10:13], v[192:195], v[220:223], v[10:13]
	v_mfma_f32_16x16x32_bf16 v[6:9], v[184:187], v[240:243], v[6:9]
	v_mfma_f32_16x16x32_bf16 v[2:5], v[192:195], v[240:243], v[2:5]
	s_setprio 0
	s_barrier
	v_or_b32_e32 v163, 0x18000, v162
	v_add_u32_e32 v168, 0x18400, v162
	ds_read_b128 v[164:167], v163
	ds_read_b128 v[168:171], v168
	v_add_u32_e32 v163, 0x18800, v162
	v_add_u32_e32 v176, 0x18c00, v162
	ds_read_b128 v[172:175], v163
	ds_read_b128 v[176:179], v176
	v_or_b32_e32 v163, 0x1c000, v162
	v_add_u32_e32 v184, 0x1c400, v162
	ds_read_b128 v[180:183], v163
	ds_read_b128 v[184:187], v184
	v_add_u32_e32 v163, 0x1c800, v162
	v_add_u32_e32 v192, 0x1cc00, v162
	ds_read_b128 v[188:191], v163
	ds_read_b128 v[192:195], v192
	s_add_u32 s52, s52, 0x40000
	s_addc_u32 s53, s53, 0
	s_mov_b32 m0, s64
	v_lshl_add_u64 v[228:229], s[52:53], 0, v[148:149]
	ds_read_b128 v[200:203], v161 offset:32768
	ds_read_b128 v[204:207], v161 offset:33792
	ds_read_b128 v[208:211], v161 offset:34816
	ds_read_b128 v[212:215], v161 offset:35840
	ds_read_b128 v[216:219], v161 offset:36864
	ds_read_b128 v[220:223], v161 offset:37888
	ds_read_b128 v[236:239], v161 offset:38912
	ds_read_b128 v[240:243], v161 offset:39936
	global_load_lds_dwordx4 v148, s[52:53]
	v_lshl_add_u64 v[228:229], s[52:53], 0, v[144:145]
	s_mov_b32 m0, s65
	s_nop 0
	global_load_lds_dwordx4 v144, s[52:53]
	s_waitcnt vmcnt(8)
	s_waitcnt lgkmcnt(0)
	s_barrier
	s_setprio 1
	s_waitcnt lgkmcnt(0)
	v_mfma_f32_16x16x32_bf16 v[126:129], v[164:167], v[200:203], v[126:129]
	v_mfma_f32_16x16x32_bf16 v[122:125], v[172:175], v[200:203], v[122:125]
	v_mfma_f32_16x16x32_bf16 v[110:113], v[164:167], v[208:211], v[110:113]
	v_mfma_f32_16x16x32_bf16 v[106:109], v[172:175], v[208:211], v[106:109]
	v_mfma_f32_16x16x32_bf16 v[94:97], v[164:167], v[216:219], v[94:97]
	v_mfma_f32_16x16x32_bf16 v[90:93], v[172:175], v[216:219], v[90:93]
	v_mfma_f32_16x16x32_bf16 v[86:89], v[164:167], v[236:239], v[86:89]
	v_mfma_f32_16x16x32_bf16 v[78:81], v[172:175], v[236:239], v[78:81]
	v_mfma_f32_16x16x32_bf16 v[126:129], v[168:171], v[204:207], v[126:129]
	v_mfma_f32_16x16x32_bf16 v[122:125], v[176:179], v[204:207], v[122:125]
	v_mfma_f32_16x16x32_bf16 v[110:113], v[168:171], v[212:215], v[110:113]
	v_mfma_f32_16x16x32_bf16 v[106:109], v[176:179], v[212:215], v[106:109]
	v_mfma_f32_16x16x32_bf16 v[94:97], v[168:171], v[220:223], v[94:97]
	v_mfma_f32_16x16x32_bf16 v[90:93], v[176:179], v[220:223], v[90:93]
	v_mfma_f32_16x16x32_bf16 v[86:89], v[168:171], v[240:243], v[86:89]
	v_mfma_f32_16x16x32_bf16 v[78:81], v[176:179], v[240:243], v[78:81]
	s_setprio 0
	s_setprio 1
	v_mfma_f32_16x16x32_bf16 v[118:121], v[180:183], v[200:203], v[118:121]
	v_mfma_f32_16x16x32_bf16 v[114:117], v[188:191], v[200:203], v[114:117]
	v_mfma_f32_16x16x32_bf16 v[102:105], v[180:183], v[208:211], v[102:105]
	v_mfma_f32_16x16x32_bf16 v[98:101], v[188:191], v[208:211], v[98:101]
	v_mfma_f32_16x16x32_bf16 v[82:85], v[180:183], v[216:219], v[82:85]
	v_mfma_f32_16x16x32_bf16 v[74:77], v[188:191], v[216:219], v[74:77]
	v_mfma_f32_16x16x32_bf16 v[70:73], v[180:183], v[236:239], v[70:73]
	v_mfma_f32_16x16x32_bf16 v[66:69], v[188:191], v[236:239], v[66:69]
	v_mfma_f32_16x16x32_bf16 v[118:121], v[184:187], v[204:207], v[118:121]
	v_mfma_f32_16x16x32_bf16 v[114:117], v[192:195], v[204:207], v[114:117]
	v_mfma_f32_16x16x32_bf16 v[102:105], v[184:187], v[212:215], v[102:105]
	v_mfma_f32_16x16x32_bf16 v[98:101], v[192:195], v[212:215], v[98:101]
	v_mfma_f32_16x16x32_bf16 v[82:85], v[184:187], v[220:223], v[82:85]
	v_mfma_f32_16x16x32_bf16 v[74:77], v[192:195], v[220:223], v[74:77]
	v_mfma_f32_16x16x32_bf16 v[70:73], v[184:187], v[240:243], v[70:73]
	v_mfma_f32_16x16x32_bf16 v[66:69], v[192:195], v[240:243], v[66:69]
	s_setprio 0
	s_barrier
	s_mov_b32 m0, s66
	v_lshl_add_u64 v[226:227], v[226:227], 0, s[18:19]
	s_add_u32 s50, s50, 0x40080
	ds_read_b128 v[200:203], v161 offset:49152
	ds_read_b128 v[204:207], v161 offset:50176
	ds_read_b128 v[208:211], v161 offset:51200
	ds_read_b128 v[212:215], v161 offset:52224
	ds_read_b128 v[216:219], v161 offset:53248
	ds_read_b128 v[220:223], v161 offset:54272
	ds_read_b128 v[236:239], v161 offset:55296
	ds_read_b128 v[240:243], v161 offset:56320
	global_load_lds_dwordx4 v[226:227], off
	v_lshl_add_u64 v[226:227], v[244:245], 0, s[18:19]
	s_mov_b32 m0, s67
	s_addc_u32 s51, s51, 0
	global_load_lds_dwordx4 v[226:227], off
	s_mov_b32 m0, s83
	s_nop 0
	global_load_lds_dwordx4 v0, s[50:51]
	s_mov_b32 m0, s84
	s_nop 0
	global_load_lds_dwordx4 v142, s[50:51]
	v_lshl_add_u64 v[226:227], v[246:247], 0, s[18:19]
	s_mov_b32 m0, s80
	s_nop 0
	global_load_lds_dwordx4 v[226:227], off
	v_lshl_add_u64 v[226:227], v[248:249], 0, s[18:19]
	s_mov_b32 m0, s82
	s_nop 0
	global_load_lds_dwordx4 v[226:227], off
	s_waitcnt vmcnt(8)
	s_waitcnt lgkmcnt(0)
	s_barrier
	s_setprio 1
	s_waitcnt lgkmcnt(0)
	v_mfma_f32_16x16x32_bf16 v[62:65], v[164:167], v[200:203], v[62:65]
	v_mfma_f32_16x16x32_bf16 v[58:61], v[172:175], v[200:203], v[58:61]
	v_mfma_f32_16x16x32_bf16 v[54:57], v[164:167], v[208:211], v[54:57]
	v_mfma_f32_16x16x32_bf16 v[46:49], v[172:175], v[208:211], v[46:49]
	v_mfma_f32_16x16x32_bf16 v[30:33], v[164:167], v[216:219], v[30:33]
	v_mfma_f32_16x16x32_bf16 v[26:29], v[172:175], v[216:219], v[26:29]
	v_mfma_f32_16x16x32_bf16 v[22:25], v[164:167], v[236:239], v[22:25]
	v_mfma_f32_16x16x32_bf16 v[14:17], v[172:175], v[236:239], v[14:17]
	v_mfma_f32_16x16x32_bf16 v[62:65], v[168:171], v[204:207], v[62:65]
	v_mfma_f32_16x16x32_bf16 v[58:61], v[176:179], v[204:207], v[58:61]
	v_mfma_f32_16x16x32_bf16 v[54:57], v[168:171], v[212:215], v[54:57]
	v_mfma_f32_16x16x32_bf16 v[46:49], v[176:179], v[212:215], v[46:49]
	v_mfma_f32_16x16x32_bf16 v[30:33], v[168:171], v[220:223], v[30:33]
	v_mfma_f32_16x16x32_bf16 v[26:29], v[176:179], v[220:223], v[26:29]
	v_mfma_f32_16x16x32_bf16 v[22:25], v[168:171], v[240:243], v[22:25]
	v_mfma_f32_16x16x32_bf16 v[14:17], v[176:179], v[240:243], v[14:17]
	s_setprio 0
	s_setprio 1
	v_mfma_f32_16x16x32_bf16 v[50:53], v[180:183], v[200:203], v[50:53]
	v_mfma_f32_16x16x32_bf16 v[42:45], v[188:191], v[200:203], v[42:45]
	v_mfma_f32_16x16x32_bf16 v[38:41], v[180:183], v[208:211], v[38:41]
	v_mfma_f32_16x16x32_bf16 v[34:37], v[188:191], v[208:211], v[34:37]
	v_mfma_f32_16x16x32_bf16 v[18:21], v[180:183], v[216:219], v[18:21]
	v_mfma_f32_16x16x32_bf16 v[10:13], v[188:191], v[216:219], v[10:13]
	v_mfma_f32_16x16x32_bf16 v[6:9], v[180:183], v[236:239], v[6:9]
	v_mfma_f32_16x16x32_bf16 v[2:5], v[188:191], v[236:239], v[2:5]
	v_mfma_f32_16x16x32_bf16 v[50:53], v[184:187], v[204:207], v[50:53]
	v_mfma_f32_16x16x32_bf16 v[42:45], v[192:195], v[204:207], v[42:45]
	v_mfma_f32_16x16x32_bf16 v[38:41], v[184:187], v[212:215], v[38:41]
	v_mfma_f32_16x16x32_bf16 v[34:37], v[192:195], v[212:215], v[34:37]
	v_mfma_f32_16x16x32_bf16 v[18:21], v[184:187], v[220:223], v[18:21]
	v_mfma_f32_16x16x32_bf16 v[10:13], v[192:195], v[220:223], v[10:13]
	v_mfma_f32_16x16x32_bf16 v[6:9], v[184:187], v[240:243], v[6:9]
	v_mfma_f32_16x16x32_bf16 v[2:5], v[192:195], v[240:243], v[2:5]
	s_setprio 0
	s_barrier
	s_add_i32 s90, s90, 2
	s_add_u32 s48, s48, 0x100
	s_addc_u32 s49, s49, 0
	s_cmp_gt_u32 s90, 13
	s_cbranch_scc0 .LBB0_438
	s_add_u32 s48, s41, 0xffffff00
	s_addc_u32 s49, s89, -1
	s_and_b64 vcc, exec, s[36:37]
	s_movk_i32 s90, 0xfea0
	s_cbranch_vccnz .LBB0_441
	v_lshl_add_u32 v2, s38, 8, v160
	v_ashrrev_i32_e32 v3, 31, v2
	v_lshl_add_u64 v[2:3], v[2:3], 3, s[14:15]
	global_load_dwordx2 v[150:151], v[2:3], off nt
	global_load_dwordx2 v[146:147], v[2:3], off offset:128 nt
	global_load_dwordx2 v[140:141], v[2:3], off offset:256 nt
	global_load_dwordx2 v[138:139], v[2:3], off offset:384 nt
	global_load_dwordx2 v[136:137], v[2:3], off offset:1024 nt
	global_load_dwordx2 v[134:135], v[2:3], off offset:1152 nt
	global_load_dwordx2 v[132:133], v[2:3], off offset:1280 nt
	global_load_dwordx2 v[130:131], v[2:3], off offset:1408 nt
	v_mov_b32_e32 v2, 0
	s_mov_b32 s0, s40
	s_mov_b32 s34, s38
	s_mov_b64 s[16:17], s[46:47]
	s_mov_b32 s85, s88
	v_mov_b32_e32 v3, v2
	v_mov_b32_e32 v4, v2
	v_mov_b32_e32 v5, v2
	v_mov_b32_e32 v6, v2
	v_mov_b32_e32 v7, v2
	v_mov_b32_e32 v8, v2
	v_mov_b32_e32 v9, v2
	v_mov_b32_e32 v10, v2
	v_mov_b32_e32 v11, v2
	v_mov_b32_e32 v12, v2
	v_mov_b32_e32 v13, v2
	v_mov_b32_e32 v18, v2
	v_mov_b32_e32 v19, v2
	v_mov_b32_e32 v20, v2
	v_mov_b32_e32 v21, v2
	v_mov_b32_e32 v34, v2
	v_mov_b32_e32 v35, v2
	v_mov_b32_e32 v36, v2
	v_mov_b32_e32 v37, v2
	v_mov_b32_e32 v38, v2
	v_mov_b32_e32 v39, v2
	v_mov_b32_e32 v40, v2
	v_mov_b32_e32 v41, v2
	v_mov_b32_e32 v42, v2
	v_mov_b32_e32 v43, v2
	v_mov_b32_e32 v44, v2
	v_mov_b32_e32 v45, v2
	v_mov_b32_e32 v50, v2
	v_mov_b32_e32 v51, v2
	v_mov_b32_e32 v52, v2
	v_mov_b32_e32 v53, v2
	v_mov_b32_e32 v14, v2
	v_mov_b32_e32 v15, v2
	v_mov_b32_e32 v16, v2
	v_mov_b32_e32 v17, v2
	v_mov_b32_e32 v22, v2
	v_mov_b32_e32 v23, v2
	v_mov_b32_e32 v24, v2
	v_mov_b32_e32 v25, v2
	v_mov_b32_e32 v26, v2
	v_mov_b32_e32 v27, v2
	v_mov_b32_e32 v28, v2
	v_mov_b32_e32 v29, v2
	v_mov_b32_e32 v30, v2
	v_mov_b32_e32 v31, v2
	v_mov_b32_e32 v32, v2
	v_mov_b32_e32 v33, v2
	v_mov_b32_e32 v46, v2
	v_mov_b32_e32 v47, v2
	v_mov_b32_e32 v48, v2
	v_mov_b32_e32 v49, v2
	v_mov_b32_e32 v54, v2
	v_mov_b32_e32 v55, v2
	v_mov_b32_e32 v56, v2
	v_mov_b32_e32 v57, v2
	v_mov_b32_e32 v58, v2
	v_mov_b32_e32 v59, v2
	v_mov_b32_e32 v60, v2
	v_mov_b32_e32 v61, v2
	v_mov_b32_e32 v62, v2
	v_mov_b32_e32 v63, v2
	v_mov_b32_e32 v64, v2
	v_mov_b32_e32 v65, v2
	v_mov_b32_e32 v66, v2
	v_mov_b32_e32 v67, v2
	v_mov_b32_e32 v68, v2
	v_mov_b32_e32 v69, v2
	v_mov_b32_e32 v70, v2
	v_mov_b32_e32 v71, v2
	v_mov_b32_e32 v72, v2
	v_mov_b32_e32 v73, v2
	v_mov_b32_e32 v74, v2
	v_mov_b32_e32 v75, v2
	v_mov_b32_e32 v76, v2
	v_mov_b32_e32 v77, v2
	v_mov_b32_e32 v82, v2
	v_mov_b32_e32 v83, v2
	v_mov_b32_e32 v84, v2
	v_mov_b32_e32 v85, v2
	v_mov_b32_e32 v98, v2
	v_mov_b32_e32 v99, v2
	v_mov_b32_e32 v100, v2
	v_mov_b32_e32 v101, v2
	v_mov_b32_e32 v102, v2
	v_mov_b32_e32 v103, v2
	v_mov_b32_e32 v104, v2
	v_mov_b32_e32 v105, v2
	v_mov_b32_e32 v114, v2
	v_mov_b32_e32 v115, v2
	v_mov_b32_e32 v116, v2
	v_mov_b32_e32 v117, v2
	v_mov_b32_e32 v118, v2
	v_mov_b32_e32 v119, v2
	v_mov_b32_e32 v120, v2
	v_mov_b32_e32 v121, v2
	v_mov_b32_e32 v78, v2
	v_mov_b32_e32 v79, v2
	v_mov_b32_e32 v80, v2
	v_mov_b32_e32 v81, v2
	v_mov_b32_e32 v86, v2
	v_mov_b32_e32 v87, v2
	v_mov_b32_e32 v88, v2
	v_mov_b32_e32 v89, v2
	v_mov_b32_e32 v90, v2
	v_mov_b32_e32 v91, v2
	v_mov_b32_e32 v92, v2
	v_mov_b32_e32 v93, v2
	v_mov_b32_e32 v94, v2
	v_mov_b32_e32 v95, v2
	v_mov_b32_e32 v96, v2
	v_mov_b32_e32 v97, v2
	v_mov_b32_e32 v106, v2
	v_mov_b32_e32 v107, v2
	v_mov_b32_e32 v108, v2
	v_mov_b32_e32 v109, v2
	v_mov_b32_e32 v110, v2
	v_mov_b32_e32 v111, v2
	v_mov_b32_e32 v112, v2
	v_mov_b32_e32 v113, v2
	v_mov_b32_e32 v122, v2
	v_mov_b32_e32 v123, v2
	v_mov_b32_e32 v124, v2
	v_mov_b32_e32 v125, v2
	v_mov_b32_e32 v126, v2
	v_mov_b32_e32 v127, v2
	v_mov_b32_e32 v128, v2
	v_mov_b32_e32 v129, v2
	s_branch .LBB0_442

.LBB0_496:
	s_add_u32 s36, s48, s52
	s_addc_u32 s37, s49, s53
	v_or_b32_e32 v146, 0x10000, v145
	v_add_u32_e32 v150, 0x10400, v145
	v_add_u32_e32 v154, 0x10800, v145
	v_add_u32_e32 v158, 0x10c00, v145
	v_or_b32_e32 v162, 0x14000, v145
	v_add_u32_e32 v166, 0x14400, v145
	v_add_u32_e32 v170, 0x14800, v145
	v_add_u32_e32 v174, 0x14c00, v145
	s_add_u32 s36, s36, 0x100
	ds_read_b128 v[146:149], v146
	ds_read_b128 v[150:153], v150
	ds_read_b128 v[154:157], v154
	ds_read_b128 v[158:161], v158
	ds_read_b128 v[162:165], v162
	ds_read_b128 v[166:169], v166
	ds_read_b128 v[170:173], v170
	ds_read_b128 v[174:177], v174
	s_addc_u32 s37, s37, 0
	s_add_u32 s54, s92, s52
	s_addc_u32 s55, s93, s53
	s_cmpk_eq_i32 s52, 0x700
	s_cselect_b32 s57, s39, s37
	s_cselect_b32 s56, s94, s36
	s_cselect_b32 s55, s41, s55
	s_cselect_b32 s54, s95, s54
	v_lshl_add_u64 v[194:195], v[140:141], 0, s[52:53]
	s_add_i32 m0, s17, 0xc000
	ds_read_b128 v[178:181], v144
	ds_read_b128 v[182:185], v144 offset:1024
	ds_read_b128 v[186:189], v144 offset:2048
	ds_read_b128 v[190:193], v144 offset:3072
	ds_read_b128 v[200:203], v144 offset:4096
	ds_read_b128 v[204:207], v144 offset:5120
	ds_read_b128 v[208:211], v144 offset:6144
	ds_read_b128 v[212:215], v144 offset:7168
	global_load_lds_dwordx4 v[194:195], off
	v_lshl_add_u64 v[194:195], v[142:143], 0, s[52:53]
	s_add_i32 m0, s17, 0xe000
	s_nop 0
	global_load_lds_dwordx4 v[194:195], off
	s_waitcnt vmcnt(8)
	s_waitcnt lgkmcnt(0)
	s_barrier
	s_setprio 1
	s_waitcnt lgkmcnt(0)
	v_mfma_f32_16x16x32_bf16 v[126:129], v[146:149], v[178:181], v[126:129]
	v_mfma_f32_16x16x32_bf16 v[122:125], v[154:157], v[178:181], v[122:125]
	v_mfma_f32_16x16x32_bf16 v[110:113], v[146:149], v[186:189], v[110:113]
	v_mfma_f32_16x16x32_bf16 v[106:109], v[154:157], v[186:189], v[106:109]
	v_mfma_f32_16x16x32_bf16 v[94:97], v[146:149], v[200:203], v[94:97]
	v_mfma_f32_16x16x32_bf16 v[90:93], v[154:157], v[200:203], v[90:93]
	v_mfma_f32_16x16x32_bf16 v[78:81], v[146:149], v[208:211], v[78:81]
	v_mfma_f32_16x16x32_bf16 v[74:77], v[154:157], v[208:211], v[74:77]
	v_mfma_f32_16x16x32_bf16 v[126:129], v[150:153], v[182:185], v[126:129]
	v_mfma_f32_16x16x32_bf16 v[122:125], v[158:161], v[182:185], v[122:125]
	v_mfma_f32_16x16x32_bf16 v[110:113], v[150:153], v[190:193], v[110:113]
	v_mfma_f32_16x16x32_bf16 v[106:109], v[158:161], v[190:193], v[106:109]
	v_mfma_f32_16x16x32_bf16 v[94:97], v[150:153], v[204:207], v[94:97]
	v_mfma_f32_16x16x32_bf16 v[90:93], v[158:161], v[204:207], v[90:93]
	v_mfma_f32_16x16x32_bf16 v[78:81], v[150:153], v[212:215], v[78:81]
	v_mfma_f32_16x16x32_bf16 v[74:77], v[158:161], v[212:215], v[74:77]
	s_setprio 0
	s_setprio 1
	v_mfma_f32_16x16x32_bf16 v[118:121], v[162:165], v[178:181], v[118:121]
	v_mfma_f32_16x16x32_bf16 v[114:117], v[170:173], v[178:181], v[114:117]
	v_mfma_f32_16x16x32_bf16 v[102:105], v[162:165], v[186:189], v[102:105]
	v_mfma_f32_16x16x32_bf16 v[98:101], v[170:173], v[186:189], v[98:101]
	v_mfma_f32_16x16x32_bf16 v[86:89], v[162:165], v[200:203], v[86:89]
	v_mfma_f32_16x16x32_bf16 v[82:85], v[170:173], v[200:203], v[82:85]
	v_mfma_f32_16x16x32_bf16 v[70:73], v[162:165], v[208:211], v[70:73]
	v_mfma_f32_16x16x32_bf16 v[66:69], v[170:173], v[208:211], v[66:69]
	v_mfma_f32_16x16x32_bf16 v[118:121], v[166:169], v[182:185], v[118:121]
	v_mfma_f32_16x16x32_bf16 v[114:117], v[174:177], v[182:185], v[114:117]
	v_mfma_f32_16x16x32_bf16 v[102:105], v[166:169], v[190:193], v[102:105]
	v_mfma_f32_16x16x32_bf16 v[98:101], v[174:177], v[190:193], v[98:101]
	v_mfma_f32_16x16x32_bf16 v[86:89], v[166:169], v[204:207], v[86:89]
	v_mfma_f32_16x16x32_bf16 v[82:85], v[174:177], v[204:207], v[82:85]
	v_mfma_f32_16x16x32_bf16 v[70:73], v[166:169], v[212:215], v[70:73]
	v_mfma_f32_16x16x32_bf16 v[66:69], v[174:177], v[212:215], v[66:69]
	s_setprio 0
	s_barrier
	s_mov_b32 m0, s60
	s_add_u32 s36, s54, 0x40000
	ds_read_b128 v[178:181], v144 offset:16384
	ds_read_b128 v[182:185], v144 offset:17408
	ds_read_b128 v[186:189], v144 offset:18432
	ds_read_b128 v[190:193], v144 offset:19456
	ds_read_b128 v[200:203], v144 offset:20480
	ds_read_b128 v[204:207], v144 offset:21504
	ds_read_b128 v[208:211], v144 offset:22528
	ds_read_b128 v[212:215], v144 offset:23552
	global_load_lds_dwordx4 v0, s[54:55]
	v_lshl_add_u64 v[216:217], s[54:55], 0, v[130:131]
	s_mov_b32 m0, s61
	s_addc_u32 s37, s55, 0
	global_load_lds_dwordx4 v130, s[54:55]
	s_mov_b32 m0, s62
	s_nop 0
	global_load_lds_dwordx4 v0, s[36:37]
	s_mov_b32 m0, s63
	s_nop 0
	global_load_lds_dwordx4 v130, s[36:37]
	s_mov_b32 m0, s17
	s_nop 0
	global_load_lds_dwordx4 v134, s[56:57]
	s_mov_b32 m0, s66
	s_nop 0
	global_load_lds_dwordx4 v132, s[56:57]
	s_waitcnt vmcnt(8)
	s_waitcnt lgkmcnt(0)
	s_barrier
	s_setprio 1
	s_waitcnt lgkmcnt(0)
	v_mfma_f32_16x16x32_bf16 v[62:65], v[146:149], v[178:181], v[62:65]
	v_mfma_f32_16x16x32_bf16 v[58:61], v[154:157], v[178:181], v[58:61]
	v_mfma_f32_16x16x32_bf16 v[46:49], v[146:149], v[186:189], v[46:49]
	v_mfma_f32_16x16x32_bf16 v[42:45], v[154:157], v[186:189], v[42:45]
	v_mfma_f32_16x16x32_bf16 v[30:33], v[146:149], v[200:203], v[30:33]
	v_mfma_f32_16x16x32_bf16 v[26:29], v[154:157], v[200:203], v[26:29]
	v_mfma_f32_16x16x32_bf16 v[14:17], v[146:149], v[208:211], v[14:17]
	v_mfma_f32_16x16x32_bf16 v[10:13], v[154:157], v[208:211], v[10:13]
	v_mfma_f32_16x16x32_bf16 v[62:65], v[150:153], v[182:185], v[62:65]
	v_mfma_f32_16x16x32_bf16 v[58:61], v[158:161], v[182:185], v[58:61]
	v_mfma_f32_16x16x32_bf16 v[46:49], v[150:153], v[190:193], v[46:49]
	v_mfma_f32_16x16x32_bf16 v[42:45], v[158:161], v[190:193], v[42:45]
	v_mfma_f32_16x16x32_bf16 v[30:33], v[150:153], v[204:207], v[30:33]
	v_mfma_f32_16x16x32_bf16 v[26:29], v[158:161], v[204:207], v[26:29]
	v_mfma_f32_16x16x32_bf16 v[14:17], v[150:153], v[212:215], v[14:17]
	v_mfma_f32_16x16x32_bf16 v[10:13], v[158:161], v[212:215], v[10:13]
	s_setprio 0
	s_setprio 1
	v_mfma_f32_16x16x32_bf16 v[54:57], v[162:165], v[178:181], v[54:57]
	v_mfma_f32_16x16x32_bf16 v[50:53], v[170:173], v[178:181], v[50:53]
	v_mfma_f32_16x16x32_bf16 v[38:41], v[162:165], v[186:189], v[38:41]
	v_mfma_f32_16x16x32_bf16 v[34:37], v[170:173], v[186:189], v[34:37]
	v_mfma_f32_16x16x32_bf16 v[22:25], v[162:165], v[200:203], v[22:25]
	v_mfma_f32_16x16x32_bf16 v[18:21], v[170:173], v[200:203], v[18:21]
	v_mfma_f32_16x16x32_bf16 v[6:9], v[162:165], v[208:211], v[6:9]
	v_mfma_f32_16x16x32_bf16 v[2:5], v[170:173], v[208:211], v[2:5]
	v_mfma_f32_16x16x32_bf16 v[54:57], v[166:169], v[182:185], v[54:57]
	v_mfma_f32_16x16x32_bf16 v[50:53], v[174:177], v[182:185], v[50:53]
	v_mfma_f32_16x16x32_bf16 v[38:41], v[166:169], v[190:193], v[38:41]
	v_mfma_f32_16x16x32_bf16 v[34:37], v[174:177], v[190:193], v[34:37]
	v_mfma_f32_16x16x32_bf16 v[22:25], v[166:169], v[204:207], v[22:25]
	v_mfma_f32_16x16x32_bf16 v[18:21], v[174:177], v[204:207], v[18:21]
	v_mfma_f32_16x16x32_bf16 v[6:9], v[166:169], v[212:215], v[6:9]
	v_mfma_f32_16x16x32_bf16 v[2:5], v[174:177], v[212:215], v[2:5]
	s_setprio 0
	s_barrier
	v_or_b32_e32 v146, 0x18000, v145
	v_add_u32_e32 v150, 0x18400, v145
	v_add_u32_e32 v154, 0x18800, v145
	v_add_u32_e32 v158, 0x18c00, v145
	v_or_b32_e32 v162, 0x1c000, v145
	v_add_u32_e32 v166, 0x1c400, v145
	v_add_u32_e32 v170, 0x1c800, v145
	v_add_u32_e32 v174, 0x1cc00, v145
	ds_read_b128 v[146:149], v146
	ds_read_b128 v[150:153], v150
	ds_read_b128 v[154:157], v154
	ds_read_b128 v[158:161], v158
	ds_read_b128 v[162:165], v162
	ds_read_b128 v[166:169], v166
	ds_read_b128 v[170:173], v170
	ds_read_b128 v[174:177], v174
	s_add_u32 s36, s56, 0x40000
	s_addc_u32 s37, s57, 0
	s_mov_b32 m0, s67
	ds_read_b128 v[178:181], v144 offset:32768
	ds_read_b128 v[182:185], v144 offset:33792
	ds_read_b128 v[186:189], v144 offset:34816
	ds_read_b128 v[190:193], v144 offset:35840
	ds_read_b128 v[200:203], v144 offset:36864
	ds_read_b128 v[204:207], v144 offset:37888
	ds_read_b128 v[208:211], v144 offset:38912
	ds_read_b128 v[212:215], v144 offset:39936
	global_load_lds_dwordx4 v134, s[36:37]
	s_mov_b32 m0, s80
	s_nop 0
	global_load_lds_dwordx4 v132, s[36:37]
	s_waitcnt vmcnt(8)
	s_waitcnt lgkmcnt(0)
	s_barrier
	s_setprio 1
	s_waitcnt lgkmcnt(0)
	v_mfma_f32_16x16x32_bf16 v[126:129], v[146:149], v[178:181], v[126:129]
	v_mfma_f32_16x16x32_bf16 v[122:125], v[154:157], v[178:181], v[122:125]
	v_mfma_f32_16x16x32_bf16 v[110:113], v[146:149], v[186:189], v[110:113]
	v_mfma_f32_16x16x32_bf16 v[106:109], v[154:157], v[186:189], v[106:109]
	v_mfma_f32_16x16x32_bf16 v[94:97], v[146:149], v[200:203], v[94:97]
	v_mfma_f32_16x16x32_bf16 v[90:93], v[154:157], v[200:203], v[90:93]
	v_mfma_f32_16x16x32_bf16 v[78:81], v[146:149], v[208:211], v[78:81]
	v_mfma_f32_16x16x32_bf16 v[74:77], v[154:157], v[208:211], v[74:77]
	v_mfma_f32_16x16x32_bf16 v[126:129], v[150:153], v[182:185], v[126:129]
	v_mfma_f32_16x16x32_bf16 v[122:125], v[158:161], v[182:185], v[122:125]
	v_mfma_f32_16x16x32_bf16 v[110:113], v[150:153], v[190:193], v[110:113]
	v_mfma_f32_16x16x32_bf16 v[106:109], v[158:161], v[190:193], v[106:109]
	v_mfma_f32_16x16x32_bf16 v[94:97], v[150:153], v[204:207], v[94:97]
	v_mfma_f32_16x16x32_bf16 v[90:93], v[158:161], v[204:207], v[90:93]
	v_mfma_f32_16x16x32_bf16 v[78:81], v[150:153], v[212:215], v[78:81]
	v_mfma_f32_16x16x32_bf16 v[74:77], v[158:161], v[212:215], v[74:77]
	s_setprio 0
	s_setprio 1
	v_mfma_f32_16x16x32_bf16 v[118:121], v[162:165], v[178:181], v[118:121]
	v_mfma_f32_16x16x32_bf16 v[114:117], v[170:173], v[178:181], v[114:117]
	v_mfma_f32_16x16x32_bf16 v[102:105], v[162:165], v[186:189], v[102:105]
	v_mfma_f32_16x16x32_bf16 v[98:101], v[170:173], v[186:189], v[98:101]
	v_mfma_f32_16x16x32_bf16 v[86:89], v[162:165], v[200:203], v[86:89]
	v_mfma_f32_16x16x32_bf16 v[82:85], v[170:173], v[200:203], v[82:85]
	v_mfma_f32_16x16x32_bf16 v[70:73], v[162:165], v[208:211], v[70:73]
	v_mfma_f32_16x16x32_bf16 v[66:69], v[170:173], v[208:211], v[66:69]
	v_mfma_f32_16x16x32_bf16 v[118:121], v[166:169], v[182:185], v[118:121]
	v_mfma_f32_16x16x32_bf16 v[114:117], v[174:177], v[182:185], v[114:117]
	v_mfma_f32_16x16x32_bf16 v[102:105], v[166:169], v[190:193], v[102:105]
	v_mfma_f32_16x16x32_bf16 v[98:101], v[174:177], v[190:193], v[98:101]
	v_mfma_f32_16x16x32_bf16 v[86:89], v[166:169], v[204:207], v[86:89]
	v_mfma_f32_16x16x32_bf16 v[82:85], v[174:177], v[204:207], v[82:85]
	v_mfma_f32_16x16x32_bf16 v[70:73], v[166:169], v[212:215], v[70:73]
	v_mfma_f32_16x16x32_bf16 v[66:69], v[174:177], v[212:215], v[66:69]
	s_setprio 0
	s_barrier
	s_add_i32 m0, s82, 0xffffff80
	s_add_u32 s36, s54, 0x40080
	ds_read_b128 v[178:181], v144 offset:49152
	ds_read_b128 v[182:185], v144 offset:50176
	ds_read_b128 v[186:189], v144 offset:51200
	ds_read_b128 v[190:193], v144 offset:52224
	ds_read_b128 v[200:203], v144 offset:53248
	ds_read_b128 v[204:207], v144 offset:54272
	ds_read_b128 v[208:211], v144 offset:55296
	ds_read_b128 v[212:215], v144 offset:56320
	global_load_lds_dwordx4 v0, s[54:55] offset:128
	v_lshl_add_u64 v[194:195], v[216:217], 0, s[18:19]
	s_mov_b32 m0, s83
	s_addc_u32 s37, s55, 0
	global_load_lds_dwordx4 v[194:195], off
	s_mov_b32 m0, s88
	s_nop 0
	global_load_lds_dwordx4 v0, s[36:37]
	s_mov_b32 m0, s89
	s_nop 0
	global_load_lds_dwordx4 v130, s[36:37]
	s_add_i32 m0, s84, 0xffffff80
	s_nop 0
	global_load_lds_dwordx4 v134, s[56:57] offset:128
	s_add_i32 m0, s85, 0xffffff80
	s_nop 0
	global_load_lds_dwordx4 v132, s[56:57] offset:128
	s_waitcnt vmcnt(8)
	s_waitcnt lgkmcnt(0)
	s_barrier
	s_setprio 1
	s_waitcnt lgkmcnt(0)
	v_mfma_f32_16x16x32_bf16 v[62:65], v[146:149], v[178:181], v[62:65]
	v_mfma_f32_16x16x32_bf16 v[58:61], v[154:157], v[178:181], v[58:61]
	v_mfma_f32_16x16x32_bf16 v[46:49], v[146:149], v[186:189], v[46:49]
	v_mfma_f32_16x16x32_bf16 v[42:45], v[154:157], v[186:189], v[42:45]
	v_mfma_f32_16x16x32_bf16 v[30:33], v[146:149], v[200:203], v[30:33]
	v_mfma_f32_16x16x32_bf16 v[26:29], v[154:157], v[200:203], v[26:29]
	v_mfma_f32_16x16x32_bf16 v[14:17], v[146:149], v[208:211], v[14:17]
	v_mfma_f32_16x16x32_bf16 v[10:13], v[154:157], v[208:211], v[10:13]
	v_mfma_f32_16x16x32_bf16 v[62:65], v[150:153], v[182:185], v[62:65]
	v_mfma_f32_16x16x32_bf16 v[58:61], v[158:161], v[182:185], v[58:61]
	v_mfma_f32_16x16x32_bf16 v[46:49], v[150:153], v[190:193], v[46:49]
	v_mfma_f32_16x16x32_bf16 v[42:45], v[158:161], v[190:193], v[42:45]
	v_mfma_f32_16x16x32_bf16 v[30:33], v[150:153], v[204:207], v[30:33]
	v_mfma_f32_16x16x32_bf16 v[26:29], v[158:161], v[204:207], v[26:29]
	v_mfma_f32_16x16x32_bf16 v[14:17], v[150:153], v[212:215], v[14:17]
	v_mfma_f32_16x16x32_bf16 v[10:13], v[158:161], v[212:215], v[10:13]
	s_setprio 0
	s_setprio 1
	v_mfma_f32_16x16x32_bf16 v[54:57], v[162:165], v[178:181], v[54:57]
	v_mfma_f32_16x16x32_bf16 v[50:53], v[170:173], v[178:181], v[50:53]
	v_mfma_f32_16x16x32_bf16 v[38:41], v[162:165], v[186:189], v[38:41]
	v_mfma_f32_16x16x32_bf16 v[34:37], v[170:173], v[186:189], v[34:37]
	v_mfma_f32_16x16x32_bf16 v[22:25], v[162:165], v[200:203], v[22:25]
	v_mfma_f32_16x16x32_bf16 v[18:21], v[170:173], v[200:203], v[18:21]
	v_mfma_f32_16x16x32_bf16 v[6:9], v[162:165], v[208:211], v[6:9]
	v_mfma_f32_16x16x32_bf16 v[2:5], v[170:173], v[208:211], v[2:5]
	v_mfma_f32_16x16x32_bf16 v[54:57], v[166:169], v[182:185], v[54:57]
	v_mfma_f32_16x16x32_bf16 v[50:53], v[174:177], v[182:185], v[50:53]
	v_mfma_f32_16x16x32_bf16 v[38:41], v[166:169], v[190:193], v[38:41]
	v_mfma_f32_16x16x32_bf16 v[34:37], v[174:177], v[190:193], v[34:37]
	v_mfma_f32_16x16x32_bf16 v[22:25], v[166:169], v[204:207], v[22:25]
	v_mfma_f32_16x16x32_bf16 v[18:21], v[174:177], v[204:207], v[18:21]
	v_mfma_f32_16x16x32_bf16 v[6:9], v[166:169], v[212:215], v[6:9]
	v_mfma_f32_16x16x32_bf16 v[2:5], v[174:177], v[212:215], v[2:5]
	s_setprio 0
	s_barrier
	s_add_i32 vcc_lo, vcc_lo, 2
	s_add_u32 s52, s52, 0x100
	s_addc_u32 s53, s53, 0
	s_cmp_gt_u32 vcc_lo, 13
	s_cbranch_scc0 .LBB0_496
	s_and_b64 vcc, exec, s[14:15]
	s_cbranch_vccz .LBB0_499
	s_barrier

.LBB0_535:
	s_add_u32 s0, s42, s52
	s_addc_u32 s1, s43, s53
	v_or_b32_e32 v146, 0x10000, v145
	v_add_u32_e32 v150, 0x10400, v145
	v_add_u32_e32 v154, 0x10800, v145
	v_add_u32_e32 v158, 0x10c00, v145
	v_or_b32_e32 v162, 0x14000, v145
	v_add_u32_e32 v166, 0x14400, v145
	v_add_u32_e32 v170, 0x14800, v145
	v_add_u32_e32 v174, 0x14c00, v145
	s_add_u32 s0, s0, 0x100
	ds_read_b128 v[146:149], v146
	ds_read_b128 v[150:153], v150
	ds_read_b128 v[154:157], v154
	ds_read_b128 v[158:161], v158
	ds_read_b128 v[162:165], v162
	ds_read_b128 v[166:169], v166
	ds_read_b128 v[170:173], v170
	ds_read_b128 v[174:177], v174
	s_addc_u32 s1, s1, 0
	s_add_u32 s54, s29, s52
	s_addc_u32 s55, s93, s53
	s_cmpk_eq_i32 s52, 0x700
	s_cselect_b32 s57, s39, s1
	s_cselect_b32 s56, s94, s0
	s_cselect_b32 s55, s41, s55
	s_cselect_b32 s54, s95, s54
	v_lshl_add_u64 v[194:195], v[140:141], 0, s[52:53]
	s_add_i32 m0, s37, 0xc000
	ds_read_b128 v[178:181], v144
	ds_read_b128 v[182:185], v144 offset:1024
	ds_read_b128 v[186:189], v144 offset:2048
	ds_read_b128 v[190:193], v144 offset:3072
	ds_read_b128 v[200:203], v144 offset:4096
	ds_read_b128 v[204:207], v144 offset:5120
	ds_read_b128 v[208:211], v144 offset:6144
	ds_read_b128 v[212:215], v144 offset:7168
	global_load_lds_dwordx4 v[194:195], off
	v_lshl_add_u64 v[194:195], v[142:143], 0, s[52:53]
	s_add_i32 m0, s37, 0xe000
	s_nop 0
	global_load_lds_dwordx4 v[194:195], off
	s_waitcnt vmcnt(8)
	s_waitcnt lgkmcnt(0)
	s_barrier
	s_setprio 1
	s_waitcnt lgkmcnt(0)
	v_mfma_f32_16x16x32_bf16 v[126:129], v[146:149], v[178:181], v[126:129]
	v_mfma_f32_16x16x32_bf16 v[122:125], v[154:157], v[178:181], v[122:125]
	v_mfma_f32_16x16x32_bf16 v[110:113], v[146:149], v[186:189], v[110:113]
	v_mfma_f32_16x16x32_bf16 v[106:109], v[154:157], v[186:189], v[106:109]
	v_mfma_f32_16x16x32_bf16 v[94:97], v[146:149], v[200:203], v[94:97]
	v_mfma_f32_16x16x32_bf16 v[90:93], v[154:157], v[200:203], v[90:93]
	v_mfma_f32_16x16x32_bf16 v[78:81], v[146:149], v[208:211], v[78:81]
	v_mfma_f32_16x16x32_bf16 v[74:77], v[154:157], v[208:211], v[74:77]
	v_mfma_f32_16x16x32_bf16 v[126:129], v[150:153], v[182:185], v[126:129]
	v_mfma_f32_16x16x32_bf16 v[122:125], v[158:161], v[182:185], v[122:125]
	v_mfma_f32_16x16x32_bf16 v[110:113], v[150:153], v[190:193], v[110:113]
	v_mfma_f32_16x16x32_bf16 v[106:109], v[158:161], v[190:193], v[106:109]
	v_mfma_f32_16x16x32_bf16 v[94:97], v[150:153], v[204:207], v[94:97]
	v_mfma_f32_16x16x32_bf16 v[90:93], v[158:161], v[204:207], v[90:93]
	v_mfma_f32_16x16x32_bf16 v[78:81], v[150:153], v[212:215], v[78:81]
	v_mfma_f32_16x16x32_bf16 v[74:77], v[158:161], v[212:215], v[74:77]
	s_setprio 0
	s_setprio 1
	v_mfma_f32_16x16x32_bf16 v[118:121], v[162:165], v[178:181], v[118:121]
	v_mfma_f32_16x16x32_bf16 v[114:117], v[170:173], v[178:181], v[114:117]
	v_mfma_f32_16x16x32_bf16 v[102:105], v[162:165], v[186:189], v[102:105]
	v_mfma_f32_16x16x32_bf16 v[98:101], v[170:173], v[186:189], v[98:101]
	v_mfma_f32_16x16x32_bf16 v[86:89], v[162:165], v[200:203], v[86:89]
	v_mfma_f32_16x16x32_bf16 v[82:85], v[170:173], v[200:203], v[82:85]
	v_mfma_f32_16x16x32_bf16 v[70:73], v[162:165], v[208:211], v[70:73]
	v_mfma_f32_16x16x32_bf16 v[66:69], v[170:173], v[208:211], v[66:69]
	v_mfma_f32_16x16x32_bf16 v[118:121], v[166:169], v[182:185], v[118:121]
	v_mfma_f32_16x16x32_bf16 v[114:117], v[174:177], v[182:185], v[114:117]
	v_mfma_f32_16x16x32_bf16 v[102:105], v[166:169], v[190:193], v[102:105]
	v_mfma_f32_16x16x32_bf16 v[98:101], v[174:177], v[190:193], v[98:101]
	v_mfma_f32_16x16x32_bf16 v[86:89], v[166:169], v[204:207], v[86:89]
	v_mfma_f32_16x16x32_bf16 v[82:85], v[174:177], v[204:207], v[82:85]
	v_mfma_f32_16x16x32_bf16 v[70:73], v[166:169], v[212:215], v[70:73]
	v_mfma_f32_16x16x32_bf16 v[66:69], v[174:177], v[212:215], v[66:69]
	s_setprio 0
	s_barrier
	s_mov_b32 m0, s62
	s_add_u32 s0, s54, 0x40000
	ds_read_b128 v[178:181], v144 offset:16384
	ds_read_b128 v[182:185], v144 offset:17408
	ds_read_b128 v[186:189], v144 offset:18432
	ds_read_b128 v[190:193], v144 offset:19456
	ds_read_b128 v[200:203], v144 offset:20480
	ds_read_b128 v[204:207], v144 offset:21504
	ds_read_b128 v[208:211], v144 offset:22528
	ds_read_b128 v[212:215], v144 offset:23552
	global_load_lds_dwordx4 v0, s[54:55]
	v_lshl_add_u64 v[216:217], s[54:55], 0, v[130:131]
	s_mov_b32 m0, s63
	s_addc_u32 s1, s55, 0
	global_load_lds_dwordx4 v130, s[54:55]
	s_mov_b32 m0, s64
	s_nop 0
	global_load_lds_dwordx4 v0, s[0:1]
	s_mov_b32 m0, s65
	s_nop 0
	global_load_lds_dwordx4 v130, s[0:1]
	s_mov_b32 m0, s37
	s_nop 0
	global_load_lds_dwordx4 v134, s[56:57]
	s_mov_b32 m0, s66
	s_nop 0
	global_load_lds_dwordx4 v132, s[56:57]
	s_waitcnt vmcnt(8)
	s_waitcnt lgkmcnt(0)
	s_barrier
	s_setprio 1
	s_waitcnt lgkmcnt(0)
	v_mfma_f32_16x16x32_bf16 v[62:65], v[146:149], v[178:181], v[62:65]
	v_mfma_f32_16x16x32_bf16 v[58:61], v[154:157], v[178:181], v[58:61]
	v_mfma_f32_16x16x32_bf16 v[46:49], v[146:149], v[186:189], v[46:49]
	v_mfma_f32_16x16x32_bf16 v[42:45], v[154:157], v[186:189], v[42:45]
	v_mfma_f32_16x16x32_bf16 v[30:33], v[146:149], v[200:203], v[30:33]
	v_mfma_f32_16x16x32_bf16 v[26:29], v[154:157], v[200:203], v[26:29]
	v_mfma_f32_16x16x32_bf16 v[14:17], v[146:149], v[208:211], v[14:17]
	v_mfma_f32_16x16x32_bf16 v[10:13], v[154:157], v[208:211], v[10:13]
	v_mfma_f32_16x16x32_bf16 v[62:65], v[150:153], v[182:185], v[62:65]
	v_mfma_f32_16x16x32_bf16 v[58:61], v[158:161], v[182:185], v[58:61]
	v_mfma_f32_16x16x32_bf16 v[46:49], v[150:153], v[190:193], v[46:49]
	v_mfma_f32_16x16x32_bf16 v[42:45], v[158:161], v[190:193], v[42:45]
	v_mfma_f32_16x16x32_bf16 v[30:33], v[150:153], v[204:207], v[30:33]
	v_mfma_f32_16x16x32_bf16 v[26:29], v[158:161], v[204:207], v[26:29]
	v_mfma_f32_16x16x32_bf16 v[14:17], v[150:153], v[212:215], v[14:17]
	v_mfma_f32_16x16x32_bf16 v[10:13], v[158:161], v[212:215], v[10:13]
	s_setprio 0
	s_setprio 1
	v_mfma_f32_16x16x32_bf16 v[54:57], v[162:165], v[178:181], v[54:57]
	v_mfma_f32_16x16x32_bf16 v[50:53], v[170:173], v[178:181], v[50:53]
	v_mfma_f32_16x16x32_bf16 v[38:41], v[162:165], v[186:189], v[38:41]
	v_mfma_f32_16x16x32_bf16 v[34:37], v[170:173], v[186:189], v[34:37]
	v_mfma_f32_16x16x32_bf16 v[22:25], v[162:165], v[200:203], v[22:25]
	v_mfma_f32_16x16x32_bf16 v[18:21], v[170:173], v[200:203], v[18:21]
	v_mfma_f32_16x16x32_bf16 v[6:9], v[162:165], v[208:211], v[6:9]
	v_mfma_f32_16x16x32_bf16 v[2:5], v[170:173], v[208:211], v[2:5]
	v_mfma_f32_16x16x32_bf16 v[54:57], v[166:169], v[182:185], v[54:57]
	v_mfma_f32_16x16x32_bf16 v[50:53], v[174:177], v[182:185], v[50:53]
	v_mfma_f32_16x16x32_bf16 v[38:41], v[166:169], v[190:193], v[38:41]
	v_mfma_f32_16x16x32_bf16 v[34:37], v[174:177], v[190:193], v[34:37]
	v_mfma_f32_16x16x32_bf16 v[22:25], v[166:169], v[204:207], v[22:25]
	v_mfma_f32_16x16x32_bf16 v[18:21], v[174:177], v[204:207], v[18:21]
	v_mfma_f32_16x16x32_bf16 v[6:9], v[166:169], v[212:215], v[6:9]
	v_mfma_f32_16x16x32_bf16 v[2:5], v[174:177], v[212:215], v[2:5]
	s_setprio 0
	s_barrier
	v_or_b32_e32 v146, 0x18000, v145
	v_add_u32_e32 v150, 0x18400, v145
	v_add_u32_e32 v154, 0x18800, v145
	v_add_u32_e32 v158, 0x18c00, v145
	v_or_b32_e32 v162, 0x1c000, v145
	v_add_u32_e32 v166, 0x1c400, v145
	v_add_u32_e32 v170, 0x1c800, v145
	v_add_u32_e32 v174, 0x1cc00, v145
	ds_read_b128 v[146:149], v146
	ds_read_b128 v[150:153], v150
	ds_read_b128 v[154:157], v154
	ds_read_b128 v[158:161], v158
	ds_read_b128 v[162:165], v162
	ds_read_b128 v[166:169], v166
	ds_read_b128 v[170:173], v170
	ds_read_b128 v[174:177], v174
	s_add_u32 s0, s56, 0x40000
	s_addc_u32 s1, s57, 0
	s_mov_b32 m0, s67
	ds_read_b128 v[178:181], v144 offset:32768
	ds_read_b128 v[182:185], v144 offset:33792
	ds_read_b128 v[186:189], v144 offset:34816
	ds_read_b128 v[190:193], v144 offset:35840
	ds_read_b128 v[200:203], v144 offset:36864
	ds_read_b128 v[204:207], v144 offset:37888
	ds_read_b128 v[208:211], v144 offset:38912
	ds_read_b128 v[212:215], v144 offset:39936
	global_load_lds_dwordx4 v134, s[0:1]
	s_mov_b32 m0, s80
	s_nop 0
	global_load_lds_dwordx4 v132, s[0:1]
	s_waitcnt vmcnt(8)
	s_waitcnt lgkmcnt(0)
	s_barrier
	s_setprio 1
	s_waitcnt lgkmcnt(0)
	v_mfma_f32_16x16x32_bf16 v[126:129], v[146:149], v[178:181], v[126:129]
	v_mfma_f32_16x16x32_bf16 v[122:125], v[154:157], v[178:181], v[122:125]
	v_mfma_f32_16x16x32_bf16 v[110:113], v[146:149], v[186:189], v[110:113]
	v_mfma_f32_16x16x32_bf16 v[106:109], v[154:157], v[186:189], v[106:109]
	v_mfma_f32_16x16x32_bf16 v[94:97], v[146:149], v[200:203], v[94:97]
	v_mfma_f32_16x16x32_bf16 v[90:93], v[154:157], v[200:203], v[90:93]
	v_mfma_f32_16x16x32_bf16 v[78:81], v[146:149], v[208:211], v[78:81]
	v_mfma_f32_16x16x32_bf16 v[74:77], v[154:157], v[208:211], v[74:77]
	v_mfma_f32_16x16x32_bf16 v[126:129], v[150:153], v[182:185], v[126:129]
	v_mfma_f32_16x16x32_bf16 v[122:125], v[158:161], v[182:185], v[122:125]
	v_mfma_f32_16x16x32_bf16 v[110:113], v[150:153], v[190:193], v[110:113]
	v_mfma_f32_16x16x32_bf16 v[106:109], v[158:161], v[190:193], v[106:109]
	v_mfma_f32_16x16x32_bf16 v[94:97], v[150:153], v[204:207], v[94:97]
	v_mfma_f32_16x16x32_bf16 v[90:93], v[158:161], v[204:207], v[90:93]
	v_mfma_f32_16x16x32_bf16 v[78:81], v[150:153], v[212:215], v[78:81]
	v_mfma_f32_16x16x32_bf16 v[74:77], v[158:161], v[212:215], v[74:77]
	s_setprio 0
	s_setprio 1
	v_mfma_f32_16x16x32_bf16 v[118:121], v[162:165], v[178:181], v[118:121]
	v_mfma_f32_16x16x32_bf16 v[114:117], v[170:173], v[178:181], v[114:117]
	v_mfma_f32_16x16x32_bf16 v[102:105], v[162:165], v[186:189], v[102:105]
	v_mfma_f32_16x16x32_bf16 v[98:101], v[170:173], v[186:189], v[98:101]
	v_mfma_f32_16x16x32_bf16 v[86:89], v[162:165], v[200:203], v[86:89]
	v_mfma_f32_16x16x32_bf16 v[82:85], v[170:173], v[200:203], v[82:85]
	v_mfma_f32_16x16x32_bf16 v[70:73], v[162:165], v[208:211], v[70:73]
	v_mfma_f32_16x16x32_bf16 v[66:69], v[170:173], v[208:211], v[66:69]
	v_mfma_f32_16x16x32_bf16 v[118:121], v[166:169], v[182:185], v[118:121]
	v_mfma_f32_16x16x32_bf16 v[114:117], v[174:177], v[182:185], v[114:117]
	v_mfma_f32_16x16x32_bf16 v[102:105], v[166:169], v[190:193], v[102:105]
	v_mfma_f32_16x16x32_bf16 v[98:101], v[174:177], v[190:193], v[98:101]
	v_mfma_f32_16x16x32_bf16 v[86:89], v[166:169], v[204:207], v[86:89]
	v_mfma_f32_16x16x32_bf16 v[82:85], v[174:177], v[204:207], v[82:85]
	v_mfma_f32_16x16x32_bf16 v[70:73], v[166:169], v[212:215], v[70:73]
	v_mfma_f32_16x16x32_bf16 v[66:69], v[174:177], v[212:215], v[66:69]
	s_setprio 0
	s_barrier
	s_add_i32 m0, s82, 0xffffff80
	s_add_u32 s0, s54, 0x40080
	ds_read_b128 v[178:181], v144 offset:49152
	ds_read_b128 v[182:185], v144 offset:50176
	ds_read_b128 v[186:189], v144 offset:51200
	ds_read_b128 v[190:193], v144 offset:52224
	ds_read_b128 v[200:203], v144 offset:53248
	ds_read_b128 v[204:207], v144 offset:54272
	ds_read_b128 v[208:211], v144 offset:55296
	ds_read_b128 v[212:215], v144 offset:56320
	global_load_lds_dwordx4 v0, s[54:55] offset:128
	v_lshl_add_u64 v[194:195], v[216:217], 0, s[18:19]
	s_mov_b32 m0, s83
	s_addc_u32 s1, s55, 0
	global_load_lds_dwordx4 v[194:195], off
	s_mov_b32 m0, s88
	s_nop 0
	global_load_lds_dwordx4 v0, s[0:1]
	s_mov_b32 m0, s89
	s_nop 0
	global_load_lds_dwordx4 v130, s[0:1]
	s_add_i32 m0, s84, 0xffffff80
	s_nop 0
	global_load_lds_dwordx4 v134, s[56:57] offset:128
	s_add_i32 m0, s85, 0xffffff80
	s_nop 0
	global_load_lds_dwordx4 v132, s[56:57] offset:128
	s_waitcnt vmcnt(8)
	s_waitcnt lgkmcnt(0)
	s_barrier
	s_setprio 1
	s_waitcnt lgkmcnt(0)
	v_mfma_f32_16x16x32_bf16 v[62:65], v[146:149], v[178:181], v[62:65]
	v_mfma_f32_16x16x32_bf16 v[58:61], v[154:157], v[178:181], v[58:61]
	v_mfma_f32_16x16x32_bf16 v[46:49], v[146:149], v[186:189], v[46:49]
	v_mfma_f32_16x16x32_bf16 v[42:45], v[154:157], v[186:189], v[42:45]
	v_mfma_f32_16x16x32_bf16 v[30:33], v[146:149], v[200:203], v[30:33]
	v_mfma_f32_16x16x32_bf16 v[26:29], v[154:157], v[200:203], v[26:29]
	v_mfma_f32_16x16x32_bf16 v[14:17], v[146:149], v[208:211], v[14:17]
	v_mfma_f32_16x16x32_bf16 v[10:13], v[154:157], v[208:211], v[10:13]
	v_mfma_f32_16x16x32_bf16 v[62:65], v[150:153], v[182:185], v[62:65]
	v_mfma_f32_16x16x32_bf16 v[58:61], v[158:161], v[182:185], v[58:61]
	v_mfma_f32_16x16x32_bf16 v[46:49], v[150:153], v[190:193], v[46:49]
	v_mfma_f32_16x16x32_bf16 v[42:45], v[158:161], v[190:193], v[42:45]
	v_mfma_f32_16x16x32_bf16 v[30:33], v[150:153], v[204:207], v[30:33]
	v_mfma_f32_16x16x32_bf16 v[26:29], v[158:161], v[204:207], v[26:29]
	v_mfma_f32_16x16x32_bf16 v[14:17], v[150:153], v[212:215], v[14:17]
	v_mfma_f32_16x16x32_bf16 v[10:13], v[158:161], v[212:215], v[10:13]
	s_setprio 0
	s_setprio 1
	v_mfma_f32_16x16x32_bf16 v[54:57], v[162:165], v[178:181], v[54:57]
	v_mfma_f32_16x16x32_bf16 v[50:53], v[170:173], v[178:181], v[50:53]
	v_mfma_f32_16x16x32_bf16 v[38:41], v[162:165], v[186:189], v[38:41]
	v_mfma_f32_16x16x32_bf16 v[34:37], v[170:173], v[186:189], v[34:37]
	v_mfma_f32_16x16x32_bf16 v[22:25], v[162:165], v[200:203], v[22:25]
	v_mfma_f32_16x16x32_bf16 v[18:21], v[170:173], v[200:203], v[18:21]
	v_mfma_f32_16x16x32_bf16 v[6:9], v[162:165], v[208:211], v[6:9]
	v_mfma_f32_16x16x32_bf16 v[2:5], v[170:173], v[208:211], v[2:5]
	v_mfma_f32_16x16x32_bf16 v[54:57], v[166:169], v[182:185], v[54:57]
	v_mfma_f32_16x16x32_bf16 v[50:53], v[174:177], v[182:185], v[50:53]
	v_mfma_f32_16x16x32_bf16 v[38:41], v[166:169], v[190:193], v[38:41]
	v_mfma_f32_16x16x32_bf16 v[34:37], v[174:177], v[190:193], v[34:37]
	v_mfma_f32_16x16x32_bf16 v[22:25], v[166:169], v[204:207], v[22:25]
	v_mfma_f32_16x16x32_bf16 v[18:21], v[174:177], v[204:207], v[18:21]
	v_mfma_f32_16x16x32_bf16 v[6:9], v[166:169], v[212:215], v[6:9]
	v_mfma_f32_16x16x32_bf16 v[2:5], v[174:177], v[212:215], v[2:5]
	s_setprio 0
	s_barrier
	s_add_i32 vcc_lo, vcc_lo, 2
	s_add_u32 s52, s52, 0x100
	s_addc_u32 s53, s53, 0
	s_cmp_gt_u32 vcc_lo, 13
	s_cbranch_scc0 .LBB0_535
	s_and_b64 vcc, exec, s[16:17]
	s_cbranch_vccz .LBB0_538
	s_barrier

.LBB0_851:
	v_or_b32_e32 v0, 0x10000, v237
	v_add_u32_e32 v134, 0x10400, v237
	ds_read_b128 v[130:133], v0
	ds_read_b128 v[134:137], v134
	v_add_u32_e32 v0, 0x10800, v237
	v_add_u32_e32 v142, 0x10c00, v237
	ds_read_b128 v[138:141], v0
	ds_read_b128 v[142:145], v142
	v_or_b32_e32 v0, 0x14000, v237
	v_add_u32_e32 v150, 0x14400, v237
	ds_read_b128 v[146:149], v0
	ds_read_b128 v[150:153], v150
	v_add_u32_e32 v0, 0x14800, v237
	v_add_u32_e32 v158, 0x14c00, v237
	ds_read_b128 v[154:157], v0
	ds_read_b128 v[158:161], v158
	s_add_u32 s43, s54, 0xfffe0080
	s_addc_u32 s45, s55, -1
	s_cmp_eq_u32 s41, 4
	s_cselect_b32 s59, s49, s45
	s_cselect_b32 s58, s48, s43
	s_cselect_b32 s57, s51, s39
	s_cselect_b32 s56, s50, s29
	s_add_i32 m0, s61, 0xc000
	ds_read_b128 v[162:165], v236
	ds_read_b128 v[166:169], v236 offset:1024
	ds_read_b128 v[170:173], v236 offset:2048
	ds_read_b128 v[174:177], v236 offset:3072
	ds_read_b128 v[178:181], v236 offset:4096
	ds_read_b128 v[182:185], v236 offset:5120
	ds_read_b128 v[186:189], v236 offset:6144
	ds_read_b128 v[190:193], v236 offset:7168
	global_load_lds_dwordx4 v206, s[54:55]
	s_add_i32 m0, s61, 0xe000
	s_nop 0
	global_load_lds_dwordx4 v208, s[54:55]
	s_waitcnt vmcnt(8)
	s_waitcnt lgkmcnt(0)
	s_barrier
	s_setprio 1
	s_waitcnt lgkmcnt(0)
	v_mfma_f32_16x16x32_bf16 v[126:129], v[130:133], v[162:165], v[126:129]
	v_mfma_f32_16x16x32_bf16 v[122:125], v[138:141], v[162:165], v[122:125]
	v_mfma_f32_16x16x32_bf16 v[118:121], v[130:133], v[170:173], v[118:121]
	v_mfma_f32_16x16x32_bf16 v[114:117], v[138:141], v[170:173], v[114:117]
	v_mfma_f32_16x16x32_bf16 v[110:113], v[130:133], v[178:181], v[110:113]
	v_mfma_f32_16x16x32_bf16 v[106:109], v[138:141], v[178:181], v[106:109]
	v_mfma_f32_16x16x32_bf16 v[102:105], v[130:133], v[186:189], v[102:105]
	v_mfma_f32_16x16x32_bf16 v[98:101], v[138:141], v[186:189], v[98:101]
	v_mfma_f32_16x16x32_bf16 v[126:129], v[134:137], v[166:169], v[126:129]
	v_mfma_f32_16x16x32_bf16 v[122:125], v[142:145], v[166:169], v[122:125]
	v_mfma_f32_16x16x32_bf16 v[118:121], v[134:137], v[174:177], v[118:121]
	v_mfma_f32_16x16x32_bf16 v[114:117], v[142:145], v[174:177], v[114:117]
	v_mfma_f32_16x16x32_bf16 v[110:113], v[134:137], v[182:185], v[110:113]
	v_mfma_f32_16x16x32_bf16 v[106:109], v[142:145], v[182:185], v[106:109]
	v_mfma_f32_16x16x32_bf16 v[102:105], v[134:137], v[190:193], v[102:105]
	v_mfma_f32_16x16x32_bf16 v[98:101], v[142:145], v[190:193], v[98:101]
	s_setprio 0
	s_setprio 1
	v_mfma_f32_16x16x32_bf16 v[94:97], v[146:149], v[162:165], v[94:97]
	v_mfma_f32_16x16x32_bf16 v[90:93], v[154:157], v[162:165], v[90:93]
	v_mfma_f32_16x16x32_bf16 v[86:89], v[146:149], v[170:173], v[86:89]
	v_mfma_f32_16x16x32_bf16 v[82:85], v[154:157], v[170:173], v[82:85]
	v_mfma_f32_16x16x32_bf16 v[78:81], v[146:149], v[178:181], v[78:81]
	v_mfma_f32_16x16x32_bf16 v[74:77], v[154:157], v[178:181], v[74:77]
	v_mfma_f32_16x16x32_bf16 v[70:73], v[146:149], v[186:189], v[70:73]
	v_mfma_f32_16x16x32_bf16 v[66:69], v[154:157], v[186:189], v[66:69]
	v_mfma_f32_16x16x32_bf16 v[94:97], v[150:153], v[166:169], v[94:97]
	v_mfma_f32_16x16x32_bf16 v[90:93], v[158:161], v[166:169], v[90:93]
	v_mfma_f32_16x16x32_bf16 v[86:89], v[150:153], v[174:177], v[86:89]
	v_mfma_f32_16x16x32_bf16 v[82:85], v[158:161], v[174:177], v[82:85]
	v_mfma_f32_16x16x32_bf16 v[78:81], v[150:153], v[182:185], v[78:81]
	v_mfma_f32_16x16x32_bf16 v[74:77], v[158:161], v[182:185], v[74:77]
	v_mfma_f32_16x16x32_bf16 v[70:73], v[150:153], v[190:193], v[70:73]
	v_mfma_f32_16x16x32_bf16 v[66:69], v[158:161], v[190:193], v[66:69]
	s_setprio 0
	s_barrier
	s_mov_b32 m0, s62
	v_lshl_add_u64 v[210:211], s[56:57], 0, v[200:201]
	s_add_u32 vcc_lo, s56, 0x20000
	ds_read_b128 v[162:165], v236 offset:16384
	ds_read_b128 v[166:169], v236 offset:17408
	ds_read_b128 v[170:173], v236 offset:18432
	ds_read_b128 v[174:177], v236 offset:19456
	ds_read_b128 v[178:181], v236 offset:20480
	ds_read_b128 v[182:185], v236 offset:21504
	ds_read_b128 v[186:189], v236 offset:22528
	ds_read_b128 v[190:193], v236 offset:23552
	global_load_lds_dwordx4 v200, s[56:57]
	v_lshl_add_u64 v[212:213], s[56:57], 0, v[204:205]
	s_mov_b32 m0, s63
	s_addc_u32 vcc_hi, s57, 0
	global_load_lds_dwordx4 v204, s[56:57]
	v_lshl_add_u64 v[214:215], vcc, 0, v[200:201]
	s_mov_b32 m0, s64
	v_lshl_add_u64 v[216:217], s[58:59], 0, v[202:203]
	global_load_lds_dwordx4 v200, vcc
	v_lshl_add_u64 v[214:215], vcc, 0, v[204:205]
	s_mov_b32 m0, s65
	s_nop 0
	global_load_lds_dwordx4 v204, vcc
	v_lshl_add_u64 v[214:215], s[58:59], 0, v[194:195]
	s_mov_b32 m0, s61
	s_nop 0
	global_load_lds_dwordx4 v194, s[58:59]
	s_mov_b32 m0, s66
	s_nop 0
	global_load_lds_dwordx4 v202, s[58:59]
	s_waitcnt vmcnt(8)
	s_waitcnt lgkmcnt(0)
	s_barrier
	s_setprio 1
	s_waitcnt lgkmcnt(0)
	v_mfma_f32_16x16x32_bf16 v[62:65], v[130:133], v[162:165], v[62:65]
	v_mfma_f32_16x16x32_bf16 v[58:61], v[138:141], v[162:165], v[58:61]
	v_mfma_f32_16x16x32_bf16 v[54:57], v[130:133], v[170:173], v[54:57]
	v_mfma_f32_16x16x32_bf16 v[50:53], v[138:141], v[170:173], v[50:53]
	v_mfma_f32_16x16x32_bf16 v[46:49], v[130:133], v[178:181], v[46:49]
	v_mfma_f32_16x16x32_bf16 v[42:45], v[138:141], v[178:181], v[42:45]
	v_mfma_f32_16x16x32_bf16 v[38:41], v[130:133], v[186:189], v[38:41]
	v_mfma_f32_16x16x32_bf16 v[34:37], v[138:141], v[186:189], v[34:37]
	v_mfma_f32_16x16x32_bf16 v[62:65], v[134:137], v[166:169], v[62:65]
	v_mfma_f32_16x16x32_bf16 v[58:61], v[142:145], v[166:169], v[58:61]
	v_mfma_f32_16x16x32_bf16 v[54:57], v[134:137], v[174:177], v[54:57]
	v_mfma_f32_16x16x32_bf16 v[50:53], v[142:145], v[174:177], v[50:53]
	v_mfma_f32_16x16x32_bf16 v[46:49], v[134:137], v[182:185], v[46:49]
	v_mfma_f32_16x16x32_bf16 v[42:45], v[142:145], v[182:185], v[42:45]
	v_mfma_f32_16x16x32_bf16 v[38:41], v[134:137], v[190:193], v[38:41]
	v_mfma_f32_16x16x32_bf16 v[34:37], v[142:145], v[190:193], v[34:37]
	s_setprio 0
	s_setprio 1
	v_mfma_f32_16x16x32_bf16 v[30:33], v[146:149], v[162:165], v[30:33]
	v_mfma_f32_16x16x32_bf16 v[26:29], v[154:157], v[162:165], v[26:29]
	v_mfma_f32_16x16x32_bf16 v[22:25], v[146:149], v[170:173], v[22:25]
	v_mfma_f32_16x16x32_bf16 v[18:21], v[154:157], v[170:173], v[18:21]
	v_mfma_f32_16x16x32_bf16 v[14:17], v[146:149], v[178:181], v[14:17]
	v_mfma_f32_16x16x32_bf16 v[10:13], v[154:157], v[178:181], v[10:13]
	v_mfma_f32_16x16x32_bf16 v[6:9], v[146:149], v[186:189], v[6:9]
	v_mfma_f32_16x16x32_bf16 v[2:5], v[154:157], v[186:189], v[2:5]
	v_mfma_f32_16x16x32_bf16 v[30:33], v[150:153], v[166:169], v[30:33]
	v_mfma_f32_16x16x32_bf16 v[26:29], v[158:161], v[166:169], v[26:29]
	v_mfma_f32_16x16x32_bf16 v[22:25], v[150:153], v[174:177], v[22:25]
	v_mfma_f32_16x16x32_bf16 v[18:21], v[158:161], v[174:177], v[18:21]
	v_mfma_f32_16x16x32_bf16 v[14:17], v[150:153], v[182:185], v[14:17]
	v_mfma_f32_16x16x32_bf16 v[10:13], v[158:161], v[182:185], v[10:13]
	v_mfma_f32_16x16x32_bf16 v[6:9], v[150:153], v[190:193], v[6:9]
	v_mfma_f32_16x16x32_bf16 v[2:5], v[158:161], v[190:193], v[2:5]
	s_setprio 0
	s_barrier
	v_or_b32_e32 v0, 0x18000, v237
	v_add_u32_e32 v134, 0x18400, v237
	ds_read_b128 v[130:133], v0
	ds_read_b128 v[134:137], v134
	v_add_u32_e32 v0, 0x18800, v237
	v_add_u32_e32 v142, 0x18c00, v237
	ds_read_b128 v[138:141], v0
	ds_read_b128 v[142:145], v142
	v_or_b32_e32 v0, 0x1c000, v237
	v_add_u32_e32 v150, 0x1c400, v237
	ds_read_b128 v[146:149], v0
	ds_read_b128 v[150:153], v150
	v_add_u32_e32 v0, 0x1c800, v237
	v_add_u32_e32 v158, 0x1cc00, v237
	ds_read_b128 v[154:157], v0
	ds_read_b128 v[158:161], v158
	s_add_u32 s58, s58, 0x20000
	s_addc_u32 s59, s59, 0
	s_mov_b32 m0, s67
	v_lshl_add_u64 v[218:219], s[58:59], 0, v[194:195]
	ds_read_b128 v[162:165], v236 offset:32768
	ds_read_b128 v[166:169], v236 offset:33792
	ds_read_b128 v[170:173], v236 offset:34816
	ds_read_b128 v[174:177], v236 offset:35840
	ds_read_b128 v[178:181], v236 offset:36864
	ds_read_b128 v[182:185], v236 offset:37888
	ds_read_b128 v[186:189], v236 offset:38912
	ds_read_b128 v[190:193], v236 offset:39936
	global_load_lds_dwordx4 v194, s[58:59]
	v_lshl_add_u64 v[218:219], s[58:59], 0, v[202:203]
	s_mov_b32 m0, s82
	s_nop 0
	global_load_lds_dwordx4 v202, s[58:59]
	s_waitcnt vmcnt(8)
	s_waitcnt lgkmcnt(0)
	s_barrier
	s_setprio 1
	s_waitcnt lgkmcnt(0)
	v_mfma_f32_16x16x32_bf16 v[126:129], v[130:133], v[162:165], v[126:129]
	v_mfma_f32_16x16x32_bf16 v[122:125], v[138:141], v[162:165], v[122:125]
	v_mfma_f32_16x16x32_bf16 v[118:121], v[130:133], v[170:173], v[118:121]
	v_mfma_f32_16x16x32_bf16 v[114:117], v[138:141], v[170:173], v[114:117]
	v_mfma_f32_16x16x32_bf16 v[110:113], v[130:133], v[178:181], v[110:113]
	v_mfma_f32_16x16x32_bf16 v[106:109], v[138:141], v[178:181], v[106:109]
	v_mfma_f32_16x16x32_bf16 v[102:105], v[130:133], v[186:189], v[102:105]
	v_mfma_f32_16x16x32_bf16 v[98:101], v[138:141], v[186:189], v[98:101]
	v_mfma_f32_16x16x32_bf16 v[126:129], v[134:137], v[166:169], v[126:129]
	v_mfma_f32_16x16x32_bf16 v[122:125], v[142:145], v[166:169], v[122:125]
	v_mfma_f32_16x16x32_bf16 v[118:121], v[134:137], v[174:177], v[118:121]
	v_mfma_f32_16x16x32_bf16 v[114:117], v[142:145], v[174:177], v[114:117]
	v_mfma_f32_16x16x32_bf16 v[110:113], v[134:137], v[182:185], v[110:113]
	v_mfma_f32_16x16x32_bf16 v[106:109], v[142:145], v[182:185], v[106:109]
	v_mfma_f32_16x16x32_bf16 v[102:105], v[134:137], v[190:193], v[102:105]
	v_mfma_f32_16x16x32_bf16 v[98:101], v[142:145], v[190:193], v[98:101]
	s_setprio 0
	s_setprio 1
	v_mfma_f32_16x16x32_bf16 v[94:97], v[146:149], v[162:165], v[94:97]
	v_mfma_f32_16x16x32_bf16 v[90:93], v[154:157], v[162:165], v[90:93]
	v_mfma_f32_16x16x32_bf16 v[86:89], v[146:149], v[170:173], v[86:89]
	v_mfma_f32_16x16x32_bf16 v[82:85], v[154:157], v[170:173], v[82:85]
	v_mfma_f32_16x16x32_bf16 v[78:81], v[146:149], v[178:181], v[78:81]
	v_mfma_f32_16x16x32_bf16 v[74:77], v[154:157], v[178:181], v[74:77]
	v_mfma_f32_16x16x32_bf16 v[70:73], v[146:149], v[186:189], v[70:73]
	v_mfma_f32_16x16x32_bf16 v[66:69], v[154:157], v[186:189], v[66:69]
	v_mfma_f32_16x16x32_bf16 v[94:97], v[150:153], v[166:169], v[94:97]
	v_mfma_f32_16x16x32_bf16 v[90:93], v[158:161], v[166:169], v[90:93]
	v_mfma_f32_16x16x32_bf16 v[86:89], v[150:153], v[174:177], v[86:89]
	v_mfma_f32_16x16x32_bf16 v[82:85], v[158:161], v[174:177], v[82:85]
	v_mfma_f32_16x16x32_bf16 v[78:81], v[150:153], v[182:185], v[78:81]
	v_mfma_f32_16x16x32_bf16 v[74:77], v[158:161], v[182:185], v[74:77]
	v_mfma_f32_16x16x32_bf16 v[70:73], v[150:153], v[190:193], v[70:73]
	v_mfma_f32_16x16x32_bf16 v[66:69], v[158:161], v[190:193], v[66:69]
	s_setprio 0
	s_barrier
	s_mov_b32 m0, s88
	v_lshl_add_u64 v[210:211], v[210:211], 0, s[18:19]
	s_add_u32 s56, s56, 0x20080
	ds_read_b128 v[162:165], v236 offset:49152
	ds_read_b128 v[166:169], v236 offset:50176
	ds_read_b128 v[170:173], v236 offset:51200
	ds_read_b128 v[174:177], v236 offset:52224
	ds_read_b128 v[178:181], v236 offset:53248
	ds_read_b128 v[182:185], v236 offset:54272
	ds_read_b128 v[186:189], v236 offset:55296
	ds_read_b128 v[190:193], v236 offset:56320
	global_load_lds_dwordx4 v[210:211], off
	v_lshl_add_u64 v[210:211], v[212:213], 0, s[18:19]
	s_mov_b32 m0, s89
	s_addc_u32 s57, s57, 0
	global_load_lds_dwordx4 v[210:211], off
	s_mov_b32 m0, s92
	s_nop 0
	global_load_lds_dwordx4 v200, s[56:57]
	s_mov_b32 m0, s93
	s_nop 0
	global_load_lds_dwordx4 v204, s[56:57]
	v_lshl_add_u64 v[210:211], v[214:215], 0, s[18:19]
	s_mov_b32 m0, s90
	s_nop 0
	global_load_lds_dwordx4 v[210:211], off
	v_lshl_add_u64 v[210:211], v[216:217], 0, s[18:19]
	s_mov_b32 m0, s91
	s_nop 0
	global_load_lds_dwordx4 v[210:211], off
	s_waitcnt vmcnt(8)
	s_waitcnt lgkmcnt(0)
	s_barrier
	s_setprio 1
	s_waitcnt lgkmcnt(0)
	v_mfma_f32_16x16x32_bf16 v[62:65], v[130:133], v[162:165], v[62:65]
	v_mfma_f32_16x16x32_bf16 v[58:61], v[138:141], v[162:165], v[58:61]
	v_mfma_f32_16x16x32_bf16 v[54:57], v[130:133], v[170:173], v[54:57]
	v_mfma_f32_16x16x32_bf16 v[50:53], v[138:141], v[170:173], v[50:53]
	v_mfma_f32_16x16x32_bf16 v[46:49], v[130:133], v[178:181], v[46:49]
	v_mfma_f32_16x16x32_bf16 v[42:45], v[138:141], v[178:181], v[42:45]
	v_mfma_f32_16x16x32_bf16 v[38:41], v[130:133], v[186:189], v[38:41]
	v_mfma_f32_16x16x32_bf16 v[34:37], v[138:141], v[186:189], v[34:37]
	v_mfma_f32_16x16x32_bf16 v[62:65], v[134:137], v[166:169], v[62:65]
	v_mfma_f32_16x16x32_bf16 v[58:61], v[142:145], v[166:169], v[58:61]
	v_mfma_f32_16x16x32_bf16 v[54:57], v[134:137], v[174:177], v[54:57]
	v_mfma_f32_16x16x32_bf16 v[50:53], v[142:145], v[174:177], v[50:53]
	v_mfma_f32_16x16x32_bf16 v[46:49], v[134:137], v[182:185], v[46:49]
	v_mfma_f32_16x16x32_bf16 v[42:45], v[142:145], v[182:185], v[42:45]
	v_mfma_f32_16x16x32_bf16 v[38:41], v[134:137], v[190:193], v[38:41]
	v_mfma_f32_16x16x32_bf16 v[34:37], v[142:145], v[190:193], v[34:37]
	s_setprio 0
	s_setprio 1
	v_mfma_f32_16x16x32_bf16 v[30:33], v[146:149], v[162:165], v[30:33]
	v_mfma_f32_16x16x32_bf16 v[26:29], v[154:157], v[162:165], v[26:29]
	v_mfma_f32_16x16x32_bf16 v[22:25], v[146:149], v[170:173], v[22:25]
	v_mfma_f32_16x16x32_bf16 v[18:21], v[154:157], v[170:173], v[18:21]
	v_mfma_f32_16x16x32_bf16 v[14:17], v[146:149], v[178:181], v[14:17]
	v_mfma_f32_16x16x32_bf16 v[10:13], v[154:157], v[178:181], v[10:13]
	v_mfma_f32_16x16x32_bf16 v[6:9], v[146:149], v[186:189], v[6:9]
	v_mfma_f32_16x16x32_bf16 v[2:5], v[154:157], v[186:189], v[2:5]
	v_mfma_f32_16x16x32_bf16 v[30:33], v[150:153], v[166:169], v[30:33]
	v_mfma_f32_16x16x32_bf16 v[26:29], v[158:161], v[166:169], v[26:29]
	v_mfma_f32_16x16x32_bf16 v[22:25], v[150:153], v[174:177], v[22:25]
	v_mfma_f32_16x16x32_bf16 v[18:21], v[158:161], v[174:177], v[18:21]
	v_mfma_f32_16x16x32_bf16 v[14:17], v[150:153], v[182:185], v[14:17]
	v_mfma_f32_16x16x32_bf16 v[10:13], v[158:161], v[182:185], v[10:13]
	v_mfma_f32_16x16x32_bf16 v[6:9], v[150:153], v[190:193], v[6:9]
	v_mfma_f32_16x16x32_bf16 v[2:5], v[158:161], v[190:193], v[2:5]
	s_setprio 0
	s_barrier
	s_add_i32 s41, s41, 2
	s_add_u32 s54, s54, 0x100
	s_addc_u32 s55, s55, 0
	s_add_u32 s29, s29, 0x100
	s_addc_u32 s39, s39, 0
	s_cmp_gt_u32 s41, 5
	s_cbranch_scc0 .LBB0_851
	s_and_b64 vcc, exec, s[16:17]
	s_cbranch_vccz .LBB0_854
	s_barrier

.LBB0_1058:
	v_or_b32_e32 v0, 0x10000, v162
	v_add_u32_e32 v158, 0x10400, v162
	ds_read_b128 v[164:167], v0
	ds_read_b128 v[168:171], v158
	v_add_u32_e32 v0, 0x10800, v162
	v_add_u32_e32 v158, 0x10c00, v162
	ds_read_b128 v[172:175], v0
	ds_read_b128 v[176:179], v158
	v_or_b32_e32 v0, 0x14000, v162
	v_add_u32_e32 v158, 0x14400, v162
	ds_read_b128 v[180:183], v0
	ds_read_b128 v[184:187], v158
	v_add_u32_e32 v0, 0x14800, v162
	v_add_u32_e32 v158, 0x14c00, v162
	ds_read_b128 v[188:191], v0
	ds_read_b128 v[192:195], v158
	s_add_u32 s48, s36, 0xfffc0080
	s_addc_u32 s49, s37, -1
	s_cmp_eq_u32 s90, 12
	s_cselect_b32 s51, s29, s49
	s_cselect_b32 s50, s39, s48
	s_cselect_b32 s49, s41, s89
	s_cselect_b32 s48, s85, s88
	v_lshl_add_u64 v[158:159], s[36:37], 0, v[138:139]
	s_add_i32 m0, s35, 0xc000
	ds_read_b128 v[200:203], v161
	ds_read_b128 v[204:207], v161 offset:1024
	ds_read_b128 v[208:211], v161 offset:2048
	ds_read_b128 v[212:215], v161 offset:3072
	ds_read_b128 v[216:219], v161 offset:4096
	ds_read_b128 v[220:223], v161 offset:5120
	ds_read_b128 v[236:239], v161 offset:6144
	ds_read_b128 v[240:243], v161 offset:7168
	global_load_lds_dwordx4 v138, s[36:37]
	v_lshl_add_u64 v[158:159], s[36:37], 0, v[140:141]
	s_add_i32 m0, s35, 0xe000
	s_nop 0
	global_load_lds_dwordx4 v140, s[36:37]
	s_waitcnt vmcnt(8)
	s_waitcnt lgkmcnt(0)
	s_barrier
	s_setprio 1
	s_waitcnt lgkmcnt(0)
	v_mfma_f32_16x16x32_bf16 v[126:129], v[164:167], v[200:203], v[126:129]
	v_mfma_f32_16x16x32_bf16 v[122:125], v[172:175], v[200:203], v[122:125]
	v_mfma_f32_16x16x32_bf16 v[110:113], v[164:167], v[208:211], v[110:113]
	v_mfma_f32_16x16x32_bf16 v[106:109], v[172:175], v[208:211], v[106:109]
	v_mfma_f32_16x16x32_bf16 v[94:97], v[164:167], v[216:219], v[94:97]
	v_mfma_f32_16x16x32_bf16 v[90:93], v[172:175], v[216:219], v[90:93]
	v_mfma_f32_16x16x32_bf16 v[78:81], v[164:167], v[236:239], v[78:81]
	v_mfma_f32_16x16x32_bf16 v[74:77], v[172:175], v[236:239], v[74:77]
	v_mfma_f32_16x16x32_bf16 v[126:129], v[168:171], v[204:207], v[126:129]
	v_mfma_f32_16x16x32_bf16 v[122:125], v[176:179], v[204:207], v[122:125]
	v_mfma_f32_16x16x32_bf16 v[110:113], v[168:171], v[212:215], v[110:113]
	v_mfma_f32_16x16x32_bf16 v[106:109], v[176:179], v[212:215], v[106:109]
	v_mfma_f32_16x16x32_bf16 v[94:97], v[168:171], v[220:223], v[94:97]
	v_mfma_f32_16x16x32_bf16 v[90:93], v[176:179], v[220:223], v[90:93]
	v_mfma_f32_16x16x32_bf16 v[78:81], v[168:171], v[240:243], v[78:81]
	v_mfma_f32_16x16x32_bf16 v[74:77], v[176:179], v[240:243], v[74:77]
	s_setprio 0
	s_setprio 1
	v_mfma_f32_16x16x32_bf16 v[118:121], v[180:183], v[200:203], v[118:121]
	v_mfma_f32_16x16x32_bf16 v[114:117], v[188:191], v[200:203], v[114:117]
	v_mfma_f32_16x16x32_bf16 v[102:105], v[180:183], v[208:211], v[102:105]
	v_mfma_f32_16x16x32_bf16 v[98:101], v[188:191], v[208:211], v[98:101]
	v_mfma_f32_16x16x32_bf16 v[86:89], v[180:183], v[216:219], v[86:89]
	v_mfma_f32_16x16x32_bf16 v[82:85], v[188:191], v[216:219], v[82:85]
	v_mfma_f32_16x16x32_bf16 v[70:73], v[180:183], v[236:239], v[70:73]
	v_mfma_f32_16x16x32_bf16 v[66:69], v[188:191], v[236:239], v[66:69]
	v_mfma_f32_16x16x32_bf16 v[118:121], v[184:187], v[204:207], v[118:121]
	v_mfma_f32_16x16x32_bf16 v[114:117], v[192:195], v[204:207], v[114:117]
	v_mfma_f32_16x16x32_bf16 v[102:105], v[184:187], v[212:215], v[102:105]
	v_mfma_f32_16x16x32_bf16 v[98:101], v[192:195], v[212:215], v[98:101]
	v_mfma_f32_16x16x32_bf16 v[86:89], v[184:187], v[220:223], v[86:89]
	v_mfma_f32_16x16x32_bf16 v[82:85], v[192:195], v[220:223], v[82:85]
	v_mfma_f32_16x16x32_bf16 v[70:73], v[184:187], v[240:243], v[70:73]
	v_mfma_f32_16x16x32_bf16 v[66:69], v[192:195], v[240:243], v[66:69]
	s_setprio 0
	s_barrier
	s_mov_b32 m0, s53
	v_lshl_add_u64 v[158:159], s[48:49], 0, v[134:135]
	s_add_u32 s92, s48, 0x40000
	ds_read_b128 v[200:203], v161 offset:16384
	ds_read_b128 v[204:207], v161 offset:17408
	ds_read_b128 v[208:211], v161 offset:18432
	ds_read_b128 v[212:215], v161 offset:19456
	ds_read_b128 v[216:219], v161 offset:20480
	ds_read_b128 v[220:223], v161 offset:21504
	ds_read_b128 v[236:239], v161 offset:22528
	ds_read_b128 v[240:243], v161 offset:23552
	global_load_lds_dwordx4 v134, s[48:49]
	v_lshl_add_u64 v[226:227], s[48:49], 0, v[130:131]
	s_mov_b32 m0, s54
	s_addc_u32 s93, s49, 0
	global_load_lds_dwordx4 v130, s[48:49]
	s_mov_b32 m0, s55
	v_lshl_add_u64 v[246:247], s[50:51], 0, v[132:133]
	global_load_lds_dwordx4 v134, s[92:93]
	s_mov_b32 m0, s56
	s_nop 0
	global_load_lds_dwordx4 v130, s[92:93]
	v_lshl_add_u64 v[244:245], s[50:51], 0, v[136:137]
	s_mov_b32 m0, s35
	s_nop 0
	global_load_lds_dwordx4 v136, s[50:51]
	s_mov_b32 m0, s57
	s_nop 0
	global_load_lds_dwordx4 v132, s[50:51]
	s_waitcnt vmcnt(8)
	s_waitcnt lgkmcnt(0)
	s_barrier
	s_setprio 1
	s_waitcnt lgkmcnt(0)
	v_mfma_f32_16x16x32_bf16 v[62:65], v[164:167], v[200:203], v[62:65]
	v_mfma_f32_16x16x32_bf16 v[58:61], v[172:175], v[200:203], v[58:61]
	v_mfma_f32_16x16x32_bf16 v[46:49], v[164:167], v[208:211], v[46:49]
	v_mfma_f32_16x16x32_bf16 v[42:45], v[172:175], v[208:211], v[42:45]
	v_mfma_f32_16x16x32_bf16 v[30:33], v[164:167], v[216:219], v[30:33]
	v_mfma_f32_16x16x32_bf16 v[26:29], v[172:175], v[216:219], v[26:29]
	v_mfma_f32_16x16x32_bf16 v[14:17], v[164:167], v[236:239], v[14:17]
	v_mfma_f32_16x16x32_bf16 v[10:13], v[172:175], v[236:239], v[10:13]
	v_mfma_f32_16x16x32_bf16 v[62:65], v[168:171], v[204:207], v[62:65]
	v_mfma_f32_16x16x32_bf16 v[58:61], v[176:179], v[204:207], v[58:61]
	v_mfma_f32_16x16x32_bf16 v[46:49], v[168:171], v[212:215], v[46:49]
	v_mfma_f32_16x16x32_bf16 v[42:45], v[176:179], v[212:215], v[42:45]
	v_mfma_f32_16x16x32_bf16 v[30:33], v[168:171], v[220:223], v[30:33]
	v_mfma_f32_16x16x32_bf16 v[26:29], v[176:179], v[220:223], v[26:29]
	v_mfma_f32_16x16x32_bf16 v[14:17], v[168:171], v[240:243], v[14:17]
	v_mfma_f32_16x16x32_bf16 v[10:13], v[176:179], v[240:243], v[10:13]
	s_setprio 0
	s_setprio 1
	v_mfma_f32_16x16x32_bf16 v[54:57], v[180:183], v[200:203], v[54:57]
	v_mfma_f32_16x16x32_bf16 v[50:53], v[188:191], v[200:203], v[50:53]
	v_mfma_f32_16x16x32_bf16 v[38:41], v[180:183], v[208:211], v[38:41]
	v_mfma_f32_16x16x32_bf16 v[34:37], v[188:191], v[208:211], v[34:37]
	v_mfma_f32_16x16x32_bf16 v[22:25], v[180:183], v[216:219], v[22:25]
	v_mfma_f32_16x16x32_bf16 v[18:21], v[188:191], v[216:219], v[18:21]
	v_mfma_f32_16x16x32_bf16 v[6:9], v[180:183], v[236:239], v[6:9]
	v_mfma_f32_16x16x32_bf16 v[2:5], v[188:191], v[236:239], v[2:5]
	v_mfma_f32_16x16x32_bf16 v[54:57], v[184:187], v[204:207], v[54:57]
	v_mfma_f32_16x16x32_bf16 v[50:53], v[192:195], v[204:207], v[50:53]
	v_mfma_f32_16x16x32_bf16 v[38:41], v[184:187], v[212:215], v[38:41]
	v_mfma_f32_16x16x32_bf16 v[34:37], v[192:195], v[212:215], v[34:37]
	v_mfma_f32_16x16x32_bf16 v[22:25], v[184:187], v[220:223], v[22:25]
	v_mfma_f32_16x16x32_bf16 v[18:21], v[192:195], v[220:223], v[18:21]
	v_mfma_f32_16x16x32_bf16 v[6:9], v[184:187], v[240:243], v[6:9]
	v_mfma_f32_16x16x32_bf16 v[2:5], v[192:195], v[240:243], v[2:5]
	s_setprio 0
	s_barrier
	v_or_b32_e32 v0, 0x18000, v162
	v_add_u32_e32 v163, 0x18400, v162
	ds_read_b128 v[164:167], v0
	ds_read_b128 v[168:171], v163
	v_add_u32_e32 v0, 0x18800, v162
	v_add_u32_e32 v163, 0x18c00, v162
	ds_read_b128 v[172:175], v0
	ds_read_b128 v[176:179], v163
	v_or_b32_e32 v0, 0x1c000, v162
	v_add_u32_e32 v163, 0x1c400, v162
	ds_read_b128 v[180:183], v0
	ds_read_b128 v[184:187], v163
	v_add_u32_e32 v0, 0x1c800, v162
	v_add_u32_e32 v163, 0x1cc00, v162
	ds_read_b128 v[188:191], v0
	ds_read_b128 v[192:195], v163
	s_add_u32 s50, s50, 0x40000
	s_addc_u32 s51, s51, 0
	s_mov_b32 m0, s58
	ds_read_b128 v[200:203], v161 offset:32768
	ds_read_b128 v[204:207], v161 offset:33792
	ds_read_b128 v[208:211], v161 offset:34816
	ds_read_b128 v[212:215], v161 offset:35840
	ds_read_b128 v[216:219], v161 offset:36864
	ds_read_b128 v[220:223], v161 offset:37888
	ds_read_b128 v[236:239], v161 offset:38912
	ds_read_b128 v[240:243], v161 offset:39936
	global_load_lds_dwordx4 v136, s[50:51]
	s_mov_b32 m0, s59
	s_nop 0
	global_load_lds_dwordx4 v132, s[50:51]
	s_waitcnt vmcnt(8)
	s_waitcnt lgkmcnt(0)
	s_barrier
	s_setprio 1
	s_waitcnt lgkmcnt(0)
	v_mfma_f32_16x16x32_bf16 v[126:129], v[164:167], v[200:203], v[126:129]
	v_mfma_f32_16x16x32_bf16 v[122:125], v[172:175], v[200:203], v[122:125]
	v_mfma_f32_16x16x32_bf16 v[110:113], v[164:167], v[208:211], v[110:113]
	v_mfma_f32_16x16x32_bf16 v[106:109], v[172:175], v[208:211], v[106:109]
	v_mfma_f32_16x16x32_bf16 v[94:97], v[164:167], v[216:219], v[94:97]
	v_mfma_f32_16x16x32_bf16 v[90:93], v[172:175], v[216:219], v[90:93]
	v_mfma_f32_16x16x32_bf16 v[78:81], v[164:167], v[236:239], v[78:81]
	v_mfma_f32_16x16x32_bf16 v[74:77], v[172:175], v[236:239], v[74:77]
	v_mfma_f32_16x16x32_bf16 v[126:129], v[168:171], v[204:207], v[126:129]
	v_mfma_f32_16x16x32_bf16 v[122:125], v[176:179], v[204:207], v[122:125]
	v_mfma_f32_16x16x32_bf16 v[110:113], v[168:171], v[212:215], v[110:113]
	v_mfma_f32_16x16x32_bf16 v[106:109], v[176:179], v[212:215], v[106:109]
	v_mfma_f32_16x16x32_bf16 v[94:97], v[168:171], v[220:223], v[94:97]
	v_mfma_f32_16x16x32_bf16 v[90:93], v[176:179], v[220:223], v[90:93]
	v_mfma_f32_16x16x32_bf16 v[78:81], v[168:171], v[240:243], v[78:81]
	v_mfma_f32_16x16x32_bf16 v[74:77], v[176:179], v[240:243], v[74:77]
	s_setprio 0
	s_setprio 1
	v_mfma_f32_16x16x32_bf16 v[118:121], v[180:183], v[200:203], v[118:121]
	v_mfma_f32_16x16x32_bf16 v[114:117], v[188:191], v[200:203], v[114:117]
	v_mfma_f32_16x16x32_bf16 v[102:105], v[180:183], v[208:211], v[102:105]
	v_mfma_f32_16x16x32_bf16 v[98:101], v[188:191], v[208:211], v[98:101]
	v_mfma_f32_16x16x32_bf16 v[86:89], v[180:183], v[216:219], v[86:89]
	v_mfma_f32_16x16x32_bf16 v[82:85], v[188:191], v[216:219], v[82:85]
	v_mfma_f32_16x16x32_bf16 v[70:73], v[180:183], v[236:239], v[70:73]
	v_mfma_f32_16x16x32_bf16 v[66:69], v[188:191], v[236:239], v[66:69]
	v_mfma_f32_16x16x32_bf16 v[118:121], v[184:187], v[204:207], v[118:121]
	v_mfma_f32_16x16x32_bf16 v[114:117], v[192:195], v[204:207], v[114:117]
	v_mfma_f32_16x16x32_bf16 v[102:105], v[184:187], v[212:215], v[102:105]
	v_mfma_f32_16x16x32_bf16 v[98:101], v[192:195], v[212:215], v[98:101]
	v_mfma_f32_16x16x32_bf16 v[86:89], v[184:187], v[220:223], v[86:89]
	v_mfma_f32_16x16x32_bf16 v[82:85], v[192:195], v[220:223], v[82:85]
	v_mfma_f32_16x16x32_bf16 v[70:73], v[184:187], v[240:243], v[70:73]
	v_mfma_f32_16x16x32_bf16 v[66:69], v[192:195], v[240:243], v[66:69]
	s_setprio 0
	s_barrier
	s_mov_b32 m0, s62
	v_lshl_add_u64 v[158:159], v[158:159], 0, s[18:19]
	s_add_u32 s48, s48, 0x40080
	ds_read_b128 v[200:203], v161 offset:49152
	ds_read_b128 v[204:207], v161 offset:50176
	ds_read_b128 v[208:211], v161 offset:51200
	ds_read_b128 v[212:215], v161 offset:52224
	ds_read_b128 v[216:219], v161 offset:53248
	ds_read_b128 v[220:223], v161 offset:54272
	ds_read_b128 v[236:239], v161 offset:55296
	ds_read_b128 v[240:243], v161 offset:56320
	global_load_lds_dwordx4 v[158:159], off
	v_lshl_add_u64 v[158:159], v[226:227], 0, s[18:19]
	s_mov_b32 m0, s63
	s_addc_u32 s49, s49, 0
	global_load_lds_dwordx4 v[158:159], off
	v_lshl_add_u64 v[158:159], s[48:49], 0, v[134:135]
	s_mov_b32 m0, s66
	s_nop 0
	global_load_lds_dwordx4 v134, s[48:49]
	v_lshl_add_u64 v[158:159], s[48:49], 0, v[130:131]
	s_mov_b32 m0, s67
	s_nop 0
	global_load_lds_dwordx4 v130, s[48:49]
	v_lshl_add_u64 v[158:159], v[244:245], 0, s[18:19]
	s_mov_b32 m0, s64
	s_nop 0
	global_load_lds_dwordx4 v[158:159], off
	v_lshl_add_u64 v[158:159], v[246:247], 0, s[18:19]
	s_mov_b32 m0, s65
	s_nop 0
	global_load_lds_dwordx4 v[158:159], off
	s_waitcnt vmcnt(8)
	s_waitcnt lgkmcnt(0)
	s_barrier
	s_setprio 1
	s_waitcnt lgkmcnt(0)
	v_mfma_f32_16x16x32_bf16 v[62:65], v[164:167], v[200:203], v[62:65]
	v_mfma_f32_16x16x32_bf16 v[58:61], v[172:175], v[200:203], v[58:61]
	v_mfma_f32_16x16x32_bf16 v[46:49], v[164:167], v[208:211], v[46:49]
	v_mfma_f32_16x16x32_bf16 v[42:45], v[172:175], v[208:211], v[42:45]
	v_mfma_f32_16x16x32_bf16 v[30:33], v[164:167], v[216:219], v[30:33]
	v_mfma_f32_16x16x32_bf16 v[26:29], v[172:175], v[216:219], v[26:29]
	v_mfma_f32_16x16x32_bf16 v[14:17], v[164:167], v[236:239], v[14:17]
	v_mfma_f32_16x16x32_bf16 v[10:13], v[172:175], v[236:239], v[10:13]
	v_mfma_f32_16x16x32_bf16 v[62:65], v[168:171], v[204:207], v[62:65]
	v_mfma_f32_16x16x32_bf16 v[58:61], v[176:179], v[204:207], v[58:61]
	v_mfma_f32_16x16x32_bf16 v[46:49], v[168:171], v[212:215], v[46:49]
	v_mfma_f32_16x16x32_bf16 v[42:45], v[176:179], v[212:215], v[42:45]
	v_mfma_f32_16x16x32_bf16 v[30:33], v[168:171], v[220:223], v[30:33]
	v_mfma_f32_16x16x32_bf16 v[26:29], v[176:179], v[220:223], v[26:29]
	v_mfma_f32_16x16x32_bf16 v[14:17], v[168:171], v[240:243], v[14:17]
	v_mfma_f32_16x16x32_bf16 v[10:13], v[176:179], v[240:243], v[10:13]
	s_setprio 0
	s_setprio 1
	v_mfma_f32_16x16x32_bf16 v[54:57], v[180:183], v[200:203], v[54:57]
	v_mfma_f32_16x16x32_bf16 v[50:53], v[188:191], v[200:203], v[50:53]
	v_mfma_f32_16x16x32_bf16 v[38:41], v[180:183], v[208:211], v[38:41]
	v_mfma_f32_16x16x32_bf16 v[34:37], v[188:191], v[208:211], v[34:37]
	v_mfma_f32_16x16x32_bf16 v[22:25], v[180:183], v[216:219], v[22:25]
	v_mfma_f32_16x16x32_bf16 v[18:21], v[188:191], v[216:219], v[18:21]
	v_mfma_f32_16x16x32_bf16 v[6:9], v[180:183], v[236:239], v[6:9]
	v_mfma_f32_16x16x32_bf16 v[2:5], v[188:191], v[236:239], v[2:5]
	v_mfma_f32_16x16x32_bf16 v[54:57], v[184:187], v[204:207], v[54:57]
	v_mfma_f32_16x16x32_bf16 v[50:53], v[192:195], v[204:207], v[50:53]
	v_mfma_f32_16x16x32_bf16 v[38:41], v[184:187], v[212:215], v[38:41]
	v_mfma_f32_16x16x32_bf16 v[34:37], v[192:195], v[212:215], v[34:37]
	v_mfma_f32_16x16x32_bf16 v[22:25], v[184:187], v[220:223], v[22:25]
	v_mfma_f32_16x16x32_bf16 v[18:21], v[192:195], v[220:223], v[18:21]
	v_mfma_f32_16x16x32_bf16 v[6:9], v[184:187], v[240:243], v[6:9]
	v_mfma_f32_16x16x32_bf16 v[2:5], v[192:195], v[240:243], v[2:5]
	s_setprio 0
	s_barrier
	s_add_i32 s90, s90, 2
	s_add_u32 s36, s36, 0x100
	s_addc_u32 s37, s37, 0
	s_add_u32 s88, s88, 0x100
	s_addc_u32 s89, s89, 0
	s_cmp_gt_u32 s90, 13
	s_cbranch_scc0 .LBB0_1058
	s_and_b64 vcc, exec, s[16:17]
	s_cbranch_vccz .LBB0_1061
	s_barrier

.LBB0_1195:
	s_add_u32 s58, s44, s52
	s_addc_u32 s59, s45, s53
	s_add_u32 s56, s58, 0x100
	s_addc_u32 s57, s59, 0
	s_and_b64 s[54:55], s[50:51], exec
	s_cselect_b32 s55, s17, s57
	s_cselect_b32 s54, s29, s56
	s_add_u32 s52, s42, s52
	s_addc_u32 s53, s43, s53
	v_or_b32_e32 v0, 0x10000, v141
	s_add_u32 s52, s52, 0x100
	ds_read_b128 v[142:145], v0
	v_add_u32_e32 v0, 0x10400, v141
	s_addc_u32 s53, s53, 0
	ds_read_b128 v[146:149], v0
	v_add_u32_e32 v0, 0x10800, v141
	s_and_b64 s[50:51], s[50:51], exec
	ds_read_b128 v[150:153], v0
	v_add_u32_e32 v0, 0x10c00, v141
	s_cselect_b32 s57, s39, s53
	s_cselect_b32 s56, s38, s52
	s_add_u32 s60, s58, 0x80080
	ds_read_b128 v[154:157], v0
	v_or_b32_e32 v0, 0x14000, v141
	s_addc_u32 s61, s59, 0
	s_add_i32 m0, s63, 0xc000
	s_add_i32 vcc_lo, s63, 0xe000
	ds_read_b128 v[158:161], v0
	v_add_u32_e32 v0, 0x14400, v141
	s_add_u32 s58, s56, 0x40000
	ds_read_b128 v[162:165], v0
	v_add_u32_e32 v0, 0x14800, v141
	s_addc_u32 s59, s57, 0
	ds_read_b128 v[166:169], v0
	v_add_u32_e32 v0, 0x14c00, v141
	s_add_u32 s52, s54, 0x80000
	ds_read_b128 v[170:173], v0
	s_addc_u32 s53, s55, 0
	s_add_u32 s50, s56, 0x40080
	s_addc_u32 s51, s57, 0
	v_lshl_add_u64 v[138:139], s[60:61], 0, v[136:137]
	ds_read_b128 v[174:177], v140
	ds_read_b128 v[178:181], v140 offset:1024
	ds_read_b128 v[182:185], v140 offset:2048
	ds_read_b128 v[186:189], v140 offset:3072
	ds_read_b128 v[190:193], v140 offset:4096
	ds_read_b128 v[200:203], v140 offset:5120
	ds_read_b128 v[204:207], v140 offset:6144
	ds_read_b128 v[208:211], v140 offset:7168
	global_load_lds_dwordx4 v136, s[60:61]
	v_lshl_add_u64 v[138:139], s[60:61], 0, v[132:133]
	s_mov_b32 m0, vcc_lo
	s_nop 0
	global_load_lds_dwordx4 v132, s[60:61]
	s_waitcnt vmcnt(8)
	s_waitcnt lgkmcnt(0)
	s_barrier
	s_setprio 1
	s_waitcnt lgkmcnt(0)
	v_mfma_f32_16x16x32_bf16 v[126:129], v[142:145], v[174:177], v[126:129]
	v_mfma_f32_16x16x32_bf16 v[122:125], v[150:153], v[174:177], v[122:125]
	v_mfma_f32_16x16x32_bf16 v[118:121], v[142:145], v[182:185], v[118:121]
	v_mfma_f32_16x16x32_bf16 v[110:113], v[150:153], v[182:185], v[110:113]
	v_mfma_f32_16x16x32_bf16 v[102:105], v[142:145], v[190:193], v[102:105]
	v_mfma_f32_16x16x32_bf16 v[94:97], v[150:153], v[190:193], v[94:97]
	v_mfma_f32_16x16x32_bf16 v[86:89], v[142:145], v[204:207], v[86:89]
	v_mfma_f32_16x16x32_bf16 v[78:81], v[150:153], v[204:207], v[78:81]
	v_mfma_f32_16x16x32_bf16 v[126:129], v[146:149], v[178:181], v[126:129]
	v_mfma_f32_16x16x32_bf16 v[122:125], v[154:157], v[178:181], v[122:125]
	v_mfma_f32_16x16x32_bf16 v[118:121], v[146:149], v[186:189], v[118:121]
	v_mfma_f32_16x16x32_bf16 v[110:113], v[154:157], v[186:189], v[110:113]
	v_mfma_f32_16x16x32_bf16 v[102:105], v[146:149], v[200:203], v[102:105]
	v_mfma_f32_16x16x32_bf16 v[94:97], v[154:157], v[200:203], v[94:97]
	v_mfma_f32_16x16x32_bf16 v[86:89], v[146:149], v[208:211], v[86:89]
	v_mfma_f32_16x16x32_bf16 v[78:81], v[154:157], v[208:211], v[78:81]
	s_setprio 0
	s_setprio 1
	v_mfma_f32_16x16x32_bf16 v[114:117], v[158:161], v[174:177], v[114:117]
	v_mfma_f32_16x16x32_bf16 v[106:109], v[166:169], v[174:177], v[106:109]
	v_mfma_f32_16x16x32_bf16 v[98:101], v[158:161], v[182:185], v[98:101]
	v_mfma_f32_16x16x32_bf16 v[90:93], v[166:169], v[182:185], v[90:93]
	v_mfma_f32_16x16x32_bf16 v[82:85], v[158:161], v[190:193], v[82:85]
	v_mfma_f32_16x16x32_bf16 v[74:77], v[166:169], v[190:193], v[74:77]
	v_mfma_f32_16x16x32_bf16 v[70:73], v[158:161], v[204:207], v[70:73]
	v_mfma_f32_16x16x32_bf16 v[66:69], v[166:169], v[204:207], v[66:69]
	v_mfma_f32_16x16x32_bf16 v[114:117], v[162:165], v[178:181], v[114:117]
	v_mfma_f32_16x16x32_bf16 v[106:109], v[170:173], v[178:181], v[106:109]
	v_mfma_f32_16x16x32_bf16 v[98:101], v[162:165], v[186:189], v[98:101]
	v_mfma_f32_16x16x32_bf16 v[90:93], v[170:173], v[186:189], v[90:93]
	v_mfma_f32_16x16x32_bf16 v[82:85], v[162:165], v[200:203], v[82:85]
	v_mfma_f32_16x16x32_bf16 v[74:77], v[170:173], v[200:203], v[74:77]
	v_mfma_f32_16x16x32_bf16 v[70:73], v[162:165], v[208:211], v[70:73]
	v_mfma_f32_16x16x32_bf16 v[66:69], v[170:173], v[208:211], v[66:69]
	s_setprio 0
	s_barrier
	s_mov_b32 m0, s64
	v_lshl_add_u64 v[138:139], s[56:57], 0, v[134:135]
	ds_read_b128 v[174:177], v140 offset:16384
	ds_read_b128 v[178:181], v140 offset:17408
	ds_read_b128 v[182:185], v140 offset:18432
	ds_read_b128 v[186:189], v140 offset:19456
	ds_read_b128 v[190:193], v140 offset:20480
	ds_read_b128 v[200:203], v140 offset:21504
	ds_read_b128 v[204:207], v140 offset:22528
	ds_read_b128 v[208:211], v140 offset:23552
	global_load_lds_dwordx4 v134, s[56:57]
	v_lshl_add_u64 v[194:195], s[56:57], 0, v[130:131]
	s_mov_b32 m0, s65
	s_nop 0
	global_load_lds_dwordx4 v130, s[56:57]
	s_mov_b32 m0, s66
	v_lshl_add_u64 v[214:215], s[54:55], 0, v[132:133]
	global_load_lds_dwordx4 v134, s[58:59]
	s_mov_b32 m0, s67
	s_nop 0
	global_load_lds_dwordx4 v130, s[58:59]
	v_lshl_add_u64 v[212:213], s[54:55], 0, v[136:137]
	s_mov_b32 m0, s63
	s_nop 0
	global_load_lds_dwordx4 v136, s[54:55]
	s_mov_b32 m0, s80
	s_nop 0
	global_load_lds_dwordx4 v132, s[54:55]
	s_waitcnt vmcnt(8)
	s_waitcnt lgkmcnt(0)
	s_barrier
	s_setprio 1
	s_waitcnt lgkmcnt(0)
	v_mfma_f32_16x16x32_bf16 v[62:65], v[142:145], v[174:177], v[62:65]
	v_mfma_f32_16x16x32_bf16 v[58:61], v[150:153], v[174:177], v[58:61]
	v_mfma_f32_16x16x32_bf16 v[54:57], v[142:145], v[182:185], v[54:57]
	v_mfma_f32_16x16x32_bf16 v[46:49], v[150:153], v[182:185], v[46:49]
	v_mfma_f32_16x16x32_bf16 v[38:41], v[142:145], v[190:193], v[38:41]
	v_mfma_f32_16x16x32_bf16 v[30:33], v[150:153], v[190:193], v[30:33]
	v_mfma_f32_16x16x32_bf16 v[22:25], v[142:145], v[204:207], v[22:25]
	v_mfma_f32_16x16x32_bf16 v[14:17], v[150:153], v[204:207], v[14:17]
	v_mfma_f32_16x16x32_bf16 v[62:65], v[146:149], v[178:181], v[62:65]
	v_mfma_f32_16x16x32_bf16 v[58:61], v[154:157], v[178:181], v[58:61]
	v_mfma_f32_16x16x32_bf16 v[54:57], v[146:149], v[186:189], v[54:57]
	v_mfma_f32_16x16x32_bf16 v[46:49], v[154:157], v[186:189], v[46:49]
	v_mfma_f32_16x16x32_bf16 v[38:41], v[146:149], v[200:203], v[38:41]
	v_mfma_f32_16x16x32_bf16 v[30:33], v[154:157], v[200:203], v[30:33]
	v_mfma_f32_16x16x32_bf16 v[22:25], v[146:149], v[208:211], v[22:25]
	v_mfma_f32_16x16x32_bf16 v[14:17], v[154:157], v[208:211], v[14:17]
	s_setprio 0
	s_setprio 1
	v_mfma_f32_16x16x32_bf16 v[50:53], v[158:161], v[174:177], v[50:53]
	v_mfma_f32_16x16x32_bf16 v[42:45], v[166:169], v[174:177], v[42:45]
	v_mfma_f32_16x16x32_bf16 v[34:37], v[158:161], v[182:185], v[34:37]
	v_mfma_f32_16x16x32_bf16 v[26:29], v[166:169], v[182:185], v[26:29]
	v_mfma_f32_16x16x32_bf16 v[18:21], v[158:161], v[190:193], v[18:21]
	v_mfma_f32_16x16x32_bf16 v[10:13], v[166:169], v[190:193], v[10:13]
	v_mfma_f32_16x16x32_bf16 v[6:9], v[158:161], v[204:207], v[6:9]
	v_mfma_f32_16x16x32_bf16 v[2:5], v[166:169], v[204:207], v[2:5]
	v_mfma_f32_16x16x32_bf16 v[50:53], v[162:165], v[178:181], v[50:53]
	v_mfma_f32_16x16x32_bf16 v[42:45], v[170:173], v[178:181], v[42:45]
	v_mfma_f32_16x16x32_bf16 v[34:37], v[162:165], v[186:189], v[34:37]
	v_mfma_f32_16x16x32_bf16 v[26:29], v[170:173], v[186:189], v[26:29]
	v_mfma_f32_16x16x32_bf16 v[18:21], v[162:165], v[200:203], v[18:21]
	v_mfma_f32_16x16x32_bf16 v[10:13], v[170:173], v[200:203], v[10:13]
	v_mfma_f32_16x16x32_bf16 v[6:9], v[162:165], v[208:211], v[6:9]
	v_mfma_f32_16x16x32_bf16 v[2:5], v[170:173], v[208:211], v[2:5]
	s_setprio 0
	s_barrier
	v_or_b32_e32 v0, 0x18000, v141
	v_add_u32_e32 v146, 0x18400, v141
	ds_read_b128 v[142:145], v0
	ds_read_b128 v[146:149], v146
	v_add_u32_e32 v0, 0x18800, v141
	v_add_u32_e32 v154, 0x18c00, v141
	ds_read_b128 v[150:153], v0
	ds_read_b128 v[154:157], v154
	v_or_b32_e32 v0, 0x1c000, v141
	v_add_u32_e32 v162, 0x1c400, v141
	ds_read_b128 v[158:161], v0
	ds_read_b128 v[162:165], v162
	v_add_u32_e32 v0, 0x1c800, v141
	v_add_u32_e32 v170, 0x1cc00, v141
	ds_read_b128 v[166:169], v0
	ds_read_b128 v[170:173], v170
	s_mov_b32 m0, s82
	ds_read_b128 v[174:177], v140 offset:32768
	ds_read_b128 v[178:181], v140 offset:33792
	ds_read_b128 v[182:185], v140 offset:34816
	ds_read_b128 v[186:189], v140 offset:35840
	ds_read_b128 v[190:193], v140 offset:36864
	ds_read_b128 v[200:203], v140 offset:37888
	ds_read_b128 v[204:207], v140 offset:38912
	ds_read_b128 v[208:211], v140 offset:39936
	global_load_lds_dwordx4 v136, s[52:53]
	s_mov_b32 m0, s83
	s_nop 0
	global_load_lds_dwordx4 v132, s[52:53]
	s_waitcnt vmcnt(8)
	s_waitcnt lgkmcnt(0)
	s_barrier
	s_setprio 1
	s_waitcnt lgkmcnt(0)
	v_mfma_f32_16x16x32_bf16 v[126:129], v[142:145], v[174:177], v[126:129]
	v_mfma_f32_16x16x32_bf16 v[122:125], v[150:153], v[174:177], v[122:125]
	v_mfma_f32_16x16x32_bf16 v[118:121], v[142:145], v[182:185], v[118:121]
	v_mfma_f32_16x16x32_bf16 v[110:113], v[150:153], v[182:185], v[110:113]
	v_mfma_f32_16x16x32_bf16 v[102:105], v[142:145], v[190:193], v[102:105]
	v_mfma_f32_16x16x32_bf16 v[94:97], v[150:153], v[190:193], v[94:97]
	v_mfma_f32_16x16x32_bf16 v[86:89], v[142:145], v[204:207], v[86:89]
	v_mfma_f32_16x16x32_bf16 v[78:81], v[150:153], v[204:207], v[78:81]
	v_mfma_f32_16x16x32_bf16 v[126:129], v[146:149], v[178:181], v[126:129]
	v_mfma_f32_16x16x32_bf16 v[122:125], v[154:157], v[178:181], v[122:125]
	v_mfma_f32_16x16x32_bf16 v[118:121], v[146:149], v[186:189], v[118:121]
	v_mfma_f32_16x16x32_bf16 v[110:113], v[154:157], v[186:189], v[110:113]
	v_mfma_f32_16x16x32_bf16 v[102:105], v[146:149], v[200:203], v[102:105]
	v_mfma_f32_16x16x32_bf16 v[94:97], v[154:157], v[200:203], v[94:97]
	v_mfma_f32_16x16x32_bf16 v[86:89], v[146:149], v[208:211], v[86:89]
	v_mfma_f32_16x16x32_bf16 v[78:81], v[154:157], v[208:211], v[78:81]
	s_setprio 0
	s_setprio 1
	v_mfma_f32_16x16x32_bf16 v[114:117], v[158:161], v[174:177], v[114:117]
	v_mfma_f32_16x16x32_bf16 v[106:109], v[166:169], v[174:177], v[106:109]
	v_mfma_f32_16x16x32_bf16 v[98:101], v[158:161], v[182:185], v[98:101]
	v_mfma_f32_16x16x32_bf16 v[90:93], v[166:169], v[182:185], v[90:93]
	v_mfma_f32_16x16x32_bf16 v[82:85], v[158:161], v[190:193], v[82:85]
	v_mfma_f32_16x16x32_bf16 v[74:77], v[166:169], v[190:193], v[74:77]
	v_mfma_f32_16x16x32_bf16 v[70:73], v[158:161], v[204:207], v[70:73]
	v_mfma_f32_16x16x32_bf16 v[66:69], v[166:169], v[204:207], v[66:69]
	v_mfma_f32_16x16x32_bf16 v[114:117], v[162:165], v[178:181], v[114:117]
	v_mfma_f32_16x16x32_bf16 v[106:109], v[170:173], v[178:181], v[106:109]
	v_mfma_f32_16x16x32_bf16 v[98:101], v[162:165], v[186:189], v[98:101]
	v_mfma_f32_16x16x32_bf16 v[90:93], v[170:173], v[186:189], v[90:93]
	v_mfma_f32_16x16x32_bf16 v[82:85], v[162:165], v[200:203], v[82:85]
	v_mfma_f32_16x16x32_bf16 v[74:77], v[170:173], v[200:203], v[74:77]
	v_mfma_f32_16x16x32_bf16 v[70:73], v[162:165], v[208:211], v[70:73]
	v_mfma_f32_16x16x32_bf16 v[66:69], v[170:173], v[208:211], v[66:69]
	s_setprio 0
	s_barrier
	s_add_i32 m0, s85, 0xffffff80
	v_lshl_add_u64 v[138:139], v[138:139], 0, s[18:19]
	ds_read_b128 v[174:177], v140 offset:49152
	ds_read_b128 v[178:181], v140 offset:50176
	ds_read_b128 v[182:185], v140 offset:51200
	ds_read_b128 v[186:189], v140 offset:52224
	ds_read_b128 v[190:193], v140 offset:53248
	ds_read_b128 v[200:203], v140 offset:54272
	ds_read_b128 v[204:207], v140 offset:55296
	ds_read_b128 v[208:211], v140 offset:56320
	global_load_lds_dwordx4 v134, s[56:57] offset:128
	v_lshl_add_u64 v[138:139], v[194:195], 0, s[18:19]
	s_add_i32 m0, s88, 0xffffff80
	s_nop 0
	global_load_lds_dwordx4 v130, s[56:57] offset:128
	v_lshl_add_u64 v[138:139], s[50:51], 0, v[134:135]
	s_mov_b32 m0, s91
	s_nop 0
	global_load_lds_dwordx4 v134, s[50:51]
	v_lshl_add_u64 v[138:139], s[50:51], 0, v[130:131]
	s_mov_b32 m0, s92
	s_nop 0
	global_load_lds_dwordx4 v130, s[50:51]
	v_lshl_add_u64 v[138:139], v[212:213], 0, s[18:19]
	s_add_i32 m0, s89, 0xffffff80
	s_nop 0
	global_load_lds_dwordx4 v136, s[54:55] offset:128
	v_lshl_add_u64 v[138:139], v[214:215], 0, s[18:19]
	s_add_i32 m0, s90, 0xffffff80
	s_nop 0
	global_load_lds_dwordx4 v132, s[54:55] offset:128
	s_waitcnt vmcnt(8)
	s_waitcnt lgkmcnt(0)
	s_barrier
	s_setprio 1
	s_waitcnt lgkmcnt(0)
	v_mfma_f32_16x16x32_bf16 v[62:65], v[142:145], v[174:177], v[62:65]
	v_mfma_f32_16x16x32_bf16 v[58:61], v[150:153], v[174:177], v[58:61]
	v_mfma_f32_16x16x32_bf16 v[54:57], v[142:145], v[182:185], v[54:57]
	v_mfma_f32_16x16x32_bf16 v[46:49], v[150:153], v[182:185], v[46:49]
	v_mfma_f32_16x16x32_bf16 v[38:41], v[142:145], v[190:193], v[38:41]
	v_mfma_f32_16x16x32_bf16 v[30:33], v[150:153], v[190:193], v[30:33]
	v_mfma_f32_16x16x32_bf16 v[22:25], v[142:145], v[204:207], v[22:25]
	v_mfma_f32_16x16x32_bf16 v[14:17], v[150:153], v[204:207], v[14:17]
	v_mfma_f32_16x16x32_bf16 v[62:65], v[146:149], v[178:181], v[62:65]
	v_mfma_f32_16x16x32_bf16 v[58:61], v[154:157], v[178:181], v[58:61]
	v_mfma_f32_16x16x32_bf16 v[54:57], v[146:149], v[186:189], v[54:57]
	v_mfma_f32_16x16x32_bf16 v[46:49], v[154:157], v[186:189], v[46:49]
	v_mfma_f32_16x16x32_bf16 v[38:41], v[146:149], v[200:203], v[38:41]
	v_mfma_f32_16x16x32_bf16 v[30:33], v[154:157], v[200:203], v[30:33]
	v_mfma_f32_16x16x32_bf16 v[22:25], v[146:149], v[208:211], v[22:25]
	v_mfma_f32_16x16x32_bf16 v[14:17], v[154:157], v[208:211], v[14:17]
	s_setprio 0
	s_setprio 1
	v_mfma_f32_16x16x32_bf16 v[50:53], v[158:161], v[174:177], v[50:53]
	v_mfma_f32_16x16x32_bf16 v[42:45], v[166:169], v[174:177], v[42:45]
	v_mfma_f32_16x16x32_bf16 v[34:37], v[158:161], v[182:185], v[34:37]
	v_mfma_f32_16x16x32_bf16 v[26:29], v[166:169], v[182:185], v[26:29]
	v_mfma_f32_16x16x32_bf16 v[18:21], v[158:161], v[190:193], v[18:21]
	v_mfma_f32_16x16x32_bf16 v[10:13], v[166:169], v[190:193], v[10:13]
	v_mfma_f32_16x16x32_bf16 v[6:9], v[158:161], v[204:207], v[6:9]
	v_mfma_f32_16x16x32_bf16 v[2:5], v[166:169], v[204:207], v[2:5]
	v_mfma_f32_16x16x32_bf16 v[50:53], v[162:165], v[178:181], v[50:53]
	v_mfma_f32_16x16x32_bf16 v[42:45], v[170:173], v[178:181], v[42:45]
	v_mfma_f32_16x16x32_bf16 v[34:37], v[162:165], v[186:189], v[34:37]
	v_mfma_f32_16x16x32_bf16 v[26:29], v[170:173], v[186:189], v[26:29]
	v_mfma_f32_16x16x32_bf16 v[18:21], v[162:165], v[200:203], v[18:21]
	v_mfma_f32_16x16x32_bf16 v[10:13], v[170:173], v[200:203], v[10:13]
	v_mfma_f32_16x16x32_bf16 v[6:9], v[162:165], v[208:211], v[6:9]
	v_mfma_f32_16x16x32_bf16 v[2:5], v[170:173], v[208:211], v[2:5]
	s_setprio 0
	s_barrier
	s_andn2_b64 vcc, exec, s[48:49]
	s_mov_b64 s[50:51], -1
	s_mov_b64 s[48:49], 0
	s_mov_b64 s[52:53], 0x100
	s_cbranch_vccz .LBB0_1195
	s_and_b64 vcc, exec, s[14:15]
	s_cbranch_vccz .LBB0_1198
	s_barrier

.LBB0_1213:
	s_add_u32 s58, s40, s52
	s_addc_u32 s59, s41, s53
	s_add_u32 s56, s58, 0x100
	s_addc_u32 s57, s59, 0
	s_and_b64 s[54:55], s[50:51], exec
	s_cselect_b32 s55, s43, s57
	s_cselect_b32 s54, s42, s56
	s_add_u32 s52, s38, s52
	s_addc_u32 s53, s39, s53
	v_or_b32_e32 v0, 0x10000, v139
	s_add_u32 s52, s52, 0x100
	ds_read_b128 v[140:143], v0
	v_add_u32_e32 v0, 0x10400, v139
	s_addc_u32 s53, s53, 0
	ds_read_b128 v[144:147], v0
	v_add_u32_e32 v0, 0x10800, v139
	s_and_b64 s[50:51], s[50:51], exec
	ds_read_b128 v[148:151], v0
	v_add_u32_e32 v0, 0x10c00, v139
	s_cselect_b32 s57, s37, s53
	s_cselect_b32 s56, s29, s52
	s_add_u32 s60, s58, 0x40080
	ds_read_b128 v[152:155], v0
	v_or_b32_e32 v0, 0x14000, v139
	s_addc_u32 s61, s59, 0
	s_add_i32 m0, s63, 0xc000
	s_add_i32 vcc_lo, s63, 0xe000
	ds_read_b128 v[156:159], v0
	v_add_u32_e32 v0, 0x14400, v139
	s_add_u32 s58, s56, 0x80000
	ds_read_b128 v[160:163], v0
	v_add_u32_e32 v0, 0x14800, v139
	s_addc_u32 s59, s57, 0
	ds_read_b128 v[164:167], v0
	v_add_u32_e32 v0, 0x14c00, v139
	s_add_u32 s52, s54, 0x40000
	ds_read_b128 v[168:171], v0
	s_addc_u32 s53, s55, 0
	s_add_u32 s50, s56, 0x80080
	s_addc_u32 s51, s57, 0
	ds_read_b128 v[172:175], v138
	ds_read_b128 v[176:179], v138 offset:1024
	ds_read_b128 v[180:183], v138 offset:2048
	ds_read_b128 v[184:187], v138 offset:3072
	ds_read_b128 v[188:191], v138 offset:4096
	ds_read_b128 v[192:195], v138 offset:5120
	ds_read_b128 v[200:203], v138 offset:6144
	ds_read_b128 v[204:207], v138 offset:7168
	global_load_lds_dwordx4 v136, s[60:61]
	s_mov_b32 m0, vcc_lo
	s_nop 0
	global_load_lds_dwordx4 v132, s[60:61]
	s_waitcnt vmcnt(8)
	s_waitcnt lgkmcnt(0)
	s_barrier
	s_setprio 1
	s_waitcnt lgkmcnt(0)
	v_mfma_f32_16x16x32_bf16 v[126:129], v[140:143], v[172:175], v[126:129]
	v_mfma_f32_16x16x32_bf16 v[122:125], v[148:151], v[172:175], v[122:125]
	v_mfma_f32_16x16x32_bf16 v[118:121], v[140:143], v[180:183], v[118:121]
	v_mfma_f32_16x16x32_bf16 v[114:117], v[148:151], v[180:183], v[114:117]
	v_mfma_f32_16x16x32_bf16 v[102:105], v[140:143], v[188:191], v[102:105]
	v_mfma_f32_16x16x32_bf16 v[98:101], v[148:151], v[188:191], v[98:101]
	v_mfma_f32_16x16x32_bf16 v[86:89], v[140:143], v[200:203], v[86:89]
	v_mfma_f32_16x16x32_bf16 v[82:85], v[148:151], v[200:203], v[82:85]
	v_mfma_f32_16x16x32_bf16 v[126:129], v[144:147], v[176:179], v[126:129]
	v_mfma_f32_16x16x32_bf16 v[122:125], v[152:155], v[176:179], v[122:125]
	v_mfma_f32_16x16x32_bf16 v[118:121], v[144:147], v[184:187], v[118:121]
	v_mfma_f32_16x16x32_bf16 v[114:117], v[152:155], v[184:187], v[114:117]
	v_mfma_f32_16x16x32_bf16 v[102:105], v[144:147], v[192:195], v[102:105]
	v_mfma_f32_16x16x32_bf16 v[98:101], v[152:155], v[192:195], v[98:101]
	v_mfma_f32_16x16x32_bf16 v[86:89], v[144:147], v[204:207], v[86:89]
	v_mfma_f32_16x16x32_bf16 v[82:85], v[152:155], v[204:207], v[82:85]
	s_setprio 0
	s_setprio 1
	v_mfma_f32_16x16x32_bf16 v[110:113], v[156:159], v[172:175], v[110:113]
	v_mfma_f32_16x16x32_bf16 v[106:109], v[164:167], v[172:175], v[106:109]
	v_mfma_f32_16x16x32_bf16 v[94:97], v[156:159], v[180:183], v[94:97]
	v_mfma_f32_16x16x32_bf16 v[90:93], v[164:167], v[180:183], v[90:93]
	v_mfma_f32_16x16x32_bf16 v[78:81], v[156:159], v[188:191], v[78:81]
	v_mfma_f32_16x16x32_bf16 v[74:77], v[164:167], v[188:191], v[74:77]
	v_mfma_f32_16x16x32_bf16 v[70:73], v[156:159], v[200:203], v[70:73]
	v_mfma_f32_16x16x32_bf16 v[66:69], v[164:167], v[200:203], v[66:69]
	v_mfma_f32_16x16x32_bf16 v[110:113], v[160:163], v[176:179], v[110:113]
	v_mfma_f32_16x16x32_bf16 v[106:109], v[168:171], v[176:179], v[106:109]
	v_mfma_f32_16x16x32_bf16 v[94:97], v[160:163], v[184:187], v[94:97]
	v_mfma_f32_16x16x32_bf16 v[90:93], v[168:171], v[184:187], v[90:93]
	v_mfma_f32_16x16x32_bf16 v[78:81], v[160:163], v[192:195], v[78:81]
	v_mfma_f32_16x16x32_bf16 v[74:77], v[168:171], v[192:195], v[74:77]
	v_mfma_f32_16x16x32_bf16 v[70:73], v[160:163], v[204:207], v[70:73]
	v_mfma_f32_16x16x32_bf16 v[66:69], v[168:171], v[204:207], v[66:69]
	s_setprio 0
	s_barrier
	s_mov_b32 m0, s64
	ds_read_b128 v[172:175], v138 offset:16384
	ds_read_b128 v[176:179], v138 offset:17408
	ds_read_b128 v[180:183], v138 offset:18432
	ds_read_b128 v[184:187], v138 offset:19456
	ds_read_b128 v[188:191], v138 offset:20480
	ds_read_b128 v[192:195], v138 offset:21504
	ds_read_b128 v[200:203], v138 offset:22528
	ds_read_b128 v[204:207], v138 offset:23552
	global_load_lds_dwordx4 v134, s[56:57]
	s_mov_b32 m0, s65
	s_nop 0
	global_load_lds_dwordx4 v130, s[56:57]
	s_mov_b32 m0, s66
	s_nop 0
	global_load_lds_dwordx4 v134, s[58:59]
	s_mov_b32 m0, s67
	s_nop 0
	global_load_lds_dwordx4 v130, s[58:59]
	s_mov_b32 m0, s63
	s_nop 0
	global_load_lds_dwordx4 v136, s[54:55]
	s_mov_b32 m0, s80
	s_nop 0
	global_load_lds_dwordx4 v132, s[54:55]
	s_waitcnt vmcnt(8)
	s_waitcnt lgkmcnt(0)
	s_barrier
	s_setprio 1
	s_waitcnt lgkmcnt(0)
	v_mfma_f32_16x16x32_bf16 v[62:65], v[140:143], v[172:175], v[62:65]
	v_mfma_f32_16x16x32_bf16 v[58:61], v[148:151], v[172:175], v[58:61]
	v_mfma_f32_16x16x32_bf16 v[54:57], v[140:143], v[180:183], v[54:57]
	v_mfma_f32_16x16x32_bf16 v[50:53], v[148:151], v[180:183], v[50:53]
	v_mfma_f32_16x16x32_bf16 v[38:41], v[140:143], v[188:191], v[38:41]
	v_mfma_f32_16x16x32_bf16 v[34:37], v[148:151], v[188:191], v[34:37]
	v_mfma_f32_16x16x32_bf16 v[22:25], v[140:143], v[200:203], v[22:25]
	v_mfma_f32_16x16x32_bf16 v[18:21], v[148:151], v[200:203], v[18:21]
	v_mfma_f32_16x16x32_bf16 v[62:65], v[144:147], v[176:179], v[62:65]
	v_mfma_f32_16x16x32_bf16 v[58:61], v[152:155], v[176:179], v[58:61]
	v_mfma_f32_16x16x32_bf16 v[54:57], v[144:147], v[184:187], v[54:57]
	v_mfma_f32_16x16x32_bf16 v[50:53], v[152:155], v[184:187], v[50:53]
	v_mfma_f32_16x16x32_bf16 v[38:41], v[144:147], v[192:195], v[38:41]
	v_mfma_f32_16x16x32_bf16 v[34:37], v[152:155], v[192:195], v[34:37]
	v_mfma_f32_16x16x32_bf16 v[22:25], v[144:147], v[204:207], v[22:25]
	v_mfma_f32_16x16x32_bf16 v[18:21], v[152:155], v[204:207], v[18:21]
	s_setprio 0
	s_setprio 1
	v_mfma_f32_16x16x32_bf16 v[46:49], v[156:159], v[172:175], v[46:49]
	v_mfma_f32_16x16x32_bf16 v[42:45], v[164:167], v[172:175], v[42:45]
	v_mfma_f32_16x16x32_bf16 v[30:33], v[156:159], v[180:183], v[30:33]
	v_mfma_f32_16x16x32_bf16 v[26:29], v[164:167], v[180:183], v[26:29]
	v_mfma_f32_16x16x32_bf16 v[14:17], v[156:159], v[188:191], v[14:17]
	v_mfma_f32_16x16x32_bf16 v[10:13], v[164:167], v[188:191], v[10:13]
	v_mfma_f32_16x16x32_bf16 v[6:9], v[156:159], v[200:203], v[6:9]
	v_mfma_f32_16x16x32_bf16 v[2:5], v[164:167], v[200:203], v[2:5]
	v_mfma_f32_16x16x32_bf16 v[46:49], v[160:163], v[176:179], v[46:49]
	v_mfma_f32_16x16x32_bf16 v[42:45], v[168:171], v[176:179], v[42:45]
	v_mfma_f32_16x16x32_bf16 v[30:33], v[160:163], v[184:187], v[30:33]
	v_mfma_f32_16x16x32_bf16 v[26:29], v[168:171], v[184:187], v[26:29]
	v_mfma_f32_16x16x32_bf16 v[14:17], v[160:163], v[192:195], v[14:17]
	v_mfma_f32_16x16x32_bf16 v[10:13], v[168:171], v[192:195], v[10:13]
	v_mfma_f32_16x16x32_bf16 v[6:9], v[160:163], v[204:207], v[6:9]
	v_mfma_f32_16x16x32_bf16 v[2:5], v[168:171], v[204:207], v[2:5]
	s_setprio 0
	s_barrier
	v_or_b32_e32 v0, 0x18000, v139
	v_add_u32_e32 v144, 0x18400, v139
	ds_read_b128 v[140:143], v0
	ds_read_b128 v[144:147], v144
	v_add_u32_e32 v0, 0x18800, v139
	v_add_u32_e32 v152, 0x18c00, v139
	ds_read_b128 v[148:151], v0
	ds_read_b128 v[152:155], v152
	v_or_b32_e32 v0, 0x1c000, v139
	v_add_u32_e32 v160, 0x1c400, v139
	ds_read_b128 v[156:159], v0
	ds_read_b128 v[160:163], v160
	v_add_u32_e32 v0, 0x1c800, v139
	v_add_u32_e32 v168, 0x1cc00, v139
	ds_read_b128 v[164:167], v0
	ds_read_b128 v[168:171], v168
	s_mov_b32 m0, s82
	ds_read_b128 v[172:175], v138 offset:32768
	ds_read_b128 v[176:179], v138 offset:33792
	ds_read_b128 v[180:183], v138 offset:34816
	ds_read_b128 v[184:187], v138 offset:35840
	ds_read_b128 v[188:191], v138 offset:36864
	ds_read_b128 v[192:195], v138 offset:37888
	ds_read_b128 v[200:203], v138 offset:38912
	ds_read_b128 v[204:207], v138 offset:39936
	global_load_lds_dwordx4 v136, s[52:53]
	s_mov_b32 m0, s83
	s_nop 0
	global_load_lds_dwordx4 v132, s[52:53]
	s_waitcnt vmcnt(8)
	s_waitcnt lgkmcnt(0)
	s_barrier
	s_setprio 1
	s_waitcnt lgkmcnt(0)
	v_mfma_f32_16x16x32_bf16 v[126:129], v[140:143], v[172:175], v[126:129]
	v_mfma_f32_16x16x32_bf16 v[122:125], v[148:151], v[172:175], v[122:125]
	v_mfma_f32_16x16x32_bf16 v[118:121], v[140:143], v[180:183], v[118:121]
	v_mfma_f32_16x16x32_bf16 v[114:117], v[148:151], v[180:183], v[114:117]
	v_mfma_f32_16x16x32_bf16 v[102:105], v[140:143], v[188:191], v[102:105]
	v_mfma_f32_16x16x32_bf16 v[98:101], v[148:151], v[188:191], v[98:101]
	v_mfma_f32_16x16x32_bf16 v[86:89], v[140:143], v[200:203], v[86:89]
	v_mfma_f32_16x16x32_bf16 v[82:85], v[148:151], v[200:203], v[82:85]
	v_mfma_f32_16x16x32_bf16 v[126:129], v[144:147], v[176:179], v[126:129]
	v_mfma_f32_16x16x32_bf16 v[122:125], v[152:155], v[176:179], v[122:125]
	v_mfma_f32_16x16x32_bf16 v[118:121], v[144:147], v[184:187], v[118:121]
	v_mfma_f32_16x16x32_bf16 v[114:117], v[152:155], v[184:187], v[114:117]
	v_mfma_f32_16x16x32_bf16 v[102:105], v[144:147], v[192:195], v[102:105]
	v_mfma_f32_16x16x32_bf16 v[98:101], v[152:155], v[192:195], v[98:101]
	v_mfma_f32_16x16x32_bf16 v[86:89], v[144:147], v[204:207], v[86:89]
	v_mfma_f32_16x16x32_bf16 v[82:85], v[152:155], v[204:207], v[82:85]
	s_setprio 0
	s_setprio 1
	v_mfma_f32_16x16x32_bf16 v[110:113], v[156:159], v[172:175], v[110:113]
	v_mfma_f32_16x16x32_bf16 v[106:109], v[164:167], v[172:175], v[106:109]
	v_mfma_f32_16x16x32_bf16 v[94:97], v[156:159], v[180:183], v[94:97]
	v_mfma_f32_16x16x32_bf16 v[90:93], v[164:167], v[180:183], v[90:93]
	v_mfma_f32_16x16x32_bf16 v[78:81], v[156:159], v[188:191], v[78:81]
	v_mfma_f32_16x16x32_bf16 v[74:77], v[164:167], v[188:191], v[74:77]
	v_mfma_f32_16x16x32_bf16 v[70:73], v[156:159], v[200:203], v[70:73]
	v_mfma_f32_16x16x32_bf16 v[66:69], v[164:167], v[200:203], v[66:69]
	v_mfma_f32_16x16x32_bf16 v[110:113], v[160:163], v[176:179], v[110:113]
	v_mfma_f32_16x16x32_bf16 v[106:109], v[168:171], v[176:179], v[106:109]
	v_mfma_f32_16x16x32_bf16 v[94:97], v[160:163], v[184:187], v[94:97]
	v_mfma_f32_16x16x32_bf16 v[90:93], v[168:171], v[184:187], v[90:93]
	v_mfma_f32_16x16x32_bf16 v[78:81], v[160:163], v[192:195], v[78:81]
	v_mfma_f32_16x16x32_bf16 v[74:77], v[168:171], v[192:195], v[74:77]
	v_mfma_f32_16x16x32_bf16 v[70:73], v[160:163], v[204:207], v[70:73]
	v_mfma_f32_16x16x32_bf16 v[66:69], v[168:171], v[204:207], v[66:69]
	s_setprio 0
	s_barrier
	s_add_i32 m0, s85, 0xffffff80
	ds_read_b128 v[172:175], v138 offset:49152
	ds_read_b128 v[176:179], v138 offset:50176
	ds_read_b128 v[180:183], v138 offset:51200
	ds_read_b128 v[184:187], v138 offset:52224
	ds_read_b128 v[188:191], v138 offset:53248
	ds_read_b128 v[192:195], v138 offset:54272
	ds_read_b128 v[200:203], v138 offset:55296
	ds_read_b128 v[204:207], v138 offset:56320
	global_load_lds_dwordx4 v134, s[56:57] offset:128
	s_add_i32 m0, s88, 0xffffff80
	s_nop 0
	global_load_lds_dwordx4 v130, s[56:57] offset:128
	s_mov_b32 m0, s91
	s_nop 0
	global_load_lds_dwordx4 v134, s[50:51]
	s_mov_b32 m0, s92
	s_nop 0
	global_load_lds_dwordx4 v130, s[50:51]
	s_add_i32 m0, s89, 0xffffff80
	s_nop 0
	global_load_lds_dwordx4 v136, s[54:55] offset:128
	s_add_i32 m0, s90, 0xffffff80
	s_nop 0
	global_load_lds_dwordx4 v132, s[54:55] offset:128
	s_waitcnt vmcnt(8)
	s_waitcnt lgkmcnt(0)
	s_barrier
	s_setprio 1
	s_waitcnt lgkmcnt(0)
	v_mfma_f32_16x16x32_bf16 v[62:65], v[140:143], v[172:175], v[62:65]
	v_mfma_f32_16x16x32_bf16 v[58:61], v[148:151], v[172:175], v[58:61]
	v_mfma_f32_16x16x32_bf16 v[54:57], v[140:143], v[180:183], v[54:57]
	v_mfma_f32_16x16x32_bf16 v[50:53], v[148:151], v[180:183], v[50:53]
	v_mfma_f32_16x16x32_bf16 v[38:41], v[140:143], v[188:191], v[38:41]
	v_mfma_f32_16x16x32_bf16 v[34:37], v[148:151], v[188:191], v[34:37]
	v_mfma_f32_16x16x32_bf16 v[22:25], v[140:143], v[200:203], v[22:25]
	v_mfma_f32_16x16x32_bf16 v[18:21], v[148:151], v[200:203], v[18:21]
	v_mfma_f32_16x16x32_bf16 v[62:65], v[144:147], v[176:179], v[62:65]
	v_mfma_f32_16x16x32_bf16 v[58:61], v[152:155], v[176:179], v[58:61]
	v_mfma_f32_16x16x32_bf16 v[54:57], v[144:147], v[184:187], v[54:57]
	v_mfma_f32_16x16x32_bf16 v[50:53], v[152:155], v[184:187], v[50:53]
	v_mfma_f32_16x16x32_bf16 v[38:41], v[144:147], v[192:195], v[38:41]
	v_mfma_f32_16x16x32_bf16 v[34:37], v[152:155], v[192:195], v[34:37]
	v_mfma_f32_16x16x32_bf16 v[22:25], v[144:147], v[204:207], v[22:25]
	v_mfma_f32_16x16x32_bf16 v[18:21], v[152:155], v[204:207], v[18:21]
	s_setprio 0
	s_setprio 1
	v_mfma_f32_16x16x32_bf16 v[46:49], v[156:159], v[172:175], v[46:49]
	v_mfma_f32_16x16x32_bf16 v[42:45], v[164:167], v[172:175], v[42:45]
	v_mfma_f32_16x16x32_bf16 v[30:33], v[156:159], v[180:183], v[30:33]
	v_mfma_f32_16x16x32_bf16 v[26:29], v[164:167], v[180:183], v[26:29]
	v_mfma_f32_16x16x32_bf16 v[14:17], v[156:159], v[188:191], v[14:17]
	v_mfma_f32_16x16x32_bf16 v[10:13], v[164:167], v[188:191], v[10:13]
	v_mfma_f32_16x16x32_bf16 v[6:9], v[156:159], v[200:203], v[6:9]
	v_mfma_f32_16x16x32_bf16 v[2:5], v[164:167], v[200:203], v[2:5]
	v_mfma_f32_16x16x32_bf16 v[46:49], v[160:163], v[176:179], v[46:49]
	v_mfma_f32_16x16x32_bf16 v[42:45], v[168:171], v[176:179], v[42:45]
	v_mfma_f32_16x16x32_bf16 v[30:33], v[160:163], v[184:187], v[30:33]
	v_mfma_f32_16x16x32_bf16 v[26:29], v[168:171], v[184:187], v[26:29]
	v_mfma_f32_16x16x32_bf16 v[14:17], v[160:163], v[192:195], v[14:17]
	v_mfma_f32_16x16x32_bf16 v[10:13], v[168:171], v[192:195], v[10:13]
	v_mfma_f32_16x16x32_bf16 v[6:9], v[160:163], v[204:207], v[6:9]
	v_mfma_f32_16x16x32_bf16 v[2:5], v[168:171], v[204:207], v[2:5]
	s_setprio 0
	s_barrier
	s_andn2_b64 vcc, exec, s[48:49]
	s_mov_b64 s[50:51], -1
	s_mov_b64 s[48:49], 0
	s_mov_b64 s[52:53], 0x100
	s_cbranch_vccz .LBB0_1213
	s_and_b64 vcc, exec, s[14:15]
	s_cbranch_vccz .LBB0_1216
	s_barrier

.LBB0_2006:
	v_or_b32_e32 v0, 0x10000, v164
	v_add_u32_e32 v165, 0x10400, v164
	ds_read_b128 v[158:161], v0
	ds_read_b128 v[166:169], v165
	v_add_u32_e32 v0, 0x10800, v164
	v_add_u32_e32 v165, 0x10c00, v164
	ds_read_b128 v[170:173], v0
	ds_read_b128 v[174:177], v165
	v_or_b32_e32 v0, 0x14000, v164
	v_add_u32_e32 v165, 0x14400, v164
	ds_read_b128 v[178:181], v0
	ds_read_b128 v[182:185], v165
	v_add_u32_e32 v0, 0x14800, v164
	v_add_u32_e32 v165, 0x14c00, v164
	ds_read_b128 v[186:189], v0
	ds_read_b128 v[190:193], v165
	s_add_u32 s40, s36, 0xfffc0080
	s_addc_u32 s41, s37, -1
	s_cmp_eq_u32 vcc_lo, 12
	s_cselect_b32 s63, s29, s41
	s_cselect_b32 s62, s47, s40
	s_cselect_b32 s61, s49, s95
	s_cselect_b32 s60, s59, s80
	s_add_i32 m0, s31, 0xc000
	ds_read_b128 v[200:203], v163
	ds_read_b128 v[204:207], v163 offset:1024
	ds_read_b128 v[208:211], v163 offset:2048
	ds_read_b128 v[212:215], v163 offset:3072
	ds_read_b128 v[216:219], v163 offset:4096
	ds_read_b128 v[220:223], v163 offset:5120
	ds_read_b128 v[236:239], v163 offset:6144
	ds_read_b128 v[240:243], v163 offset:7168
	global_load_lds_dwordx4 v138, s[36:37]
	s_add_i32 m0, s31, 0xe000
	s_nop 0
	global_load_lds_dwordx4 v140, s[36:37]
	s_waitcnt vmcnt(8)
	s_waitcnt lgkmcnt(0)
	s_barrier
	s_setprio 1
	s_waitcnt lgkmcnt(0)
	v_mfma_f32_16x16x32_bf16 v[126:129], v[158:161], v[200:203], v[126:129]
	v_mfma_f32_16x16x32_bf16 v[122:125], v[170:173], v[200:203], v[122:125]
	v_mfma_f32_16x16x32_bf16 v[114:117], v[158:161], v[208:211], v[114:117]
	v_mfma_f32_16x16x32_bf16 v[106:109], v[170:173], v[208:211], v[106:109]
	v_mfma_f32_16x16x32_bf16 v[98:101], v[158:161], v[216:219], v[98:101]
	v_mfma_f32_16x16x32_bf16 v[90:93], v[170:173], v[216:219], v[90:93]
	v_mfma_f32_16x16x32_bf16 v[82:85], v[158:161], v[236:239], v[82:85]
	v_mfma_f32_16x16x32_bf16 v[74:77], v[170:173], v[236:239], v[74:77]
	v_mfma_f32_16x16x32_bf16 v[126:129], v[166:169], v[204:207], v[126:129]
	v_mfma_f32_16x16x32_bf16 v[122:125], v[174:177], v[204:207], v[122:125]
	v_mfma_f32_16x16x32_bf16 v[114:117], v[166:169], v[212:215], v[114:117]
	v_mfma_f32_16x16x32_bf16 v[106:109], v[174:177], v[212:215], v[106:109]
	v_mfma_f32_16x16x32_bf16 v[98:101], v[166:169], v[220:223], v[98:101]
	v_mfma_f32_16x16x32_bf16 v[90:93], v[174:177], v[220:223], v[90:93]
	v_mfma_f32_16x16x32_bf16 v[82:85], v[166:169], v[240:243], v[82:85]
	v_mfma_f32_16x16x32_bf16 v[74:77], v[174:177], v[240:243], v[74:77]
	s_setprio 0
	s_setprio 1
	v_mfma_f32_16x16x32_bf16 v[118:121], v[178:181], v[200:203], v[118:121]
	v_mfma_f32_16x16x32_bf16 v[110:113], v[186:189], v[200:203], v[110:113]
	v_mfma_f32_16x16x32_bf16 v[102:105], v[178:181], v[208:211], v[102:105]
	v_mfma_f32_16x16x32_bf16 v[94:97], v[186:189], v[208:211], v[94:97]
	v_mfma_f32_16x16x32_bf16 v[86:89], v[178:181], v[216:219], v[86:89]
	v_mfma_f32_16x16x32_bf16 v[78:81], v[186:189], v[216:219], v[78:81]
	v_mfma_f32_16x16x32_bf16 v[70:73], v[178:181], v[236:239], v[70:73]
	v_mfma_f32_16x16x32_bf16 v[66:69], v[186:189], v[236:239], v[66:69]
	v_mfma_f32_16x16x32_bf16 v[118:121], v[182:185], v[204:207], v[118:121]
	v_mfma_f32_16x16x32_bf16 v[110:113], v[190:193], v[204:207], v[110:113]
	v_mfma_f32_16x16x32_bf16 v[102:105], v[182:185], v[212:215], v[102:105]
	v_mfma_f32_16x16x32_bf16 v[94:97], v[190:193], v[212:215], v[94:97]
	v_mfma_f32_16x16x32_bf16 v[86:89], v[182:185], v[220:223], v[86:89]
	v_mfma_f32_16x16x32_bf16 v[78:81], v[190:193], v[220:223], v[78:81]
	v_mfma_f32_16x16x32_bf16 v[70:73], v[182:185], v[240:243], v[70:73]
	v_mfma_f32_16x16x32_bf16 v[66:69], v[190:193], v[240:243], v[66:69]
	s_setprio 0
	s_barrier
	s_mov_b32 m0, s51
	s_add_u32 s40, s60, 0x40000
	ds_read_b128 v[200:203], v163 offset:16384
	ds_read_b128 v[204:207], v163 offset:17408
	ds_read_b128 v[208:211], v163 offset:18432
	ds_read_b128 v[212:215], v163 offset:19456
	ds_read_b128 v[216:219], v163 offset:20480
	ds_read_b128 v[220:223], v163 offset:21504
	ds_read_b128 v[236:239], v163 offset:22528
	ds_read_b128 v[240:243], v163 offset:23552
	global_load_lds_dwordx4 v132, s[60:61]
	v_lshl_add_u64 v[226:227], s[60:61], 0, v[136:137]
	s_mov_b32 m0, s65
	s_addc_u32 s41, s61, 0
	global_load_lds_dwordx4 v136, s[60:61]
	s_mov_b32 m0, s66
	s_nop 0
	global_load_lds_dwordx4 v132, s[40:41]
	s_mov_b32 m0, s67
	s_nop 0
	global_load_lds_dwordx4 v136, s[40:41]
	s_mov_b32 m0, s31
	s_nop 0
	global_load_lds_dwordx4 v130, s[62:63]
	s_mov_b32 m0, s82
	s_nop 0
	global_load_lds_dwordx4 v134, s[62:63]
	s_waitcnt vmcnt(8)
	s_waitcnt lgkmcnt(0)
	s_barrier
	s_setprio 1
	s_waitcnt lgkmcnt(0)
	v_mfma_f32_16x16x32_bf16 v[62:65], v[158:161], v[200:203], v[62:65]
	v_mfma_f32_16x16x32_bf16 v[58:61], v[170:173], v[200:203], v[58:61]
	v_mfma_f32_16x16x32_bf16 v[54:57], v[158:161], v[208:211], v[54:57]
	v_mfma_f32_16x16x32_bf16 v[46:49], v[170:173], v[208:211], v[46:49]
	v_mfma_f32_16x16x32_bf16 v[38:41], v[158:161], v[216:219], v[38:41]
	v_mfma_f32_16x16x32_bf16 v[30:33], v[170:173], v[216:219], v[30:33]
	v_mfma_f32_16x16x32_bf16 v[22:25], v[158:161], v[236:239], v[22:25]
	v_mfma_f32_16x16x32_bf16 v[14:17], v[170:173], v[236:239], v[14:17]
	v_mfma_f32_16x16x32_bf16 v[62:65], v[166:169], v[204:207], v[62:65]
	v_mfma_f32_16x16x32_bf16 v[58:61], v[174:177], v[204:207], v[58:61]
	v_mfma_f32_16x16x32_bf16 v[54:57], v[166:169], v[212:215], v[54:57]
	v_mfma_f32_16x16x32_bf16 v[46:49], v[174:177], v[212:215], v[46:49]
	v_mfma_f32_16x16x32_bf16 v[38:41], v[166:169], v[220:223], v[38:41]
	v_mfma_f32_16x16x32_bf16 v[30:33], v[174:177], v[220:223], v[30:33]
	v_mfma_f32_16x16x32_bf16 v[22:25], v[166:169], v[240:243], v[22:25]
	v_mfma_f32_16x16x32_bf16 v[14:17], v[174:177], v[240:243], v[14:17]
	s_setprio 0
	s_setprio 1
	v_mfma_f32_16x16x32_bf16 v[50:53], v[178:181], v[200:203], v[50:53]
	v_mfma_f32_16x16x32_bf16 v[42:45], v[186:189], v[200:203], v[42:45]
	v_mfma_f32_16x16x32_bf16 v[34:37], v[178:181], v[208:211], v[34:37]
	v_mfma_f32_16x16x32_bf16 v[26:29], v[186:189], v[208:211], v[26:29]
	v_mfma_f32_16x16x32_bf16 v[18:21], v[178:181], v[216:219], v[18:21]
	v_mfma_f32_16x16x32_bf16 v[10:13], v[186:189], v[216:219], v[10:13]
	v_mfma_f32_16x16x32_bf16 v[6:9], v[178:181], v[236:239], v[6:9]
	v_mfma_f32_16x16x32_bf16 v[2:5], v[186:189], v[236:239], v[2:5]
	v_mfma_f32_16x16x32_bf16 v[50:53], v[182:185], v[204:207], v[50:53]
	v_mfma_f32_16x16x32_bf16 v[42:45], v[190:193], v[204:207], v[42:45]
	v_mfma_f32_16x16x32_bf16 v[34:37], v[182:185], v[212:215], v[34:37]
	v_mfma_f32_16x16x32_bf16 v[26:29], v[190:193], v[212:215], v[26:29]
	v_mfma_f32_16x16x32_bf16 v[18:21], v[182:185], v[220:223], v[18:21]
	v_mfma_f32_16x16x32_bf16 v[10:13], v[190:193], v[220:223], v[10:13]
	v_mfma_f32_16x16x32_bf16 v[6:9], v[182:185], v[240:243], v[6:9]
	v_mfma_f32_16x16x32_bf16 v[2:5], v[190:193], v[240:243], v[2:5]
	s_setprio 0
	s_barrier
	v_or_b32_e32 v0, 0x18000, v164
	v_add_u32_e32 v165, 0x18400, v164
	ds_read_b128 v[158:161], v0
	ds_read_b128 v[166:169], v165
	v_add_u32_e32 v0, 0x18800, v164
	v_add_u32_e32 v165, 0x18c00, v164
	ds_read_b128 v[170:173], v0
	ds_read_b128 v[174:177], v165
	v_or_b32_e32 v0, 0x1c000, v164
	v_add_u32_e32 v165, 0x1c400, v164
	ds_read_b128 v[178:181], v0
	ds_read_b128 v[182:185], v165
	v_add_u32_e32 v0, 0x1c800, v164
	v_add_u32_e32 v165, 0x1cc00, v164
	ds_read_b128 v[186:189], v0
	ds_read_b128 v[190:193], v165
	s_add_u32 s40, s62, 0x40000
	s_addc_u32 s41, s63, 0
	s_mov_b32 m0, s83
	ds_read_b128 v[200:203], v163 offset:32768
	ds_read_b128 v[204:207], v163 offset:33792
	ds_read_b128 v[208:211], v163 offset:34816
	ds_read_b128 v[212:215], v163 offset:35840
	ds_read_b128 v[216:219], v163 offset:36864
	ds_read_b128 v[220:223], v163 offset:37888
	ds_read_b128 v[236:239], v163 offset:38912
	ds_read_b128 v[240:243], v163 offset:39936
	global_load_lds_dwordx4 v130, s[40:41]
	s_mov_b32 m0, s84
	s_nop 0
	global_load_lds_dwordx4 v134, s[40:41]
	s_waitcnt vmcnt(8)
	s_waitcnt lgkmcnt(0)
	s_barrier
	s_setprio 1
	s_waitcnt lgkmcnt(0)
	v_mfma_f32_16x16x32_bf16 v[126:129], v[158:161], v[200:203], v[126:129]
	v_mfma_f32_16x16x32_bf16 v[122:125], v[170:173], v[200:203], v[122:125]
	v_mfma_f32_16x16x32_bf16 v[114:117], v[158:161], v[208:211], v[114:117]
	v_mfma_f32_16x16x32_bf16 v[106:109], v[170:173], v[208:211], v[106:109]
	v_mfma_f32_16x16x32_bf16 v[98:101], v[158:161], v[216:219], v[98:101]
	v_mfma_f32_16x16x32_bf16 v[90:93], v[170:173], v[216:219], v[90:93]
	v_mfma_f32_16x16x32_bf16 v[82:85], v[158:161], v[236:239], v[82:85]
	v_mfma_f32_16x16x32_bf16 v[74:77], v[170:173], v[236:239], v[74:77]
	v_mfma_f32_16x16x32_bf16 v[126:129], v[166:169], v[204:207], v[126:129]
	v_mfma_f32_16x16x32_bf16 v[122:125], v[174:177], v[204:207], v[122:125]
	v_mfma_f32_16x16x32_bf16 v[114:117], v[166:169], v[212:215], v[114:117]
	v_mfma_f32_16x16x32_bf16 v[106:109], v[174:177], v[212:215], v[106:109]
	v_mfma_f32_16x16x32_bf16 v[98:101], v[166:169], v[220:223], v[98:101]
	v_mfma_f32_16x16x32_bf16 v[90:93], v[174:177], v[220:223], v[90:93]
	v_mfma_f32_16x16x32_bf16 v[82:85], v[166:169], v[240:243], v[82:85]
	v_mfma_f32_16x16x32_bf16 v[74:77], v[174:177], v[240:243], v[74:77]
	s_setprio 0
	s_setprio 1
	v_mfma_f32_16x16x32_bf16 v[118:121], v[178:181], v[200:203], v[118:121]
	v_mfma_f32_16x16x32_bf16 v[110:113], v[186:189], v[200:203], v[110:113]
	v_mfma_f32_16x16x32_bf16 v[102:105], v[178:181], v[208:211], v[102:105]
	v_mfma_f32_16x16x32_bf16 v[94:97], v[186:189], v[208:211], v[94:97]
	v_mfma_f32_16x16x32_bf16 v[86:89], v[178:181], v[216:219], v[86:89]
	v_mfma_f32_16x16x32_bf16 v[78:81], v[186:189], v[216:219], v[78:81]
	v_mfma_f32_16x16x32_bf16 v[70:73], v[178:181], v[236:239], v[70:73]
	v_mfma_f32_16x16x32_bf16 v[66:69], v[186:189], v[236:239], v[66:69]
	v_mfma_f32_16x16x32_bf16 v[118:121], v[182:185], v[204:207], v[118:121]
	v_mfma_f32_16x16x32_bf16 v[110:113], v[190:193], v[204:207], v[110:113]
	v_mfma_f32_16x16x32_bf16 v[102:105], v[182:185], v[212:215], v[102:105]
	v_mfma_f32_16x16x32_bf16 v[94:97], v[190:193], v[212:215], v[94:97]
	v_mfma_f32_16x16x32_bf16 v[86:89], v[182:185], v[220:223], v[86:89]
	v_mfma_f32_16x16x32_bf16 v[78:81], v[190:193], v[220:223], v[78:81]
	v_mfma_f32_16x16x32_bf16 v[70:73], v[182:185], v[240:243], v[70:73]
	v_mfma_f32_16x16x32_bf16 v[66:69], v[190:193], v[240:243], v[66:69]
	s_setprio 0
	s_barrier
	s_add_i32 m0, s88, 0xffffff80
	s_add_u32 s40, s60, 0x40080
	ds_read_b128 v[200:203], v163 offset:49152
	ds_read_b128 v[204:207], v163 offset:50176
	ds_read_b128 v[208:211], v163 offset:51200
	ds_read_b128 v[212:215], v163 offset:52224
	ds_read_b128 v[216:219], v163 offset:53248
	ds_read_b128 v[220:223], v163 offset:54272
	ds_read_b128 v[236:239], v163 offset:55296
	ds_read_b128 v[240:243], v163 offset:56320
	global_load_lds_dwordx4 v132, s[60:61] offset:128
	v_lshl_add_u64 v[194:195], v[226:227], 0, s[18:19]
	s_mov_b32 m0, s89
	s_addc_u32 s41, s61, 0
	global_load_lds_dwordx4 v[194:195], off
	s_mov_b32 m0, s92
	s_nop 0
	global_load_lds_dwordx4 v132, s[40:41]
	s_mov_b32 m0, s93
	s_nop 0
	global_load_lds_dwordx4 v136, s[40:41]
	s_add_i32 m0, s90, 0xffffff80
	s_nop 0
	global_load_lds_dwordx4 v130, s[62:63] offset:128
	s_add_i32 m0, s91, 0xffffff80
	s_nop 0
	global_load_lds_dwordx4 v134, s[62:63] offset:128
	s_waitcnt vmcnt(8)
	s_waitcnt lgkmcnt(0)
	s_barrier
	s_setprio 1
	s_waitcnt lgkmcnt(0)
	v_mfma_f32_16x16x32_bf16 v[62:65], v[158:161], v[200:203], v[62:65]
	v_mfma_f32_16x16x32_bf16 v[58:61], v[170:173], v[200:203], v[58:61]
	v_mfma_f32_16x16x32_bf16 v[54:57], v[158:161], v[208:211], v[54:57]
	v_mfma_f32_16x16x32_bf16 v[46:49], v[170:173], v[208:211], v[46:49]
	v_mfma_f32_16x16x32_bf16 v[38:41], v[158:161], v[216:219], v[38:41]
	v_mfma_f32_16x16x32_bf16 v[30:33], v[170:173], v[216:219], v[30:33]
	v_mfma_f32_16x16x32_bf16 v[22:25], v[158:161], v[236:239], v[22:25]
	v_mfma_f32_16x16x32_bf16 v[14:17], v[170:173], v[236:239], v[14:17]
	v_mfma_f32_16x16x32_bf16 v[62:65], v[166:169], v[204:207], v[62:65]
	v_mfma_f32_16x16x32_bf16 v[58:61], v[174:177], v[204:207], v[58:61]
	v_mfma_f32_16x16x32_bf16 v[54:57], v[166:169], v[212:215], v[54:57]
	v_mfma_f32_16x16x32_bf16 v[46:49], v[174:177], v[212:215], v[46:49]
	v_mfma_f32_16x16x32_bf16 v[38:41], v[166:169], v[220:223], v[38:41]
	v_mfma_f32_16x16x32_bf16 v[30:33], v[174:177], v[220:223], v[30:33]
	v_mfma_f32_16x16x32_bf16 v[22:25], v[166:169], v[240:243], v[22:25]
	v_mfma_f32_16x16x32_bf16 v[14:17], v[174:177], v[240:243], v[14:17]
	s_setprio 0
	s_setprio 1
	v_mfma_f32_16x16x32_bf16 v[50:53], v[178:181], v[200:203], v[50:53]
	v_mfma_f32_16x16x32_bf16 v[42:45], v[186:189], v[200:203], v[42:45]
	v_mfma_f32_16x16x32_bf16 v[34:37], v[178:181], v[208:211], v[34:37]
	v_mfma_f32_16x16x32_bf16 v[26:29], v[186:189], v[208:211], v[26:29]
	v_mfma_f32_16x16x32_bf16 v[18:21], v[178:181], v[216:219], v[18:21]
	v_mfma_f32_16x16x32_bf16 v[10:13], v[186:189], v[216:219], v[10:13]
	v_mfma_f32_16x16x32_bf16 v[6:9], v[178:181], v[236:239], v[6:9]
	v_mfma_f32_16x16x32_bf16 v[2:5], v[186:189], v[236:239], v[2:5]
	v_mfma_f32_16x16x32_bf16 v[50:53], v[182:185], v[204:207], v[50:53]
	v_mfma_f32_16x16x32_bf16 v[42:45], v[190:193], v[204:207], v[42:45]
	v_mfma_f32_16x16x32_bf16 v[34:37], v[182:185], v[212:215], v[34:37]
	v_mfma_f32_16x16x32_bf16 v[26:29], v[190:193], v[212:215], v[26:29]
	v_mfma_f32_16x16x32_bf16 v[18:21], v[182:185], v[220:223], v[18:21]
	v_mfma_f32_16x16x32_bf16 v[10:13], v[190:193], v[220:223], v[10:13]
	v_mfma_f32_16x16x32_bf16 v[6:9], v[182:185], v[240:243], v[6:9]
	v_mfma_f32_16x16x32_bf16 v[2:5], v[190:193], v[240:243], v[2:5]
	s_setprio 0
	s_barrier
	s_add_i32 vcc_lo, vcc_lo, 2
	s_add_u32 s36, s36, 0x100
	s_addc_u32 s37, s37, 0
	s_add_u32 s80, s80, 0x100
	s_addc_u32 s95, s95, 0
	s_cmp_gt_u32 vcc_lo, 13
	s_cbranch_scc0 .LBB0_2006
	s_and_b64 vcc, exec, s[16:17]
	s_cbranch_vccz .LBB0_2009
	s_barrier

.LBB0_2067:
	v_or_b32_e32 v0, 0x10000, v143
	v_add_u32_e32 v148, 0x10400, v143
	ds_read_b128 v[144:147], v0
	ds_read_b128 v[148:151], v148
	v_add_u32_e32 v0, 0x10800, v143
	v_add_u32_e32 v156, 0x10c00, v143
	ds_read_b128 v[152:155], v0
	ds_read_b128 v[156:159], v156
	v_or_b32_e32 v0, 0x14000, v143
	v_add_u32_e32 v164, 0x14400, v143
	ds_read_b128 v[160:163], v0
	ds_read_b128 v[164:167], v164
	v_add_u32_e32 v0, 0x14800, v143
	v_add_u32_e32 v172, 0x14c00, v143
	ds_read_b128 v[168:171], v0
	ds_read_b128 v[172:175], v172
	s_add_u32 s41, s52, 0xfffc0080
	s_addc_u32 s43, s53, -1
	s_cmp_eq_u32 s39, 12
	s_cselect_b32 s57, s47, s43
	s_cselect_b32 s56, s46, s41
	s_cselect_b32 s55, s49, s29
	s_cselect_b32 s54, s48, s17
	s_add_i32 m0, s59, 0xc000
	ds_read_b128 v[176:179], v142
	ds_read_b128 v[180:183], v142 offset:1024
	ds_read_b128 v[184:187], v142 offset:2048
	ds_read_b128 v[188:191], v142 offset:3072
	ds_read_b128 v[192:195], v142 offset:4096
	ds_read_b128 v[200:203], v142 offset:5120
	ds_read_b128 v[204:207], v142 offset:6144
	ds_read_b128 v[208:211], v142 offset:7168
	global_load_lds_dwordx4 v138, s[52:53]
	s_add_i32 m0, s59, 0xe000
	s_nop 0
	global_load_lds_dwordx4 v140, s[52:53]
	s_waitcnt vmcnt(8)
	s_waitcnt lgkmcnt(0)
	s_barrier
	s_setprio 1
	s_waitcnt lgkmcnt(0)
	v_mfma_f32_16x16x32_bf16 v[126:129], v[144:147], v[176:179], v[126:129]
	v_mfma_f32_16x16x32_bf16 v[122:125], v[152:155], v[176:179], v[122:125]
	v_mfma_f32_16x16x32_bf16 v[118:121], v[144:147], v[184:187], v[118:121]
	v_mfma_f32_16x16x32_bf16 v[114:117], v[152:155], v[184:187], v[114:117]
	v_mfma_f32_16x16x32_bf16 v[102:105], v[144:147], v[192:195], v[102:105]
	v_mfma_f32_16x16x32_bf16 v[98:101], v[152:155], v[192:195], v[98:101]
	v_mfma_f32_16x16x32_bf16 v[86:89], v[144:147], v[204:207], v[86:89]
	v_mfma_f32_16x16x32_bf16 v[82:85], v[152:155], v[204:207], v[82:85]
	v_mfma_f32_16x16x32_bf16 v[126:129], v[148:151], v[180:183], v[126:129]
	v_mfma_f32_16x16x32_bf16 v[122:125], v[156:159], v[180:183], v[122:125]
	v_mfma_f32_16x16x32_bf16 v[118:121], v[148:151], v[188:191], v[118:121]
	v_mfma_f32_16x16x32_bf16 v[114:117], v[156:159], v[188:191], v[114:117]
	v_mfma_f32_16x16x32_bf16 v[102:105], v[148:151], v[200:203], v[102:105]
	v_mfma_f32_16x16x32_bf16 v[98:101], v[156:159], v[200:203], v[98:101]
	v_mfma_f32_16x16x32_bf16 v[86:89], v[148:151], v[208:211], v[86:89]
	v_mfma_f32_16x16x32_bf16 v[82:85], v[156:159], v[208:211], v[82:85]
	s_setprio 0
	s_setprio 1
	v_mfma_f32_16x16x32_bf16 v[110:113], v[160:163], v[176:179], v[110:113]
	v_mfma_f32_16x16x32_bf16 v[106:109], v[168:171], v[176:179], v[106:109]
	v_mfma_f32_16x16x32_bf16 v[94:97], v[160:163], v[184:187], v[94:97]
	v_mfma_f32_16x16x32_bf16 v[90:93], v[168:171], v[184:187], v[90:93]
	v_mfma_f32_16x16x32_bf16 v[78:81], v[160:163], v[192:195], v[78:81]
	v_mfma_f32_16x16x32_bf16 v[74:77], v[168:171], v[192:195], v[74:77]
	v_mfma_f32_16x16x32_bf16 v[70:73], v[160:163], v[204:207], v[70:73]
	v_mfma_f32_16x16x32_bf16 v[66:69], v[168:171], v[204:207], v[66:69]
	v_mfma_f32_16x16x32_bf16 v[110:113], v[164:167], v[180:183], v[110:113]
	v_mfma_f32_16x16x32_bf16 v[106:109], v[172:175], v[180:183], v[106:109]
	v_mfma_f32_16x16x32_bf16 v[94:97], v[164:167], v[188:191], v[94:97]
	v_mfma_f32_16x16x32_bf16 v[90:93], v[172:175], v[188:191], v[90:93]
	v_mfma_f32_16x16x32_bf16 v[78:81], v[164:167], v[200:203], v[78:81]
	v_mfma_f32_16x16x32_bf16 v[74:77], v[172:175], v[200:203], v[74:77]
	v_mfma_f32_16x16x32_bf16 v[70:73], v[164:167], v[208:211], v[70:73]
	v_mfma_f32_16x16x32_bf16 v[66:69], v[172:175], v[208:211], v[66:69]
	s_setprio 0
	s_barrier
	s_mov_b32 m0, s60
	v_lshl_add_u64 v[212:213], s[54:55], 0, v[132:133]
	s_add_u32 s94, s54, 0x40000
	ds_read_b128 v[176:179], v142 offset:16384
	ds_read_b128 v[180:183], v142 offset:17408
	ds_read_b128 v[184:187], v142 offset:18432
	ds_read_b128 v[188:191], v142 offset:19456
	ds_read_b128 v[192:195], v142 offset:20480
	ds_read_b128 v[200:203], v142 offset:21504
	ds_read_b128 v[204:207], v142 offset:22528
	ds_read_b128 v[208:211], v142 offset:23552
	global_load_lds_dwordx4 v132, s[54:55]
	v_lshl_add_u64 v[214:215], s[54:55], 0, v[136:137]
	s_mov_b32 m0, s61
	s_addc_u32 s95, s55, 0
	global_load_lds_dwordx4 v136, s[54:55]
	s_mov_b32 m0, s62
	v_lshl_add_u64 v[218:219], s[56:57], 0, v[134:135]
	global_load_lds_dwordx4 v132, s[94:95]
	s_mov_b32 m0, s63
	s_nop 0
	global_load_lds_dwordx4 v136, s[94:95]
	v_lshl_add_u64 v[216:217], s[56:57], 0, v[130:131]
	s_mov_b32 m0, s59
	s_nop 0
	global_load_lds_dwordx4 v130, s[56:57]
	s_mov_b32 m0, s64
	s_nop 0
	global_load_lds_dwordx4 v134, s[56:57]
	s_waitcnt vmcnt(8)
	s_waitcnt lgkmcnt(0)
	s_barrier
	s_setprio 1
	s_waitcnt lgkmcnt(0)
	v_mfma_f32_16x16x32_bf16 v[62:65], v[144:147], v[176:179], v[62:65]
	v_mfma_f32_16x16x32_bf16 v[58:61], v[152:155], v[176:179], v[58:61]
	v_mfma_f32_16x16x32_bf16 v[54:57], v[144:147], v[184:187], v[54:57]
	v_mfma_f32_16x16x32_bf16 v[50:53], v[152:155], v[184:187], v[50:53]
	v_mfma_f32_16x16x32_bf16 v[38:41], v[144:147], v[192:195], v[38:41]
	v_mfma_f32_16x16x32_bf16 v[34:37], v[152:155], v[192:195], v[34:37]
	v_mfma_f32_16x16x32_bf16 v[22:25], v[144:147], v[204:207], v[22:25]
	v_mfma_f32_16x16x32_bf16 v[18:21], v[152:155], v[204:207], v[18:21]
	v_mfma_f32_16x16x32_bf16 v[62:65], v[148:151], v[180:183], v[62:65]
	v_mfma_f32_16x16x32_bf16 v[58:61], v[156:159], v[180:183], v[58:61]
	v_mfma_f32_16x16x32_bf16 v[54:57], v[148:151], v[188:191], v[54:57]
	v_mfma_f32_16x16x32_bf16 v[50:53], v[156:159], v[188:191], v[50:53]
	v_mfma_f32_16x16x32_bf16 v[38:41], v[148:151], v[200:203], v[38:41]
	v_mfma_f32_16x16x32_bf16 v[34:37], v[156:159], v[200:203], v[34:37]
	v_mfma_f32_16x16x32_bf16 v[22:25], v[148:151], v[208:211], v[22:25]
	v_mfma_f32_16x16x32_bf16 v[18:21], v[156:159], v[208:211], v[18:21]
	s_setprio 0
	s_setprio 1
	v_mfma_f32_16x16x32_bf16 v[46:49], v[160:163], v[176:179], v[46:49]
	v_mfma_f32_16x16x32_bf16 v[42:45], v[168:171], v[176:179], v[42:45]
	v_mfma_f32_16x16x32_bf16 v[30:33], v[160:163], v[184:187], v[30:33]
	v_mfma_f32_16x16x32_bf16 v[26:29], v[168:171], v[184:187], v[26:29]
	v_mfma_f32_16x16x32_bf16 v[14:17], v[160:163], v[192:195], v[14:17]
	v_mfma_f32_16x16x32_bf16 v[10:13], v[168:171], v[192:195], v[10:13]
	v_mfma_f32_16x16x32_bf16 v[6:9], v[160:163], v[204:207], v[6:9]
	v_mfma_f32_16x16x32_bf16 v[2:5], v[168:171], v[204:207], v[2:5]
	v_mfma_f32_16x16x32_bf16 v[46:49], v[164:167], v[180:183], v[46:49]
	v_mfma_f32_16x16x32_bf16 v[42:45], v[172:175], v[180:183], v[42:45]
	v_mfma_f32_16x16x32_bf16 v[30:33], v[164:167], v[188:191], v[30:33]
	v_mfma_f32_16x16x32_bf16 v[26:29], v[172:175], v[188:191], v[26:29]
	v_mfma_f32_16x16x32_bf16 v[14:17], v[164:167], v[200:203], v[14:17]
	v_mfma_f32_16x16x32_bf16 v[10:13], v[172:175], v[200:203], v[10:13]
	v_mfma_f32_16x16x32_bf16 v[6:9], v[164:167], v[208:211], v[6:9]
	v_mfma_f32_16x16x32_bf16 v[2:5], v[172:175], v[208:211], v[2:5]
	s_setprio 0
	s_barrier
	v_or_b32_e32 v0, 0x18000, v143
	v_add_u32_e32 v148, 0x18400, v143
	ds_read_b128 v[144:147], v0
	ds_read_b128 v[148:151], v148
	v_add_u32_e32 v0, 0x18800, v143
	v_add_u32_e32 v156, 0x18c00, v143
	ds_read_b128 v[152:155], v0
	ds_read_b128 v[156:159], v156
	v_or_b32_e32 v0, 0x1c000, v143
	v_add_u32_e32 v164, 0x1c400, v143
	ds_read_b128 v[160:163], v0
	ds_read_b128 v[164:167], v164
	v_add_u32_e32 v0, 0x1c800, v143
	v_add_u32_e32 v172, 0x1cc00, v143
	ds_read_b128 v[168:171], v0
	ds_read_b128 v[172:175], v172
	s_add_u32 s56, s56, 0x40000
	s_addc_u32 s57, s57, 0
	s_mov_b32 m0, s65
	ds_read_b128 v[176:179], v142 offset:32768
	ds_read_b128 v[180:183], v142 offset:33792
	ds_read_b128 v[184:187], v142 offset:34816
	ds_read_b128 v[188:191], v142 offset:35840
	ds_read_b128 v[192:195], v142 offset:36864
	ds_read_b128 v[200:203], v142 offset:37888
	ds_read_b128 v[204:207], v142 offset:38912
	ds_read_b128 v[208:211], v142 offset:39936
	global_load_lds_dwordx4 v130, s[56:57]
	s_mov_b32 m0, s66
	s_nop 0
	global_load_lds_dwordx4 v134, s[56:57]
	s_waitcnt vmcnt(8)
	s_waitcnt lgkmcnt(0)
	s_barrier
	s_setprio 1
	s_waitcnt lgkmcnt(0)
	v_mfma_f32_16x16x32_bf16 v[126:129], v[144:147], v[176:179], v[126:129]
	v_mfma_f32_16x16x32_bf16 v[122:125], v[152:155], v[176:179], v[122:125]
	v_mfma_f32_16x16x32_bf16 v[118:121], v[144:147], v[184:187], v[118:121]
	v_mfma_f32_16x16x32_bf16 v[114:117], v[152:155], v[184:187], v[114:117]
	v_mfma_f32_16x16x32_bf16 v[102:105], v[144:147], v[192:195], v[102:105]
	v_mfma_f32_16x16x32_bf16 v[98:101], v[152:155], v[192:195], v[98:101]
	v_mfma_f32_16x16x32_bf16 v[86:89], v[144:147], v[204:207], v[86:89]
	v_mfma_f32_16x16x32_bf16 v[82:85], v[152:155], v[204:207], v[82:85]
	v_mfma_f32_16x16x32_bf16 v[126:129], v[148:151], v[180:183], v[126:129]
	v_mfma_f32_16x16x32_bf16 v[122:125], v[156:159], v[180:183], v[122:125]
	v_mfma_f32_16x16x32_bf16 v[118:121], v[148:151], v[188:191], v[118:121]
	v_mfma_f32_16x16x32_bf16 v[114:117], v[156:159], v[188:191], v[114:117]
	v_mfma_f32_16x16x32_bf16 v[102:105], v[148:151], v[200:203], v[102:105]
	v_mfma_f32_16x16x32_bf16 v[98:101], v[156:159], v[200:203], v[98:101]
	v_mfma_f32_16x16x32_bf16 v[86:89], v[148:151], v[208:211], v[86:89]
	v_mfma_f32_16x16x32_bf16 v[82:85], v[156:159], v[208:211], v[82:85]
	s_setprio 0
	s_setprio 1
	v_mfma_f32_16x16x32_bf16 v[110:113], v[160:163], v[176:179], v[110:113]
	v_mfma_f32_16x16x32_bf16 v[106:109], v[168:171], v[176:179], v[106:109]
	v_mfma_f32_16x16x32_bf16 v[94:97], v[160:163], v[184:187], v[94:97]
	v_mfma_f32_16x16x32_bf16 v[90:93], v[168:171], v[184:187], v[90:93]
	v_mfma_f32_16x16x32_bf16 v[78:81], v[160:163], v[192:195], v[78:81]
	v_mfma_f32_16x16x32_bf16 v[74:77], v[168:171], v[192:195], v[74:77]
	v_mfma_f32_16x16x32_bf16 v[70:73], v[160:163], v[204:207], v[70:73]
	v_mfma_f32_16x16x32_bf16 v[66:69], v[168:171], v[204:207], v[66:69]
	v_mfma_f32_16x16x32_bf16 v[110:113], v[164:167], v[180:183], v[110:113]
	v_mfma_f32_16x16x32_bf16 v[106:109], v[172:175], v[180:183], v[106:109]
	v_mfma_f32_16x16x32_bf16 v[94:97], v[164:167], v[188:191], v[94:97]
	v_mfma_f32_16x16x32_bf16 v[90:93], v[172:175], v[188:191], v[90:93]
	v_mfma_f32_16x16x32_bf16 v[78:81], v[164:167], v[200:203], v[78:81]
	v_mfma_f32_16x16x32_bf16 v[74:77], v[172:175], v[200:203], v[74:77]
	v_mfma_f32_16x16x32_bf16 v[70:73], v[164:167], v[208:211], v[70:73]
	v_mfma_f32_16x16x32_bf16 v[66:69], v[172:175], v[208:211], v[66:69]
	s_setprio 0
	s_barrier
	s_mov_b32 m0, s80
	v_lshl_add_u64 v[212:213], v[212:213], 0, s[18:19]
	s_add_u32 s54, s54, 0x40080
	ds_read_b128 v[176:179], v142 offset:49152
	ds_read_b128 v[180:183], v142 offset:50176
	ds_read_b128 v[184:187], v142 offset:51200
	ds_read_b128 v[188:191], v142 offset:52224
	ds_read_b128 v[192:195], v142 offset:53248
	ds_read_b128 v[200:203], v142 offset:54272
	ds_read_b128 v[204:207], v142 offset:55296
	ds_read_b128 v[208:211], v142 offset:56320
	global_load_lds_dwordx4 v[212:213], off
	v_lshl_add_u64 v[212:213], v[214:215], 0, s[18:19]
	s_mov_b32 m0, s82
	s_addc_u32 s55, s55, 0
	global_load_lds_dwordx4 v[212:213], off
	s_mov_b32 m0, s85
	s_nop 0
	global_load_lds_dwordx4 v132, s[54:55]
	s_mov_b32 m0, s88
	s_nop 0
	global_load_lds_dwordx4 v136, s[54:55]
	v_lshl_add_u64 v[212:213], v[216:217], 0, s[18:19]
	s_mov_b32 m0, s83
	s_nop 0
	global_load_lds_dwordx4 v[212:213], off
	v_lshl_add_u64 v[212:213], v[218:219], 0, s[18:19]
	s_mov_b32 m0, s84
	s_nop 0
	global_load_lds_dwordx4 v[212:213], off
	s_waitcnt vmcnt(8)
	s_waitcnt lgkmcnt(0)
	s_barrier
	s_setprio 1
	s_waitcnt lgkmcnt(0)
	v_mfma_f32_16x16x32_bf16 v[62:65], v[144:147], v[176:179], v[62:65]
	v_mfma_f32_16x16x32_bf16 v[58:61], v[152:155], v[176:179], v[58:61]
	v_mfma_f32_16x16x32_bf16 v[54:57], v[144:147], v[184:187], v[54:57]
	v_mfma_f32_16x16x32_bf16 v[50:53], v[152:155], v[184:187], v[50:53]
	v_mfma_f32_16x16x32_bf16 v[38:41], v[144:147], v[192:195], v[38:41]
	v_mfma_f32_16x16x32_bf16 v[34:37], v[152:155], v[192:195], v[34:37]
	v_mfma_f32_16x16x32_bf16 v[22:25], v[144:147], v[204:207], v[22:25]
	v_mfma_f32_16x16x32_bf16 v[18:21], v[152:155], v[204:207], v[18:21]
	v_mfma_f32_16x16x32_bf16 v[62:65], v[148:151], v[180:183], v[62:65]
	v_mfma_f32_16x16x32_bf16 v[58:61], v[156:159], v[180:183], v[58:61]
	v_mfma_f32_16x16x32_bf16 v[54:57], v[148:151], v[188:191], v[54:57]
	v_mfma_f32_16x16x32_bf16 v[50:53], v[156:159], v[188:191], v[50:53]
	v_mfma_f32_16x16x32_bf16 v[38:41], v[148:151], v[200:203], v[38:41]
	v_mfma_f32_16x16x32_bf16 v[34:37], v[156:159], v[200:203], v[34:37]
	v_mfma_f32_16x16x32_bf16 v[22:25], v[148:151], v[208:211], v[22:25]
	v_mfma_f32_16x16x32_bf16 v[18:21], v[156:159], v[208:211], v[18:21]
	s_setprio 0
	s_setprio 1
	v_mfma_f32_16x16x32_bf16 v[46:49], v[160:163], v[176:179], v[46:49]
	v_mfma_f32_16x16x32_bf16 v[42:45], v[168:171], v[176:179], v[42:45]
	v_mfma_f32_16x16x32_bf16 v[30:33], v[160:163], v[184:187], v[30:33]
	v_mfma_f32_16x16x32_bf16 v[26:29], v[168:171], v[184:187], v[26:29]
	v_mfma_f32_16x16x32_bf16 v[14:17], v[160:163], v[192:195], v[14:17]
	v_mfma_f32_16x16x32_bf16 v[10:13], v[168:171], v[192:195], v[10:13]
	v_mfma_f32_16x16x32_bf16 v[6:9], v[160:163], v[204:207], v[6:9]
	v_mfma_f32_16x16x32_bf16 v[2:5], v[168:171], v[204:207], v[2:5]
	v_mfma_f32_16x16x32_bf16 v[46:49], v[164:167], v[180:183], v[46:49]
	v_mfma_f32_16x16x32_bf16 v[42:45], v[172:175], v[180:183], v[42:45]
	v_mfma_f32_16x16x32_bf16 v[30:33], v[164:167], v[188:191], v[30:33]
	v_mfma_f32_16x16x32_bf16 v[26:29], v[172:175], v[188:191], v[26:29]
	v_mfma_f32_16x16x32_bf16 v[14:17], v[164:167], v[200:203], v[14:17]
	v_mfma_f32_16x16x32_bf16 v[10:13], v[172:175], v[200:203], v[10:13]
	v_mfma_f32_16x16x32_bf16 v[6:9], v[164:167], v[208:211], v[6:9]
	v_mfma_f32_16x16x32_bf16 v[2:5], v[172:175], v[208:211], v[2:5]
	s_setprio 0
	s_barrier
	s_add_i32 s39, s39, 2
	s_add_u32 s52, s52, 0x100
	s_addc_u32 s53, s53, 0
	s_add_u32 s17, s17, 0x100
	s_addc_u32 s29, s29, 0
	s_cmp_gt_u32 s39, 13
	s_cbranch_scc0 .LBB0_2067
	s_and_b64 vcc, exec, s[14:15]
	s_cbranch_vccz .LBB0_2070
	s_barrier
